# GEMM K-loops (17 of 25): LDS-DMA via scalar-base addressing, 64-bit VALU address adds removed
# speedup vs baseline: 1.0031x; 1.0031x over previous
; #define PG8_STAGE(bufoff, gbase, voff) do { _Pragma("unroll") for (int _i = 0; _i < 2; ++_i) \
;         __builtin_amdgcn_global_load_lds((const unsigned*)((const char*)(gbase) + (voff)[_i]), (PG8_LAS unsigned*)(lds + (bufoff) + ldsw + _i * 8192), 16, 0, 0); } while (0)
; #define PG8_LDA(dst, b, h) do { if constexpr (DT != 1) { _Pragma("unroll") for (int m = 0; m < 4; ++m) _Pragma("unroll") for (int k = 0; k < 2; ++k) dst[m][k] = *(const PG8_LAS bf16x8*)(lds + PG8_SA(b, h) + aoff + m * 2048 + k * 1024); } \
;         else { _Pragma("unroll") for (int m = 0; m < 4; ++m) dst##8[m] = ld32(lds + PG8_SA(b, h) + aoff + m * 2048); } } while (0)
; #define PG8_LDB(dst, b, h) do { if constexpr (DT != 1) { _Pragma("unroll") for (int n = 0; n < 2; ++n) _Pragma("unroll") for (int k = 0; k < 2; ++k) dst[n][k] = *(const PG8_LAS bf16x8*)(lds + PG8_SB(b, h) + boff + n * 2048 + k * 1024); } \
;         else { _Pragma("unroll") for (int n = 0; n < 2; ++n) dst##8[n] = ld32(lds + PG8_SB(b, h) + boff + n * 2048); } } while (0)
; #define PG8_WAIT_V(n) asm volatile("s_waitcnt vmcnt(" #n ")" ::: "memory")
; #define PG8_WAIT_L(n) asm volatile("s_waitcnt lgkmcnt(" #n ")" ::: "memory")
; #define PG8_BAR __builtin_amdgcn_s_barrier()
; #define PG8_SCHED __builtin_amdgcn_sched_barrier(0)
;     ...
;             PG8_LDB(B0, 0, 0); PG8_LDB(B1, 0, 1); PG8_SCHED; PG8_LDA(At, 0, 0); PG8_STAGE(PG8_SA(1, 1), a1 + hstepA, voffA);
;             PG8_WAIT_V(8); PG8_WAIT_L(0); PG8_BAR; PG8_MMA(0, 0, At, B0); PG8_MMA(0, 1, At, B1); PG8_BAR; PG8_SCHED;
;             PG8_LDA(At, 0, 1); PG8_STAGE(PG8_SB(0, 0), b2, voffB); PG8_STAGE(PG8_SB(0, 1), b2 + hstepB, voffB); PG8_STAGE(PG8_SA(0, 0), a2, voffA);
;             PG8_WAIT_V(8); PG8_WAIT_L(0); PG8_BAR; PG8_MMA(1, 0, At, B0); PG8_MMA(1, 1, At, B1); PG8_BAR; PG8_SCHED;
.LBB0_227:
	v_add_u32_e32 v142, s35, v164
	v_add_u32_e32 v180, s36, v164
	ds_read_b128 v[130:133], v142
	ds_read_b128 v[134:137], v142 offset:1024
	ds_read_b128 v[138:141], v142 offset:2048
	ds_read_b128 v[142:145], v142 offset:3072
	ds_read_b128 v[168:171], v180
	ds_read_b128 v[172:175], v180 offset:1024
	ds_read_b128 v[176:179], v180 offset:2048
	ds_read_b128 v[180:183], v180 offset:3072
	s_add_i32 s68, s26, 2
	s_add_u32 s27, s24, 0xfffc0080
	s_addc_u32 s28, s25, -1
	s_cmp_eq_u32 s61, s26
	s_cselect_b32 s26, s65, s66
	s_cselect_b32 s29, s15, s28
	s_cselect_b32 s28, s17, s27
	s_cselect_b32 s27, s64, s67
	s_add_i32 m0, s46, 0xc000
	ds_read_b128 v[184:187], v167
	ds_read_b128 v[188:191], v167 offset:1024
	ds_read_b128 v[192:195], v167 offset:2048
	ds_read_b128 v[196:199], v167 offset:3072
	ds_read_b128 v[200:203], v167 offset:4096
	ds_read_b128 v[204:207], v167 offset:5120
	ds_read_b128 v[208:211], v167 offset:6144
	ds_read_b128 v[212:215], v167 offset:7168
	global_load_lds_dwordx4 v158, s[24:25]
	s_add_i32 m0, s46, 0xe000
	s_nop 0
	global_load_lds_dwordx4 v156, s[24:25]
	s_waitcnt vmcnt(8)
	s_waitcnt lgkmcnt(0)
	s_barrier
	s_setprio 1
	s_waitcnt lgkmcnt(0)
	v_mfma_i32_16x16x64_i8 v[126:129], v[130:133], v[184:187], v[126:129]
	v_mfma_i32_16x16x64_i8 v[118:121], v[138:141], v[184:187], v[118:121]
	v_mfma_i32_16x16x64_i8 v[110:113], v[130:133], v[192:195], v[110:113]
	v_mfma_i32_16x16x64_i8 v[102:105], v[138:141], v[192:195], v[102:105]
	v_mfma_i32_16x16x64_i8 v[94:97], v[130:133], v[200:203], v[94:97]
	v_mfma_i32_16x16x64_i8 v[86:89], v[138:141], v[200:203], v[86:89]
	v_mfma_i32_16x16x64_i8 v[78:81], v[130:133], v[208:211], v[78:81]
	v_mfma_i32_16x16x64_i8 v[70:73], v[138:141], v[208:211], v[70:73]
	v_mfma_i32_16x16x64_i8 v[126:129], v[134:137], v[188:191], v[126:129]
	v_mfma_i32_16x16x64_i8 v[118:121], v[142:145], v[188:191], v[118:121]
	v_mfma_i32_16x16x64_i8 v[110:113], v[134:137], v[196:199], v[110:113]
	v_mfma_i32_16x16x64_i8 v[102:105], v[142:145], v[196:199], v[102:105]
	v_mfma_i32_16x16x64_i8 v[94:97], v[134:137], v[204:207], v[94:97]
	v_mfma_i32_16x16x64_i8 v[86:89], v[142:145], v[204:207], v[86:89]
	v_mfma_i32_16x16x64_i8 v[78:81], v[134:137], v[212:215], v[78:81]
	v_mfma_i32_16x16x64_i8 v[70:73], v[142:145], v[212:215], v[70:73]
	s_setprio 0
	s_setprio 1
	v_mfma_i32_16x16x64_i8 v[122:125], v[168:171], v[184:187], v[122:125]
	v_mfma_i32_16x16x64_i8 v[114:117], v[176:179], v[184:187], v[114:117]
	v_mfma_i32_16x16x64_i8 v[106:109], v[168:171], v[192:195], v[106:109]
	v_mfma_i32_16x16x64_i8 v[98:101], v[176:179], v[192:195], v[98:101]
	v_mfma_i32_16x16x64_i8 v[90:93], v[168:171], v[200:203], v[90:93]
	v_mfma_i32_16x16x64_i8 v[82:85], v[176:179], v[200:203], v[82:85]
	v_mfma_i32_16x16x64_i8 v[74:77], v[168:171], v[208:211], v[74:77]
	v_mfma_i32_16x16x64_i8 v[66:69], v[176:179], v[208:211], v[66:69]
	v_mfma_i32_16x16x64_i8 v[122:125], v[172:175], v[188:191], v[122:125]
	v_mfma_i32_16x16x64_i8 v[114:117], v[180:183], v[188:191], v[114:117]
	v_mfma_i32_16x16x64_i8 v[106:109], v[172:175], v[196:199], v[106:109]
	v_mfma_i32_16x16x64_i8 v[98:101], v[180:183], v[196:199], v[98:101]
	v_mfma_i32_16x16x64_i8 v[90:93], v[172:175], v[204:207], v[90:93]
	v_mfma_i32_16x16x64_i8 v[82:85], v[180:183], v[204:207], v[82:85]
	v_mfma_i32_16x16x64_i8 v[74:77], v[172:175], v[212:215], v[74:77]
	v_mfma_i32_16x16x64_i8 v[66:69], v[180:183], v[212:215], v[66:69]
	s_setprio 0
	s_barrier
	s_mov_b32 m0, s23
	s_add_u32 s98, s26, 0x80
	s_addc_u32 s99, s27, 0
	s_add_u32 s70, s26, 0x40000
	ds_read_b128 v[184:187], v167 offset:16384
	ds_read_b128 v[188:191], v167 offset:17408
	ds_read_b128 v[192:195], v167 offset:18432
	ds_read_b128 v[196:199], v167 offset:19456
	ds_read_b128 v[200:203], v167 offset:20480
	ds_read_b128 v[204:207], v167 offset:21504
	ds_read_b128 v[208:211], v167 offset:22528
	ds_read_b128 v[212:215], v167 offset:23552
	global_load_lds_dwordx4 v148, s[26:27]
	s_mov_b32 m0, s43
	s_addc_u32 s71, s27, 0
	global_load_lds_dwordx4 v152, s[26:27]
	s_mov_b32 m0, s44
	s_nop 0
	global_load_lds_dwordx4 v148, s[70:71]
	s_mov_b32 m0, s45
	s_nop 0
	global_load_lds_dwordx4 v152, s[70:71]
	s_add_u32 s100, s28, 0x80
	s_addc_u32 s101, s29, 0
	s_mov_b32 m0, s46
	s_nop 0
	global_load_lds_dwordx4 v146, s[28:29]
	s_mov_b32 m0, s47
	s_nop 0
	global_load_lds_dwordx4 v150, s[28:29]
	s_waitcnt vmcnt(8)
	s_waitcnt lgkmcnt(0)
	s_barrier
	s_setprio 1
	s_waitcnt lgkmcnt(0)
	v_mfma_i32_16x16x64_i8 v[62:65], v[130:133], v[184:187], v[62:65]
	v_mfma_i32_16x16x64_i8 v[54:57], v[138:141], v[184:187], v[54:57]
	v_mfma_i32_16x16x64_i8 v[46:49], v[130:133], v[192:195], v[46:49]
	v_mfma_i32_16x16x64_i8 v[38:41], v[138:141], v[192:195], v[38:41]
	v_mfma_i32_16x16x64_i8 v[30:33], v[130:133], v[200:203], v[30:33]
	v_mfma_i32_16x16x64_i8 v[22:25], v[138:141], v[200:203], v[22:25]
	v_mfma_i32_16x16x64_i8 v[14:17], v[130:133], v[208:211], v[14:17]
	v_mfma_i32_16x16x64_i8 v[6:9], v[138:141], v[208:211], v[6:9]
	v_mfma_i32_16x16x64_i8 v[62:65], v[134:137], v[188:191], v[62:65]
	v_mfma_i32_16x16x64_i8 v[54:57], v[142:145], v[188:191], v[54:57]
	v_mfma_i32_16x16x64_i8 v[46:49], v[134:137], v[196:199], v[46:49]
	v_mfma_i32_16x16x64_i8 v[38:41], v[142:145], v[196:199], v[38:41]
	v_mfma_i32_16x16x64_i8 v[30:33], v[134:137], v[204:207], v[30:33]
	v_mfma_i32_16x16x64_i8 v[22:25], v[142:145], v[204:207], v[22:25]
	v_mfma_i32_16x16x64_i8 v[14:17], v[134:137], v[212:215], v[14:17]
	v_mfma_i32_16x16x64_i8 v[6:9], v[142:145], v[212:215], v[6:9]
	s_setprio 0
	s_setprio 1
	v_mfma_i32_16x16x64_i8 v[58:61], v[168:171], v[184:187], v[58:61]
	v_mfma_i32_16x16x64_i8 v[50:53], v[176:179], v[184:187], v[50:53]
	v_mfma_i32_16x16x64_i8 v[42:45], v[168:171], v[192:195], v[42:45]
	v_mfma_i32_16x16x64_i8 v[34:37], v[176:179], v[192:195], v[34:37]
	v_mfma_i32_16x16x64_i8 v[26:29], v[168:171], v[200:203], v[26:29]
	v_mfma_i32_16x16x64_i8 v[18:21], v[176:179], v[200:203], v[18:21]
	v_mfma_i32_16x16x64_i8 v[10:13], v[168:171], v[208:211], v[10:13]
	v_mfma_i32_16x16x64_i8 v[2:5], v[176:179], v[208:211], v[2:5]
	v_mfma_i32_16x16x64_i8 v[58:61], v[172:175], v[188:191], v[58:61]
	v_mfma_i32_16x16x64_i8 v[50:53], v[180:183], v[188:191], v[50:53]
	v_mfma_i32_16x16x64_i8 v[42:45], v[172:175], v[196:199], v[42:45]
	v_mfma_i32_16x16x64_i8 v[34:37], v[180:183], v[196:199], v[34:37]
	v_mfma_i32_16x16x64_i8 v[26:29], v[172:175], v[204:207], v[26:29]
	v_mfma_i32_16x16x64_i8 v[18:21], v[180:183], v[204:207], v[18:21]
	v_mfma_i32_16x16x64_i8 v[10:13], v[172:175], v[212:215], v[10:13]
	v_mfma_i32_16x16x64_i8 v[2:5], v[180:183], v[212:215], v[2:5]
	s_setprio 0
	s_barrier
; #define PG8_STAGE(bufoff, gbase, voff) do { _Pragma("unroll") for (int _i = 0; _i < 2; ++_i) \
;         __builtin_amdgcn_global_load_lds((const unsigned*)((const char*)(gbase) + (voff)[_i]), (PG8_LAS unsigned*)(lds + (bufoff) + ldsw + _i * 8192), 16, 0, 0); } while (0)
; #define PG8_LDA(dst, b, h) do { if constexpr (DT != 1) { _Pragma("unroll") for (int m = 0; m < 4; ++m) _Pragma("unroll") for (int k = 0; k < 2; ++k) dst[m][k] = *(const PG8_LAS bf16x8*)(lds + PG8_SA(b, h) + aoff + m * 2048 + k * 1024); } \
;         else { _Pragma("unroll") for (int m = 0; m < 4; ++m) dst##8[m] = ld32(lds + PG8_SA(b, h) + aoff + m * 2048); } } while (0)
; #define PG8_LDB(dst, b, h) do { if constexpr (DT != 1) { _Pragma("unroll") for (int n = 0; n < 2; ++n) _Pragma("unroll") for (int k = 0; k < 2; ++k) dst[n][k] = *(const PG8_LAS bf16x8*)(lds + PG8_SB(b, h) + boff + n * 2048 + k * 1024); } \
;         else { _Pragma("unroll") for (int n = 0; n < 2; ++n) dst##8[n] = ld32(lds + PG8_SB(b, h) + boff + n * 2048); } } while (0)
; #define PG8_WAIT_V(n) asm volatile("s_waitcnt vmcnt(" #n ")" ::: "memory")
; #define PG8_WAIT_L(n) asm volatile("s_waitcnt lgkmcnt(" #n ")" ::: "memory")
; #define PG8_BAR __builtin_amdgcn_s_barrier()
; #define PG8_SCHED __builtin_amdgcn_sched_barrier(0)
;     ...
;             PG8_LDB(B0, 1, 0); PG8_LDB(B1, 1, 1); PG8_SCHED; PG8_LDA(At, 1, 0); PG8_STAGE(PG8_SA(0, 1), a2 + hstepA, voffA);
;             PG8_WAIT_V(8); PG8_WAIT_L(0); PG8_BAR; PG8_MMA(0, 0, At, B0); PG8_MMA(0, 1, At, B1); PG8_BAR; PG8_SCHED;
;             PG8_LDA(At, 1, 1); PG8_STAGE(PG8_SB(1, 0), b3, voffB); PG8_STAGE(PG8_SB(1, 1), b3 + hstepB, voffB); PG8_STAGE(PG8_SA(1, 0), a3, voffA);
;             PG8_WAIT_V(8); PG8_WAIT_L(0); PG8_BAR; PG8_MMA(1, 0, At, B0); PG8_MMA(1, 1, At, B1); PG8_BAR; PG8_SCHED;
	v_add_u32_e32 v142, s51, v164
	v_add_u32_e32 v180, s52, v164
	ds_read_b128 v[130:133], v142
	ds_read_b128 v[134:137], v142 offset:1024
	ds_read_b128 v[138:141], v142 offset:2048
	ds_read_b128 v[142:145], v142 offset:3072
	ds_read_b128 v[168:171], v180
	ds_read_b128 v[172:175], v180 offset:1024
	ds_read_b128 v[176:179], v180 offset:2048
	ds_read_b128 v[180:183], v180 offset:3072
	s_add_u32 s28, s28, 0x40000
	s_addc_u32 s29, s29, 0
	s_mov_b32 m0, s48
	ds_read_b128 v[184:187], v167 offset:32768
	ds_read_b128 v[188:191], v167 offset:33792
	ds_read_b128 v[192:195], v167 offset:34816
	ds_read_b128 v[196:199], v167 offset:35840
	ds_read_b128 v[200:203], v167 offset:36864
	ds_read_b128 v[204:207], v167 offset:37888
	ds_read_b128 v[208:211], v167 offset:38912
	ds_read_b128 v[212:215], v167 offset:39936
	global_load_lds_dwordx4 v146, s[28:29]
	s_mov_b32 m0, s49
	s_nop 0
	global_load_lds_dwordx4 v150, s[28:29]
	s_waitcnt vmcnt(8)
	s_waitcnt lgkmcnt(0)
	s_barrier
	s_setprio 1
	s_waitcnt lgkmcnt(0)
	v_mfma_i32_16x16x64_i8 v[126:129], v[130:133], v[184:187], v[126:129]
	v_mfma_i32_16x16x64_i8 v[118:121], v[138:141], v[184:187], v[118:121]
	v_mfma_i32_16x16x64_i8 v[110:113], v[130:133], v[192:195], v[110:113]
	v_mfma_i32_16x16x64_i8 v[102:105], v[138:141], v[192:195], v[102:105]
	v_mfma_i32_16x16x64_i8 v[94:97], v[130:133], v[200:203], v[94:97]
	v_mfma_i32_16x16x64_i8 v[86:89], v[138:141], v[200:203], v[86:89]
	v_mfma_i32_16x16x64_i8 v[78:81], v[130:133], v[208:211], v[78:81]
	v_mfma_i32_16x16x64_i8 v[70:73], v[138:141], v[208:211], v[70:73]
	v_mfma_i32_16x16x64_i8 v[126:129], v[134:137], v[188:191], v[126:129]
	v_mfma_i32_16x16x64_i8 v[118:121], v[142:145], v[188:191], v[118:121]
	v_mfma_i32_16x16x64_i8 v[110:113], v[134:137], v[196:199], v[110:113]
	v_mfma_i32_16x16x64_i8 v[102:105], v[142:145], v[196:199], v[102:105]
	v_mfma_i32_16x16x64_i8 v[94:97], v[134:137], v[204:207], v[94:97]
	v_mfma_i32_16x16x64_i8 v[86:89], v[142:145], v[204:207], v[86:89]
	v_mfma_i32_16x16x64_i8 v[78:81], v[134:137], v[212:215], v[78:81]
	v_mfma_i32_16x16x64_i8 v[70:73], v[142:145], v[212:215], v[70:73]
	s_setprio 0
	s_setprio 1
	v_mfma_i32_16x16x64_i8 v[122:125], v[168:171], v[184:187], v[122:125]
	v_mfma_i32_16x16x64_i8 v[114:117], v[176:179], v[184:187], v[114:117]
	v_mfma_i32_16x16x64_i8 v[106:109], v[168:171], v[192:195], v[106:109]
	v_mfma_i32_16x16x64_i8 v[98:101], v[176:179], v[192:195], v[98:101]
	v_mfma_i32_16x16x64_i8 v[90:93], v[168:171], v[200:203], v[90:93]
	v_mfma_i32_16x16x64_i8 v[82:85], v[176:179], v[200:203], v[82:85]
	v_mfma_i32_16x16x64_i8 v[74:77], v[168:171], v[208:211], v[74:77]
	v_mfma_i32_16x16x64_i8 v[66:69], v[176:179], v[208:211], v[66:69]
	v_mfma_i32_16x16x64_i8 v[122:125], v[172:175], v[188:191], v[122:125]
	v_mfma_i32_16x16x64_i8 v[114:117], v[180:183], v[188:191], v[114:117]
	v_mfma_i32_16x16x64_i8 v[106:109], v[172:175], v[196:199], v[106:109]
	v_mfma_i32_16x16x64_i8 v[98:101], v[180:183], v[196:199], v[98:101]
	v_mfma_i32_16x16x64_i8 v[90:93], v[172:175], v[204:207], v[90:93]
	v_mfma_i32_16x16x64_i8 v[82:85], v[180:183], v[204:207], v[82:85]
	v_mfma_i32_16x16x64_i8 v[74:77], v[172:175], v[212:215], v[74:77]
	v_mfma_i32_16x16x64_i8 v[66:69], v[180:183], v[212:215], v[66:69]
	s_setprio 0
	s_barrier
	s_mov_b32 m0, s55
	s_add_u32 s26, s26, 0x40080
	ds_read_b128 v[184:187], v167 offset:49152
	ds_read_b128 v[188:191], v167 offset:50176
	ds_read_b128 v[192:195], v167 offset:51200
	ds_read_b128 v[196:199], v167 offset:52224
	ds_read_b128 v[200:203], v167 offset:53248
	ds_read_b128 v[204:207], v167 offset:54272
	ds_read_b128 v[208:211], v167 offset:55296
	ds_read_b128 v[212:215], v167 offset:56320
	global_load_lds_dwordx4 v148, s[98:99]
	s_mov_b32 m0, s56
	s_addc_u32 s27, s27, 0
	global_load_lds_dwordx4 v152, s[98:99]
	s_mov_b32 m0, s59
	s_nop 0
	global_load_lds_dwordx4 v148, s[26:27]
	s_mov_b32 m0, s60
	s_nop 0
	global_load_lds_dwordx4 v152, s[26:27]
	s_mov_b32 m0, s57
	s_nop 0
	global_load_lds_dwordx4 v146, s[100:101]
	s_mov_b32 m0, s58
	s_nop 0
	global_load_lds_dwordx4 v150, s[100:101]
	s_waitcnt vmcnt(8)
	s_waitcnt lgkmcnt(0)
	s_barrier
	s_setprio 1
	s_waitcnt lgkmcnt(0)
	v_mfma_i32_16x16x64_i8 v[62:65], v[130:133], v[184:187], v[62:65]
	v_mfma_i32_16x16x64_i8 v[54:57], v[138:141], v[184:187], v[54:57]
	v_mfma_i32_16x16x64_i8 v[46:49], v[130:133], v[192:195], v[46:49]
	v_mfma_i32_16x16x64_i8 v[38:41], v[138:141], v[192:195], v[38:41]
	v_mfma_i32_16x16x64_i8 v[30:33], v[130:133], v[200:203], v[30:33]
	v_mfma_i32_16x16x64_i8 v[22:25], v[138:141], v[200:203], v[22:25]
	v_mfma_i32_16x16x64_i8 v[14:17], v[130:133], v[208:211], v[14:17]
	v_mfma_i32_16x16x64_i8 v[6:9], v[138:141], v[208:211], v[6:9]
	v_mfma_i32_16x16x64_i8 v[62:65], v[134:137], v[188:191], v[62:65]
	v_mfma_i32_16x16x64_i8 v[54:57], v[142:145], v[188:191], v[54:57]
	v_mfma_i32_16x16x64_i8 v[46:49], v[134:137], v[196:199], v[46:49]
	v_mfma_i32_16x16x64_i8 v[38:41], v[142:145], v[196:199], v[38:41]
	v_mfma_i32_16x16x64_i8 v[30:33], v[134:137], v[204:207], v[30:33]
	v_mfma_i32_16x16x64_i8 v[22:25], v[142:145], v[204:207], v[22:25]
	v_mfma_i32_16x16x64_i8 v[14:17], v[134:137], v[212:215], v[14:17]
	v_mfma_i32_16x16x64_i8 v[6:9], v[142:145], v[212:215], v[6:9]
	s_setprio 0
	s_setprio 1
	v_mfma_i32_16x16x64_i8 v[58:61], v[168:171], v[184:187], v[58:61]
	v_mfma_i32_16x16x64_i8 v[50:53], v[176:179], v[184:187], v[50:53]
	v_mfma_i32_16x16x64_i8 v[42:45], v[168:171], v[192:195], v[42:45]
	v_mfma_i32_16x16x64_i8 v[34:37], v[176:179], v[192:195], v[34:37]
	v_mfma_i32_16x16x64_i8 v[26:29], v[168:171], v[200:203], v[26:29]
	v_mfma_i32_16x16x64_i8 v[18:21], v[176:179], v[200:203], v[18:21]
	v_mfma_i32_16x16x64_i8 v[10:13], v[168:171], v[208:211], v[10:13]
	v_mfma_i32_16x16x64_i8 v[2:5], v[176:179], v[208:211], v[2:5]
	v_mfma_i32_16x16x64_i8 v[58:61], v[172:175], v[188:191], v[58:61]
	v_mfma_i32_16x16x64_i8 v[50:53], v[180:183], v[188:191], v[50:53]
	v_mfma_i32_16x16x64_i8 v[42:45], v[172:175], v[196:199], v[42:45]
	v_mfma_i32_16x16x64_i8 v[34:37], v[180:183], v[196:199], v[34:37]
	v_mfma_i32_16x16x64_i8 v[26:29], v[172:175], v[204:207], v[26:29]
	v_mfma_i32_16x16x64_i8 v[18:21], v[180:183], v[204:207], v[18:21]
	v_mfma_i32_16x16x64_i8 v[10:13], v[172:175], v[212:215], v[10:13]
	v_mfma_i32_16x16x64_i8 v[2:5], v[180:183], v[212:215], v[2:5]
	s_setprio 0
	s_barrier
	s_add_u32 s66, s66, 0x100
	s_addc_u32 s67, s67, 0
	s_add_u32 s24, s24, 0x100
	s_addc_u32 s25, s25, 0
	s_cmp_ge_i32 s68, s54
	s_mov_b32 s26, s68
	s_cbranch_scc0 .LBB0_227

; #define PG8_STAGE(bufoff, gbase, voff) do { _Pragma("unroll") for (int _i = 0; _i < 2; ++_i) \
;         __builtin_amdgcn_global_load_lds((const unsigned*)((const char*)(gbase) + (voff)[_i]), (PG8_LAS unsigned*)(lds + (bufoff) + ldsw + _i * 8192), 16, 0, 0); } while (0)
; #define PG8_LDA(dst, b, h) do { if constexpr (DT != 1) { _Pragma("unroll") for (int m = 0; m < 4; ++m) _Pragma("unroll") for (int k = 0; k < 2; ++k) dst[m][k] = *(const PG8_LAS bf16x8*)(lds + PG8_SA(b, h) + aoff + m * 2048 + k * 1024); } \
;         else { _Pragma("unroll") for (int m = 0; m < 4; ++m) dst##8[m] = ld32(lds + PG8_SA(b, h) + aoff + m * 2048); } } while (0)
; #define PG8_LDB(dst, b, h) do { if constexpr (DT != 1) { _Pragma("unroll") for (int n = 0; n < 2; ++n) _Pragma("unroll") for (int k = 0; k < 2; ++k) dst[n][k] = *(const PG8_LAS bf16x8*)(lds + PG8_SB(b, h) + boff + n * 2048 + k * 1024); } \
;         else { _Pragma("unroll") for (int n = 0; n < 2; ++n) dst##8[n] = ld32(lds + PG8_SB(b, h) + boff + n * 2048); } } while (0)
; #define PG8_WAIT_V(n) asm volatile("s_waitcnt vmcnt(" #n ")" ::: "memory")
; #define PG8_WAIT_L(n) asm volatile("s_waitcnt lgkmcnt(" #n ")" ::: "memory")
; #define PG8_BAR __builtin_amdgcn_s_barrier()
; #define PG8_SCHED __builtin_amdgcn_sched_barrier(0)
;     ...
;             PG8_LDB(B0, 0, 0); PG8_LDB(B1, 0, 1); PG8_SCHED; PG8_LDA(At, 0, 0); PG8_STAGE(PG8_SA(1, 1), a1 + hstepA, voffA);
;             PG8_WAIT_V(8); PG8_WAIT_L(0); PG8_BAR; PG8_MMA(0, 0, At, B0); PG8_MMA(0, 1, At, B1); PG8_BAR; PG8_SCHED;
;             PG8_LDA(At, 0, 1); PG8_STAGE(PG8_SB(0, 0), b2, voffB); PG8_STAGE(PG8_SB(0, 1), b2 + hstepB, voffB); PG8_STAGE(PG8_SA(0, 0), a2, voffA);
;             PG8_WAIT_V(8); PG8_WAIT_L(0); PG8_BAR; PG8_MMA(1, 0, At, B0); PG8_MMA(1, 1, At, B1); PG8_BAR; PG8_SCHED;
.LBB0_418:
	ds_read_b128 v[156:159], v150
	ds_read_b128 v[160:163], v150 offset:1024
	ds_read_b128 v[164:167], v150 offset:2048
	ds_read_b128 v[168:171], v150 offset:3072
	ds_read_b128 v[172:175], v151
	ds_read_b128 v[176:179], v151 offset:1024
	ds_read_b128 v[180:183], v151 offset:2048
	ds_read_b128 v[184:187], v151 offset:3072
	s_add_i32 s65, s28, 2
	s_add_u32 s29, s26, 0xfff80080
	s_addc_u32 s30, s27, -1
	s_cmp_eq_u32 s59, s28
	s_cselect_b32 s28, s62, s63
	s_cselect_b32 s31, s19, s30
	s_cselect_b32 s30, s21, s29
	s_cselect_b32 s29, s61, s64
	s_add_i32 m0, s45, 0xc000
	ds_read_b128 v[188:191], v152
	ds_read_b128 v[192:195], v152 offset:1024
	ds_read_b128 v[196:199], v152 offset:2048
	ds_read_b128 v[200:203], v152 offset:3072
	ds_read_b128 v[204:207], v152 offset:4096
	ds_read_b128 v[208:211], v152 offset:5120
	ds_read_b128 v[212:215], v152 offset:6144
	ds_read_b128 v[216:219], v152 offset:7168
	global_load_lds_dwordx4 v144, s[26:27]
	s_add_i32 m0, s45, 0xe000
	s_nop 0
	global_load_lds_dwordx4 v142, s[26:27]
	s_waitcnt vmcnt(8)
	s_waitcnt lgkmcnt(0)
	s_barrier
	s_setprio 1
	s_waitcnt lgkmcnt(0)
	v_mfma_f32_16x16x32_bf16 v[122:125], v[156:159], v[188:191], v[122:125]
	v_mfma_f32_16x16x32_bf16 v[126:129], v[164:167], v[188:191], v[126:129]
	v_mfma_f32_16x16x32_bf16 v[110:113], v[156:159], v[196:199], v[110:113]
	v_mfma_f32_16x16x32_bf16 v[106:109], v[164:167], v[196:199], v[106:109]
	v_mfma_f32_16x16x32_bf16 v[94:97], v[156:159], v[204:207], v[94:97]
	v_mfma_f32_16x16x32_bf16 v[90:93], v[164:167], v[204:207], v[90:93]
	v_mfma_f32_16x16x32_bf16 v[78:81], v[156:159], v[212:215], v[78:81]
	v_mfma_f32_16x16x32_bf16 v[74:77], v[164:167], v[212:215], v[74:77]
	v_mfma_f32_16x16x32_bf16 v[122:125], v[160:163], v[192:195], v[122:125]
	v_mfma_f32_16x16x32_bf16 v[126:129], v[168:171], v[192:195], v[126:129]
	v_mfma_f32_16x16x32_bf16 v[110:113], v[160:163], v[200:203], v[110:113]
	v_mfma_f32_16x16x32_bf16 v[106:109], v[168:171], v[200:203], v[106:109]
	v_mfma_f32_16x16x32_bf16 v[94:97], v[160:163], v[208:211], v[94:97]
	v_mfma_f32_16x16x32_bf16 v[90:93], v[168:171], v[208:211], v[90:93]
	v_mfma_f32_16x16x32_bf16 v[78:81], v[160:163], v[216:219], v[78:81]
	v_mfma_f32_16x16x32_bf16 v[74:77], v[168:171], v[216:219], v[74:77]
	s_setprio 0
	s_setprio 1
	v_mfma_f32_16x16x32_bf16 v[118:121], v[172:175], v[188:191], v[118:121]
	v_mfma_f32_16x16x32_bf16 v[114:117], v[180:183], v[188:191], v[114:117]
	v_mfma_f32_16x16x32_bf16 v[102:105], v[172:175], v[196:199], v[102:105]
	v_mfma_f32_16x16x32_bf16 v[98:101], v[180:183], v[196:199], v[98:101]
	v_mfma_f32_16x16x32_bf16 v[86:89], v[172:175], v[204:207], v[86:89]
	v_mfma_f32_16x16x32_bf16 v[82:85], v[180:183], v[204:207], v[82:85]
	v_mfma_f32_16x16x32_bf16 v[70:73], v[172:175], v[212:215], v[70:73]
	v_mfma_f32_16x16x32_bf16 v[66:69], v[180:183], v[212:215], v[66:69]
	v_mfma_f32_16x16x32_bf16 v[118:121], v[176:179], v[192:195], v[118:121]
	v_mfma_f32_16x16x32_bf16 v[114:117], v[184:187], v[192:195], v[114:117]
	v_mfma_f32_16x16x32_bf16 v[102:105], v[176:179], v[200:203], v[102:105]
	v_mfma_f32_16x16x32_bf16 v[98:101], v[184:187], v[200:203], v[98:101]
	v_mfma_f32_16x16x32_bf16 v[86:89], v[176:179], v[208:211], v[86:89]
	v_mfma_f32_16x16x32_bf16 v[82:85], v[184:187], v[208:211], v[82:85]
	v_mfma_f32_16x16x32_bf16 v[70:73], v[176:179], v[216:219], v[70:73]
	v_mfma_f32_16x16x32_bf16 v[66:69], v[184:187], v[216:219], v[66:69]
	s_setprio 0
	s_barrier
	s_mov_b32 m0, s41
	s_add_u32 s98, s28, 0x80
	s_addc_u32 s99, s29, 0
	s_add_u32 s66, s28, 0x80000
	ds_read_b128 v[188:191], v152 offset:16384
	ds_read_b128 v[192:195], v152 offset:17408
	ds_read_b128 v[196:199], v152 offset:18432
	ds_read_b128 v[200:203], v152 offset:19456
	ds_read_b128 v[204:207], v152 offset:20480
	ds_read_b128 v[208:211], v152 offset:21504
	ds_read_b128 v[212:215], v152 offset:22528
	ds_read_b128 v[216:219], v152 offset:23552
	global_load_lds_dwordx4 v132, s[28:29]
	s_mov_b32 m0, s42
	s_addc_u32 s67, s29, 0
	global_load_lds_dwordx4 v136, s[28:29]
	s_mov_b32 m0, s43
	s_nop 0
	global_load_lds_dwordx4 v132, s[66:67]
	s_mov_b32 m0, s44
	s_nop 0
	global_load_lds_dwordx4 v136, s[66:67]
	s_add_u32 s100, s30, 0x80
	s_addc_u32 s101, s31, 0
	s_mov_b32 m0, s45
	s_nop 0
	global_load_lds_dwordx4 v130, s[30:31]
	s_mov_b32 m0, s46
	s_nop 0
	global_load_lds_dwordx4 v134, s[30:31]
	s_waitcnt vmcnt(8)
	s_waitcnt lgkmcnt(0)
	s_barrier
	s_setprio 1
	s_waitcnt lgkmcnt(0)
	v_mfma_f32_16x16x32_bf16 v[62:65], v[156:159], v[188:191], v[62:65]
	v_mfma_f32_16x16x32_bf16 v[58:61], v[164:167], v[188:191], v[58:61]
	v_mfma_f32_16x16x32_bf16 v[46:49], v[156:159], v[196:199], v[46:49]
	v_mfma_f32_16x16x32_bf16 v[42:45], v[164:167], v[196:199], v[42:45]
	v_mfma_f32_16x16x32_bf16 v[30:33], v[156:159], v[204:207], v[30:33]
	v_mfma_f32_16x16x32_bf16 v[26:29], v[164:167], v[204:207], v[26:29]
	v_mfma_f32_16x16x32_bf16 v[14:17], v[156:159], v[212:215], v[14:17]
	v_mfma_f32_16x16x32_bf16 v[10:13], v[164:167], v[212:215], v[10:13]
	v_mfma_f32_16x16x32_bf16 v[62:65], v[160:163], v[192:195], v[62:65]
	v_mfma_f32_16x16x32_bf16 v[58:61], v[168:171], v[192:195], v[58:61]
	v_mfma_f32_16x16x32_bf16 v[46:49], v[160:163], v[200:203], v[46:49]
	v_mfma_f32_16x16x32_bf16 v[42:45], v[168:171], v[200:203], v[42:45]
	v_mfma_f32_16x16x32_bf16 v[30:33], v[160:163], v[208:211], v[30:33]
	v_mfma_f32_16x16x32_bf16 v[26:29], v[168:171], v[208:211], v[26:29]
	v_mfma_f32_16x16x32_bf16 v[14:17], v[160:163], v[216:219], v[14:17]
	v_mfma_f32_16x16x32_bf16 v[10:13], v[168:171], v[216:219], v[10:13]
	s_setprio 0
	s_setprio 1
	v_mfma_f32_16x16x32_bf16 v[54:57], v[172:175], v[188:191], v[54:57]
	v_mfma_f32_16x16x32_bf16 v[50:53], v[180:183], v[188:191], v[50:53]
	v_mfma_f32_16x16x32_bf16 v[38:41], v[172:175], v[196:199], v[38:41]
	v_mfma_f32_16x16x32_bf16 v[34:37], v[180:183], v[196:199], v[34:37]
	v_mfma_f32_16x16x32_bf16 v[22:25], v[172:175], v[204:207], v[22:25]
	v_mfma_f32_16x16x32_bf16 v[18:21], v[180:183], v[204:207], v[18:21]
	v_mfma_f32_16x16x32_bf16 v[6:9], v[172:175], v[212:215], v[6:9]
	v_mfma_f32_16x16x32_bf16 v[2:5], v[180:183], v[212:215], v[2:5]
	v_mfma_f32_16x16x32_bf16 v[54:57], v[176:179], v[192:195], v[54:57]
	v_mfma_f32_16x16x32_bf16 v[50:53], v[184:187], v[192:195], v[50:53]
	v_mfma_f32_16x16x32_bf16 v[38:41], v[176:179], v[200:203], v[38:41]
	v_mfma_f32_16x16x32_bf16 v[34:37], v[184:187], v[200:203], v[34:37]
	v_mfma_f32_16x16x32_bf16 v[22:25], v[176:179], v[208:211], v[22:25]
	v_mfma_f32_16x16x32_bf16 v[18:21], v[184:187], v[208:211], v[18:21]
	v_mfma_f32_16x16x32_bf16 v[6:9], v[176:179], v[216:219], v[6:9]
	v_mfma_f32_16x16x32_bf16 v[2:5], v[184:187], v[216:219], v[2:5]
	s_setprio 0
	s_barrier
; #define PG8_STAGE(bufoff, gbase, voff) do { _Pragma("unroll") for (int _i = 0; _i < 2; ++_i) \
;         __builtin_amdgcn_global_load_lds((const unsigned*)((const char*)(gbase) + (voff)[_i]), (PG8_LAS unsigned*)(lds + (bufoff) + ldsw + _i * 8192), 16, 0, 0); } while (0)
; #define PG8_LDA(dst, b, h) do { if constexpr (DT != 1) { _Pragma("unroll") for (int m = 0; m < 4; ++m) _Pragma("unroll") for (int k = 0; k < 2; ++k) dst[m][k] = *(const PG8_LAS bf16x8*)(lds + PG8_SA(b, h) + aoff + m * 2048 + k * 1024); } \
;         else { _Pragma("unroll") for (int m = 0; m < 4; ++m) dst##8[m] = ld32(lds + PG8_SA(b, h) + aoff + m * 2048); } } while (0)
; #define PG8_LDB(dst, b, h) do { if constexpr (DT != 1) { _Pragma("unroll") for (int n = 0; n < 2; ++n) _Pragma("unroll") for (int k = 0; k < 2; ++k) dst[n][k] = *(const PG8_LAS bf16x8*)(lds + PG8_SB(b, h) + boff + n * 2048 + k * 1024); } \
;         else { _Pragma("unroll") for (int n = 0; n < 2; ++n) dst##8[n] = ld32(lds + PG8_SB(b, h) + boff + n * 2048); } } while (0)
; #define PG8_WAIT_V(n) asm volatile("s_waitcnt vmcnt(" #n ")" ::: "memory")
; #define PG8_WAIT_L(n) asm volatile("s_waitcnt lgkmcnt(" #n ")" ::: "memory")
; #define PG8_BAR __builtin_amdgcn_s_barrier()
; #define PG8_SCHED __builtin_amdgcn_sched_barrier(0)
;     ...
;             PG8_LDB(B0, 1, 0); PG8_LDB(B1, 1, 1); PG8_SCHED; PG8_LDA(At, 1, 0); PG8_STAGE(PG8_SA(0, 1), a2 + hstepA, voffA);
;             PG8_WAIT_V(8); PG8_WAIT_L(0); PG8_BAR; PG8_MMA(0, 0, At, B0); PG8_MMA(0, 1, At, B1); PG8_BAR; PG8_SCHED;
;             PG8_LDA(At, 1, 1); PG8_STAGE(PG8_SB(1, 0), b3, voffB); PG8_STAGE(PG8_SB(1, 1), b3 + hstepB, voffB); PG8_STAGE(PG8_SA(1, 0), a3, voffA);
;             PG8_WAIT_V(8); PG8_WAIT_L(0); PG8_BAR; PG8_MMA(1, 0, At, B0); PG8_MMA(1, 1, At, B1); PG8_BAR; PG8_SCHED;
	ds_read_b128 v[156:159], v153
	ds_read_b128 v[160:163], v153 offset:1024
	ds_read_b128 v[164:167], v153 offset:2048
	ds_read_b128 v[168:171], v153 offset:3072
	ds_read_b128 v[172:175], v154
	ds_read_b128 v[176:179], v154 offset:1024
	ds_read_b128 v[180:183], v154 offset:2048
	ds_read_b128 v[184:187], v154 offset:3072
	s_add_u32 s30, s30, 0x80000
	s_addc_u32 s31, s31, 0
	s_mov_b32 m0, s47
	ds_read_b128 v[188:191], v152 offset:32768
	ds_read_b128 v[192:195], v152 offset:33792
	ds_read_b128 v[196:199], v152 offset:34816
	ds_read_b128 v[200:203], v152 offset:35840
	ds_read_b128 v[204:207], v152 offset:36864
	ds_read_b128 v[208:211], v152 offset:37888
	ds_read_b128 v[212:215], v152 offset:38912
	ds_read_b128 v[216:219], v152 offset:39936
	global_load_lds_dwordx4 v130, s[30:31]
	s_mov_b32 m0, s48
	s_nop 0
	global_load_lds_dwordx4 v134, s[30:31]
	s_waitcnt vmcnt(8)
	s_waitcnt lgkmcnt(0)
	s_barrier
	s_setprio 1
	s_waitcnt lgkmcnt(0)
	v_mfma_f32_16x16x32_bf16 v[122:125], v[156:159], v[188:191], v[122:125]
	v_mfma_f32_16x16x32_bf16 v[126:129], v[164:167], v[188:191], v[126:129]
	v_mfma_f32_16x16x32_bf16 v[110:113], v[156:159], v[196:199], v[110:113]
	v_mfma_f32_16x16x32_bf16 v[106:109], v[164:167], v[196:199], v[106:109]
	v_mfma_f32_16x16x32_bf16 v[94:97], v[156:159], v[204:207], v[94:97]
	v_mfma_f32_16x16x32_bf16 v[90:93], v[164:167], v[204:207], v[90:93]
	v_mfma_f32_16x16x32_bf16 v[78:81], v[156:159], v[212:215], v[78:81]
	v_mfma_f32_16x16x32_bf16 v[74:77], v[164:167], v[212:215], v[74:77]
	v_mfma_f32_16x16x32_bf16 v[122:125], v[160:163], v[192:195], v[122:125]
	v_mfma_f32_16x16x32_bf16 v[126:129], v[168:171], v[192:195], v[126:129]
	v_mfma_f32_16x16x32_bf16 v[110:113], v[160:163], v[200:203], v[110:113]
	v_mfma_f32_16x16x32_bf16 v[106:109], v[168:171], v[200:203], v[106:109]
	v_mfma_f32_16x16x32_bf16 v[94:97], v[160:163], v[208:211], v[94:97]
	v_mfma_f32_16x16x32_bf16 v[90:93], v[168:171], v[208:211], v[90:93]
	v_mfma_f32_16x16x32_bf16 v[78:81], v[160:163], v[216:219], v[78:81]
	v_mfma_f32_16x16x32_bf16 v[74:77], v[168:171], v[216:219], v[74:77]
	s_setprio 0
	s_setprio 1
	v_mfma_f32_16x16x32_bf16 v[118:121], v[172:175], v[188:191], v[118:121]
	v_mfma_f32_16x16x32_bf16 v[114:117], v[180:183], v[188:191], v[114:117]
	v_mfma_f32_16x16x32_bf16 v[102:105], v[172:175], v[196:199], v[102:105]
	v_mfma_f32_16x16x32_bf16 v[98:101], v[180:183], v[196:199], v[98:101]
	v_mfma_f32_16x16x32_bf16 v[86:89], v[172:175], v[204:207], v[86:89]
	v_mfma_f32_16x16x32_bf16 v[82:85], v[180:183], v[204:207], v[82:85]
	v_mfma_f32_16x16x32_bf16 v[70:73], v[172:175], v[212:215], v[70:73]
	v_mfma_f32_16x16x32_bf16 v[66:69], v[180:183], v[212:215], v[66:69]
	v_mfma_f32_16x16x32_bf16 v[118:121], v[176:179], v[192:195], v[118:121]
	v_mfma_f32_16x16x32_bf16 v[114:117], v[184:187], v[192:195], v[114:117]
	v_mfma_f32_16x16x32_bf16 v[102:105], v[176:179], v[200:203], v[102:105]
	v_mfma_f32_16x16x32_bf16 v[98:101], v[184:187], v[200:203], v[98:101]
	v_mfma_f32_16x16x32_bf16 v[86:89], v[176:179], v[208:211], v[86:89]
	v_mfma_f32_16x16x32_bf16 v[82:85], v[184:187], v[208:211], v[82:85]
	v_mfma_f32_16x16x32_bf16 v[70:73], v[176:179], v[216:219], v[70:73]
	v_mfma_f32_16x16x32_bf16 v[66:69], v[184:187], v[216:219], v[66:69]
	s_setprio 0
	s_barrier
	s_mov_b32 m0, s50
	s_add_u32 s28, s28, 0x80080
	ds_read_b128 v[188:191], v152 offset:49152
	ds_read_b128 v[192:195], v152 offset:50176
	ds_read_b128 v[196:199], v152 offset:51200
	ds_read_b128 v[200:203], v152 offset:52224
	ds_read_b128 v[204:207], v152 offset:53248
	ds_read_b128 v[208:211], v152 offset:54272
	ds_read_b128 v[212:215], v152 offset:55296
	ds_read_b128 v[216:219], v152 offset:56320
	global_load_lds_dwordx4 v132, s[98:99]
	s_mov_b32 m0, s51
	s_addc_u32 s29, s29, 0
	global_load_lds_dwordx4 v136, s[98:99]
	s_mov_b32 m0, s54
	s_nop 0
	global_load_lds_dwordx4 v132, s[28:29]
	s_mov_b32 m0, s55
	s_nop 0
	global_load_lds_dwordx4 v136, s[28:29]
	s_mov_b32 m0, s52
	s_nop 0
	global_load_lds_dwordx4 v130, s[100:101]
	s_mov_b32 m0, s53
	s_nop 0
	global_load_lds_dwordx4 v134, s[100:101]
	s_waitcnt vmcnt(8)
	s_waitcnt lgkmcnt(0)
	s_barrier
	s_setprio 1
	s_waitcnt lgkmcnt(0)
	v_mfma_f32_16x16x32_bf16 v[62:65], v[156:159], v[188:191], v[62:65]
	v_mfma_f32_16x16x32_bf16 v[58:61], v[164:167], v[188:191], v[58:61]
	v_mfma_f32_16x16x32_bf16 v[46:49], v[156:159], v[196:199], v[46:49]
	v_mfma_f32_16x16x32_bf16 v[42:45], v[164:167], v[196:199], v[42:45]
	v_mfma_f32_16x16x32_bf16 v[30:33], v[156:159], v[204:207], v[30:33]
	v_mfma_f32_16x16x32_bf16 v[26:29], v[164:167], v[204:207], v[26:29]
	v_mfma_f32_16x16x32_bf16 v[14:17], v[156:159], v[212:215], v[14:17]
	v_mfma_f32_16x16x32_bf16 v[10:13], v[164:167], v[212:215], v[10:13]
	v_mfma_f32_16x16x32_bf16 v[62:65], v[160:163], v[192:195], v[62:65]
	v_mfma_f32_16x16x32_bf16 v[58:61], v[168:171], v[192:195], v[58:61]
	v_mfma_f32_16x16x32_bf16 v[46:49], v[160:163], v[200:203], v[46:49]
	v_mfma_f32_16x16x32_bf16 v[42:45], v[168:171], v[200:203], v[42:45]
	v_mfma_f32_16x16x32_bf16 v[30:33], v[160:163], v[208:211], v[30:33]
	v_mfma_f32_16x16x32_bf16 v[26:29], v[168:171], v[208:211], v[26:29]
	v_mfma_f32_16x16x32_bf16 v[14:17], v[160:163], v[216:219], v[14:17]
	v_mfma_f32_16x16x32_bf16 v[10:13], v[168:171], v[216:219], v[10:13]
	s_setprio 0
	s_setprio 1
	v_mfma_f32_16x16x32_bf16 v[54:57], v[172:175], v[188:191], v[54:57]
	v_mfma_f32_16x16x32_bf16 v[50:53], v[180:183], v[188:191], v[50:53]
	v_mfma_f32_16x16x32_bf16 v[38:41], v[172:175], v[196:199], v[38:41]
	v_mfma_f32_16x16x32_bf16 v[34:37], v[180:183], v[196:199], v[34:37]
	v_mfma_f32_16x16x32_bf16 v[22:25], v[172:175], v[204:207], v[22:25]
	v_mfma_f32_16x16x32_bf16 v[18:21], v[180:183], v[204:207], v[18:21]
	v_mfma_f32_16x16x32_bf16 v[6:9], v[172:175], v[212:215], v[6:9]
	v_mfma_f32_16x16x32_bf16 v[2:5], v[180:183], v[212:215], v[2:5]
	v_mfma_f32_16x16x32_bf16 v[54:57], v[176:179], v[192:195], v[54:57]
	v_mfma_f32_16x16x32_bf16 v[50:53], v[184:187], v[192:195], v[50:53]
	v_mfma_f32_16x16x32_bf16 v[38:41], v[176:179], v[200:203], v[38:41]
	v_mfma_f32_16x16x32_bf16 v[34:37], v[184:187], v[200:203], v[34:37]
	v_mfma_f32_16x16x32_bf16 v[22:25], v[176:179], v[208:211], v[22:25]
	v_mfma_f32_16x16x32_bf16 v[18:21], v[184:187], v[208:211], v[18:21]
	v_mfma_f32_16x16x32_bf16 v[6:9], v[176:179], v[216:219], v[6:9]
	v_mfma_f32_16x16x32_bf16 v[2:5], v[184:187], v[216:219], v[2:5]
	s_setprio 0
	s_barrier
	s_add_u32 s63, s63, 0x100
	s_addc_u32 s64, s64, 0
	s_add_u32 s26, s26, 0x100
	s_addc_u32 s27, s27, 0
	s_cmp_ge_i32 s65, s49
	s_mov_b32 s28, s65
	s_cbranch_scc0 .LBB0_418

; #define PG8_STAGE(bufoff, gbase, voff) do { _Pragma("unroll") for (int _i = 0; _i < 2; ++_i) \
;         __builtin_amdgcn_global_load_lds((const unsigned*)((const char*)(gbase) + (voff)[_i]), (PG8_LAS unsigned*)(lds + (bufoff) + ldsw + _i * 8192), 16, 0, 0); } while (0)
; #define PG8_LDA(dst, b, h) do { if constexpr (DT != 1) { _Pragma("unroll") for (int m = 0; m < 4; ++m) _Pragma("unroll") for (int k = 0; k < 2; ++k) dst[m][k] = *(const PG8_LAS bf16x8*)(lds + PG8_SA(b, h) + aoff + m * 2048 + k * 1024); } \
;         else { _Pragma("unroll") for (int m = 0; m < 4; ++m) dst##8[m] = ld32(lds + PG8_SA(b, h) + aoff + m * 2048); } } while (0)
; #define PG8_LDB(dst, b, h) do { if constexpr (DT != 1) { _Pragma("unroll") for (int n = 0; n < 2; ++n) _Pragma("unroll") for (int k = 0; k < 2; ++k) dst[n][k] = *(const PG8_LAS bf16x8*)(lds + PG8_SB(b, h) + boff + n * 2048 + k * 1024); } \
;         else { _Pragma("unroll") for (int n = 0; n < 2; ++n) dst##8[n] = ld32(lds + PG8_SB(b, h) + boff + n * 2048); } } while (0)
; #define PG8_WAIT_V(n) asm volatile("s_waitcnt vmcnt(" #n ")" ::: "memory")
; #define PG8_WAIT_L(n) asm volatile("s_waitcnt lgkmcnt(" #n ")" ::: "memory")
; #define PG8_BAR __builtin_amdgcn_s_barrier()
; #define PG8_SCHED __builtin_amdgcn_sched_barrier(0)
;     ...
;             const char* a1 = cA + (size_t)(t + 1) * kstep;
;             const char* a2 = last ? nA : cA + (size_t)(t + 2) * kstep; const char* b2 = last ? nB : cB + (size_t)(t + 2) * kstep;
;             const char* a3 = a2 + kstep; const char* b3 = b2 + kstep;
;             if (last && has_next) S.a_ready(nxt);
;             if constexpr (SP2) {
;             PG8_LDB(B0, 0, 0); PG8_LDB(B1, 0, 1); PG8_SCHED; PG8_LDA(At, 0, 0); PG8_STAGE(PG8_SA(1, 1), a1 + hstepA, voffA);
;             PG8_WAIT_V(8); PG8_WAIT_L(0); PG8_BAR; PG8_MMA(0, 0, At, B0); PG8_MMA(0, 1, At, B1); PG8_BAR; PG8_SCHED;
;             PG8_LDA(At, 0, 1); PG8_STAGE(PG8_SB(0, 0), b2, voffB); PG8_STAGE(PG8_SB(0, 1), b2 + hstepB, voffB); PG8_STAGE(PG8_SA(0, 0), a2, voffA);
;             PG8_WAIT_V(8); PG8_WAIT_L(0); PG8_BAR; PG8_MMA(1, 0, At, B0); PG8_MMA(1, 1, At, B1); PG8_BAR; PG8_SCHED;
.LBB0_713:
	ds_read_b128 v[130:133], v173
	ds_read_b128 v[134:137], v173 offset:1024
	ds_read_b128 v[138:141], v173 offset:2048
	ds_read_b128 v[142:145], v173 offset:3072
	ds_read_b128 v[162:165], v174
	ds_read_b128 v[166:169], v174 offset:1024
	ds_read_b128 v[178:181], v174 offset:2048
	ds_read_b128 v[182:185], v174 offset:3072
	s_add_i32 s69, s36, 2
	s_add_u32 s37, s34, 0xfff80080
	s_addc_u32 s38, s35, -1
	s_cmp_eq_u32 s61, s36
	s_cselect_b32 s36, s66, s67
	s_cselect_b32 s39, s23, s38
	s_cselect_b32 s38, s25, s37
	s_cselect_b32 s37, s65, s68
	s_add_i32 m0, s49, 0xc000
	ds_read_b128 v[186:189], v175
	ds_read_b128 v[190:193], v175 offset:1024
	ds_read_b128 v[194:197], v175 offset:2048
	ds_read_b128 v[198:201], v175 offset:3072
	ds_read_b128 v[202:205], v175 offset:4096
	ds_read_b128 v[206:209], v175 offset:5120
	ds_read_b128 v[210:213], v175 offset:6144
	ds_read_b128 v[214:217], v175 offset:7168
	global_load_lds_dwordx4 v156, s[34:35]
	s_add_i32 m0, s49, 0xe000
	s_nop 0
	global_load_lds_dwordx4 v154, s[34:35]
	s_waitcnt vmcnt(8)
	s_waitcnt lgkmcnt(0)
	s_barrier
	s_setprio 1
	s_waitcnt lgkmcnt(0)
	v_mfma_f32_16x16x32_bf16 v[122:125], v[130:133], v[186:189], v[122:125]
	v_mfma_f32_16x16x32_bf16 v[126:129], v[138:141], v[186:189], v[126:129]
	v_mfma_f32_16x16x32_bf16 v[110:113], v[130:133], v[194:197], v[110:113]
	v_mfma_f32_16x16x32_bf16 v[106:109], v[138:141], v[194:197], v[106:109]
	v_mfma_f32_16x16x32_bf16 v[94:97], v[130:133], v[202:205], v[94:97]
	v_mfma_f32_16x16x32_bf16 v[90:93], v[138:141], v[202:205], v[90:93]
	v_mfma_f32_16x16x32_bf16 v[78:81], v[130:133], v[210:213], v[78:81]
	v_mfma_f32_16x16x32_bf16 v[74:77], v[138:141], v[210:213], v[74:77]
	v_mfma_f32_16x16x32_bf16 v[122:125], v[134:137], v[190:193], v[122:125]
	v_mfma_f32_16x16x32_bf16 v[126:129], v[142:145], v[190:193], v[126:129]
	v_mfma_f32_16x16x32_bf16 v[110:113], v[134:137], v[198:201], v[110:113]
	v_mfma_f32_16x16x32_bf16 v[106:109], v[142:145], v[198:201], v[106:109]
	v_mfma_f32_16x16x32_bf16 v[94:97], v[134:137], v[206:209], v[94:97]
	v_mfma_f32_16x16x32_bf16 v[90:93], v[142:145], v[206:209], v[90:93]
	v_mfma_f32_16x16x32_bf16 v[78:81], v[134:137], v[214:217], v[78:81]
	v_mfma_f32_16x16x32_bf16 v[74:77], v[142:145], v[214:217], v[74:77]
	s_setprio 0
	s_setprio 1
	v_mfma_f32_16x16x32_bf16 v[118:121], v[162:165], v[186:189], v[118:121]
	v_mfma_f32_16x16x32_bf16 v[114:117], v[178:181], v[186:189], v[114:117]
	v_mfma_f32_16x16x32_bf16 v[102:105], v[162:165], v[194:197], v[102:105]
	v_mfma_f32_16x16x32_bf16 v[98:101], v[178:181], v[194:197], v[98:101]
	v_mfma_f32_16x16x32_bf16 v[86:89], v[162:165], v[202:205], v[86:89]
	v_mfma_f32_16x16x32_bf16 v[82:85], v[178:181], v[202:205], v[82:85]
	v_mfma_f32_16x16x32_bf16 v[70:73], v[162:165], v[210:213], v[70:73]
	v_mfma_f32_16x16x32_bf16 v[66:69], v[178:181], v[210:213], v[66:69]
	v_mfma_f32_16x16x32_bf16 v[118:121], v[166:169], v[190:193], v[118:121]
	v_mfma_f32_16x16x32_bf16 v[114:117], v[182:185], v[190:193], v[114:117]
	v_mfma_f32_16x16x32_bf16 v[102:105], v[166:169], v[198:201], v[102:105]
	v_mfma_f32_16x16x32_bf16 v[98:101], v[182:185], v[198:201], v[98:101]
	v_mfma_f32_16x16x32_bf16 v[86:89], v[166:169], v[206:209], v[86:89]
	v_mfma_f32_16x16x32_bf16 v[82:85], v[182:185], v[206:209], v[82:85]
	v_mfma_f32_16x16x32_bf16 v[70:73], v[166:169], v[214:217], v[70:73]
	v_mfma_f32_16x16x32_bf16 v[66:69], v[182:185], v[214:217], v[66:69]
	s_setprio 0
	s_barrier
	s_mov_b32 m0, s31
	s_add_u32 s98, s36, 0x80
	s_addc_u32 s99, s37, 0
	s_add_u32 s70, s36, 0x80000
	ds_read_b128 v[186:189], v175 offset:16384
	ds_read_b128 v[190:193], v175 offset:17408
	ds_read_b128 v[194:197], v175 offset:18432
	ds_read_b128 v[198:201], v175 offset:19456
	ds_read_b128 v[202:205], v175 offset:20480
	ds_read_b128 v[206:209], v175 offset:21504
	ds_read_b128 v[210:213], v175 offset:22528
	ds_read_b128 v[214:217], v175 offset:23552
	global_load_lds_dwordx4 v148, s[36:37]
	s_mov_b32 m0, s46
	s_addc_u32 s71, s37, 0
	global_load_lds_dwordx4 v152, s[36:37]
	s_mov_b32 m0, s47
	s_nop 0
	global_load_lds_dwordx4 v148, s[70:71]
	s_mov_b32 m0, s48
	s_nop 0
	global_load_lds_dwordx4 v152, s[70:71]
	s_add_u32 s100, s38, 0x80
	s_addc_u32 s101, s39, 0
	s_mov_b32 m0, s49
	s_nop 0
	global_load_lds_dwordx4 v146, s[38:39]
	s_mov_b32 m0, s50
	s_nop 0
	global_load_lds_dwordx4 v150, s[38:39]
	s_waitcnt vmcnt(8)
	s_waitcnt lgkmcnt(0)
	s_barrier
	s_setprio 1
	s_waitcnt lgkmcnt(0)
	v_mfma_f32_16x16x32_bf16 v[62:65], v[130:133], v[186:189], v[62:65]
	v_mfma_f32_16x16x32_bf16 v[58:61], v[138:141], v[186:189], v[58:61]
	v_mfma_f32_16x16x32_bf16 v[46:49], v[130:133], v[194:197], v[46:49]
	v_mfma_f32_16x16x32_bf16 v[42:45], v[138:141], v[194:197], v[42:45]
	v_mfma_f32_16x16x32_bf16 v[30:33], v[130:133], v[202:205], v[30:33]
	v_mfma_f32_16x16x32_bf16 v[26:29], v[138:141], v[202:205], v[26:29]
	v_mfma_f32_16x16x32_bf16 v[14:17], v[130:133], v[210:213], v[14:17]
	v_mfma_f32_16x16x32_bf16 v[10:13], v[138:141], v[210:213], v[10:13]
	v_mfma_f32_16x16x32_bf16 v[62:65], v[134:137], v[190:193], v[62:65]
	v_mfma_f32_16x16x32_bf16 v[58:61], v[142:145], v[190:193], v[58:61]
	v_mfma_f32_16x16x32_bf16 v[46:49], v[134:137], v[198:201], v[46:49]
	v_mfma_f32_16x16x32_bf16 v[42:45], v[142:145], v[198:201], v[42:45]
	v_mfma_f32_16x16x32_bf16 v[30:33], v[134:137], v[206:209], v[30:33]
	v_mfma_f32_16x16x32_bf16 v[26:29], v[142:145], v[206:209], v[26:29]
	v_mfma_f32_16x16x32_bf16 v[14:17], v[134:137], v[214:217], v[14:17]
	v_mfma_f32_16x16x32_bf16 v[10:13], v[142:145], v[214:217], v[10:13]
	s_setprio 0
	s_setprio 1
	v_mfma_f32_16x16x32_bf16 v[54:57], v[162:165], v[186:189], v[54:57]
	v_mfma_f32_16x16x32_bf16 v[50:53], v[178:181], v[186:189], v[50:53]
	v_mfma_f32_16x16x32_bf16 v[38:41], v[162:165], v[194:197], v[38:41]
	v_mfma_f32_16x16x32_bf16 v[34:37], v[178:181], v[194:197], v[34:37]
	v_mfma_f32_16x16x32_bf16 v[22:25], v[162:165], v[202:205], v[22:25]
	v_mfma_f32_16x16x32_bf16 v[18:21], v[178:181], v[202:205], v[18:21]
	v_mfma_f32_16x16x32_bf16 v[6:9], v[162:165], v[210:213], v[6:9]
	v_mfma_f32_16x16x32_bf16 v[2:5], v[178:181], v[210:213], v[2:5]
	v_mfma_f32_16x16x32_bf16 v[54:57], v[166:169], v[190:193], v[54:57]
	v_mfma_f32_16x16x32_bf16 v[50:53], v[182:185], v[190:193], v[50:53]
	v_mfma_f32_16x16x32_bf16 v[38:41], v[166:169], v[198:201], v[38:41]
	v_mfma_f32_16x16x32_bf16 v[34:37], v[182:185], v[198:201], v[34:37]
	v_mfma_f32_16x16x32_bf16 v[22:25], v[166:169], v[206:209], v[22:25]
	v_mfma_f32_16x16x32_bf16 v[18:21], v[182:185], v[206:209], v[18:21]
	v_mfma_f32_16x16x32_bf16 v[6:9], v[166:169], v[214:217], v[6:9]
	v_mfma_f32_16x16x32_bf16 v[2:5], v[182:185], v[214:217], v[2:5]
	s_setprio 0
	s_barrier
; #define PG8_STAGE(bufoff, gbase, voff) do { _Pragma("unroll") for (int _i = 0; _i < 2; ++_i) \
;         __builtin_amdgcn_global_load_lds((const unsigned*)((const char*)(gbase) + (voff)[_i]), (PG8_LAS unsigned*)(lds + (bufoff) + ldsw + _i * 8192), 16, 0, 0); } while (0)
; #define PG8_LDA(dst, b, h) do { if constexpr (DT != 1) { _Pragma("unroll") for (int m = 0; m < 4; ++m) _Pragma("unroll") for (int k = 0; k < 2; ++k) dst[m][k] = *(const PG8_LAS bf16x8*)(lds + PG8_SA(b, h) + aoff + m * 2048 + k * 1024); } \
;         else { _Pragma("unroll") for (int m = 0; m < 4; ++m) dst##8[m] = ld32(lds + PG8_SA(b, h) + aoff + m * 2048); } } while (0)
; #define PG8_LDB(dst, b, h) do { if constexpr (DT != 1) { _Pragma("unroll") for (int n = 0; n < 2; ++n) _Pragma("unroll") for (int k = 0; k < 2; ++k) dst[n][k] = *(const PG8_LAS bf16x8*)(lds + PG8_SB(b, h) + boff + n * 2048 + k * 1024); } \
;         else { _Pragma("unroll") for (int n = 0; n < 2; ++n) dst##8[n] = ld32(lds + PG8_SB(b, h) + boff + n * 2048); } } while (0)
; #define PG8_WAIT_V(n) asm volatile("s_waitcnt vmcnt(" #n ")" ::: "memory")
; #define PG8_WAIT_L(n) asm volatile("s_waitcnt lgkmcnt(" #n ")" ::: "memory")
; #define PG8_BAR __builtin_amdgcn_s_barrier()
; #define PG8_SCHED __builtin_amdgcn_sched_barrier(0)
;     ...
;             PG8_LDB(B0, 1, 0); PG8_LDB(B1, 1, 1); PG8_SCHED; PG8_LDA(At, 1, 0); PG8_STAGE(PG8_SA(0, 1), a2 + hstepA, voffA);
;             PG8_WAIT_V(8); PG8_WAIT_L(0); PG8_BAR; PG8_MMA(0, 0, At, B0); PG8_MMA(0, 1, At, B1); PG8_BAR; PG8_SCHED;
;             PG8_LDA(At, 1, 1); PG8_STAGE(PG8_SB(1, 0), b3, voffB); PG8_STAGE(PG8_SB(1, 1), b3 + hstepB, voffB); PG8_STAGE(PG8_SA(1, 0), a3, voffA);
;             PG8_WAIT_V(8); PG8_WAIT_L(0); PG8_BAR; PG8_MMA(1, 0, At, B0); PG8_MMA(1, 1, At, B1); PG8_BAR; PG8_SCHED;
	ds_read_b128 v[130:133], v176
	ds_read_b128 v[134:137], v176 offset:1024
	ds_read_b128 v[138:141], v176 offset:2048
	ds_read_b128 v[142:145], v176 offset:3072
	ds_read_b128 v[162:165], v177
	ds_read_b128 v[166:169], v177 offset:1024
	ds_read_b128 v[178:181], v177 offset:2048
	ds_read_b128 v[182:185], v177 offset:3072
	s_add_u32 s38, s38, 0x80000
	s_addc_u32 s39, s39, 0
	s_mov_b32 m0, s51
	ds_read_b128 v[186:189], v175 offset:32768
	ds_read_b128 v[190:193], v175 offset:33792
	ds_read_b128 v[194:197], v175 offset:34816
	ds_read_b128 v[198:201], v175 offset:35840
	ds_read_b128 v[202:205], v175 offset:36864
	ds_read_b128 v[206:209], v175 offset:37888
	ds_read_b128 v[210:213], v175 offset:38912
	ds_read_b128 v[214:217], v175 offset:39936
	global_load_lds_dwordx4 v146, s[38:39]
	s_mov_b32 m0, s52
	s_nop 0
	global_load_lds_dwordx4 v150, s[38:39]
	s_waitcnt vmcnt(8)
	s_waitcnt lgkmcnt(0)
	s_barrier
	s_setprio 1
	s_waitcnt lgkmcnt(0)
	v_mfma_f32_16x16x32_bf16 v[122:125], v[130:133], v[186:189], v[122:125]
	v_mfma_f32_16x16x32_bf16 v[126:129], v[138:141], v[186:189], v[126:129]
	v_mfma_f32_16x16x32_bf16 v[110:113], v[130:133], v[194:197], v[110:113]
	v_mfma_f32_16x16x32_bf16 v[106:109], v[138:141], v[194:197], v[106:109]
	v_mfma_f32_16x16x32_bf16 v[94:97], v[130:133], v[202:205], v[94:97]
	v_mfma_f32_16x16x32_bf16 v[90:93], v[138:141], v[202:205], v[90:93]
	v_mfma_f32_16x16x32_bf16 v[78:81], v[130:133], v[210:213], v[78:81]
	v_mfma_f32_16x16x32_bf16 v[74:77], v[138:141], v[210:213], v[74:77]
	v_mfma_f32_16x16x32_bf16 v[122:125], v[134:137], v[190:193], v[122:125]
	v_mfma_f32_16x16x32_bf16 v[126:129], v[142:145], v[190:193], v[126:129]
	v_mfma_f32_16x16x32_bf16 v[110:113], v[134:137], v[198:201], v[110:113]
	v_mfma_f32_16x16x32_bf16 v[106:109], v[142:145], v[198:201], v[106:109]
	v_mfma_f32_16x16x32_bf16 v[94:97], v[134:137], v[206:209], v[94:97]
	v_mfma_f32_16x16x32_bf16 v[90:93], v[142:145], v[206:209], v[90:93]
	v_mfma_f32_16x16x32_bf16 v[78:81], v[134:137], v[214:217], v[78:81]
	v_mfma_f32_16x16x32_bf16 v[74:77], v[142:145], v[214:217], v[74:77]
	s_setprio 0
	s_setprio 1
	v_mfma_f32_16x16x32_bf16 v[118:121], v[162:165], v[186:189], v[118:121]
	v_mfma_f32_16x16x32_bf16 v[114:117], v[178:181], v[186:189], v[114:117]
	v_mfma_f32_16x16x32_bf16 v[102:105], v[162:165], v[194:197], v[102:105]
	v_mfma_f32_16x16x32_bf16 v[98:101], v[178:181], v[194:197], v[98:101]
	v_mfma_f32_16x16x32_bf16 v[86:89], v[162:165], v[202:205], v[86:89]
	v_mfma_f32_16x16x32_bf16 v[82:85], v[178:181], v[202:205], v[82:85]
	v_mfma_f32_16x16x32_bf16 v[70:73], v[162:165], v[210:213], v[70:73]
	v_mfma_f32_16x16x32_bf16 v[66:69], v[178:181], v[210:213], v[66:69]
	v_mfma_f32_16x16x32_bf16 v[118:121], v[166:169], v[190:193], v[118:121]
	v_mfma_f32_16x16x32_bf16 v[114:117], v[182:185], v[190:193], v[114:117]
	v_mfma_f32_16x16x32_bf16 v[102:105], v[166:169], v[198:201], v[102:105]
	v_mfma_f32_16x16x32_bf16 v[98:101], v[182:185], v[198:201], v[98:101]
	v_mfma_f32_16x16x32_bf16 v[86:89], v[166:169], v[206:209], v[86:89]
	v_mfma_f32_16x16x32_bf16 v[82:85], v[182:185], v[206:209], v[82:85]
	v_mfma_f32_16x16x32_bf16 v[70:73], v[166:169], v[214:217], v[70:73]
	v_mfma_f32_16x16x32_bf16 v[66:69], v[182:185], v[214:217], v[66:69]
	s_setprio 0
	s_barrier
	s_mov_b32 m0, s55
	s_add_u32 s36, s36, 0x80080
	ds_read_b128 v[186:189], v175 offset:49152
	ds_read_b128 v[190:193], v175 offset:50176
	ds_read_b128 v[194:197], v175 offset:51200
	ds_read_b128 v[198:201], v175 offset:52224
	ds_read_b128 v[202:205], v175 offset:53248
	ds_read_b128 v[206:209], v175 offset:54272
	ds_read_b128 v[210:213], v175 offset:55296
	ds_read_b128 v[214:217], v175 offset:56320
	global_load_lds_dwordx4 v148, s[98:99]
	s_mov_b32 m0, s56
	s_addc_u32 s37, s37, 0
	global_load_lds_dwordx4 v152, s[98:99]
	s_mov_b32 m0, s59
	s_nop 0
	global_load_lds_dwordx4 v148, s[36:37]
	s_mov_b32 m0, s60
	s_nop 0
	global_load_lds_dwordx4 v152, s[36:37]
	s_mov_b32 m0, s57
	s_nop 0
	global_load_lds_dwordx4 v146, s[100:101]
	s_mov_b32 m0, s58
	s_nop 0
	global_load_lds_dwordx4 v150, s[100:101]
	s_waitcnt vmcnt(8)
	s_waitcnt lgkmcnt(0)
	s_barrier
	s_setprio 1
	s_waitcnt lgkmcnt(0)
	v_mfma_f32_16x16x32_bf16 v[62:65], v[130:133], v[186:189], v[62:65]
	v_mfma_f32_16x16x32_bf16 v[58:61], v[138:141], v[186:189], v[58:61]
	v_mfma_f32_16x16x32_bf16 v[46:49], v[130:133], v[194:197], v[46:49]
	v_mfma_f32_16x16x32_bf16 v[42:45], v[138:141], v[194:197], v[42:45]
	v_mfma_f32_16x16x32_bf16 v[30:33], v[130:133], v[202:205], v[30:33]
	v_mfma_f32_16x16x32_bf16 v[26:29], v[138:141], v[202:205], v[26:29]
	v_mfma_f32_16x16x32_bf16 v[14:17], v[130:133], v[210:213], v[14:17]
	v_mfma_f32_16x16x32_bf16 v[10:13], v[138:141], v[210:213], v[10:13]
	v_mfma_f32_16x16x32_bf16 v[62:65], v[134:137], v[190:193], v[62:65]
	v_mfma_f32_16x16x32_bf16 v[58:61], v[142:145], v[190:193], v[58:61]
	v_mfma_f32_16x16x32_bf16 v[46:49], v[134:137], v[198:201], v[46:49]
	v_mfma_f32_16x16x32_bf16 v[42:45], v[142:145], v[198:201], v[42:45]
	v_mfma_f32_16x16x32_bf16 v[30:33], v[134:137], v[206:209], v[30:33]
	v_mfma_f32_16x16x32_bf16 v[26:29], v[142:145], v[206:209], v[26:29]
	v_mfma_f32_16x16x32_bf16 v[14:17], v[134:137], v[214:217], v[14:17]
	v_mfma_f32_16x16x32_bf16 v[10:13], v[142:145], v[214:217], v[10:13]
	s_setprio 0
	s_setprio 1
	v_mfma_f32_16x16x32_bf16 v[54:57], v[162:165], v[186:189], v[54:57]
	v_mfma_f32_16x16x32_bf16 v[50:53], v[178:181], v[186:189], v[50:53]
	v_mfma_f32_16x16x32_bf16 v[38:41], v[162:165], v[194:197], v[38:41]
	v_mfma_f32_16x16x32_bf16 v[34:37], v[178:181], v[194:197], v[34:37]
	v_mfma_f32_16x16x32_bf16 v[22:25], v[162:165], v[202:205], v[22:25]
	v_mfma_f32_16x16x32_bf16 v[18:21], v[178:181], v[202:205], v[18:21]
	v_mfma_f32_16x16x32_bf16 v[6:9], v[162:165], v[210:213], v[6:9]
	v_mfma_f32_16x16x32_bf16 v[2:5], v[178:181], v[210:213], v[2:5]
	v_mfma_f32_16x16x32_bf16 v[54:57], v[166:169], v[190:193], v[54:57]
	v_mfma_f32_16x16x32_bf16 v[50:53], v[182:185], v[190:193], v[50:53]
	v_mfma_f32_16x16x32_bf16 v[38:41], v[166:169], v[198:201], v[38:41]
	v_mfma_f32_16x16x32_bf16 v[34:37], v[182:185], v[198:201], v[34:37]
	v_mfma_f32_16x16x32_bf16 v[22:25], v[166:169], v[206:209], v[22:25]
	v_mfma_f32_16x16x32_bf16 v[18:21], v[182:185], v[206:209], v[18:21]
	v_mfma_f32_16x16x32_bf16 v[6:9], v[166:169], v[214:217], v[6:9]
	v_mfma_f32_16x16x32_bf16 v[2:5], v[182:185], v[214:217], v[2:5]
	s_setprio 0
	s_barrier
	s_add_u32 s67, s67, 0x100
	s_addc_u32 s68, s68, 0
	s_add_u32 s34, s34, 0x100
	s_addc_u32 s35, s35, 0
	s_cmp_ge_i32 s69, s54
	s_mov_b32 s36, s69
	s_cbranch_scc0 .LBB0_713

; #define PG8_STAGE(bufoff, gbase, voff) do { _Pragma("unroll") for (int _i = 0; _i < 2; ++_i) \
;         __builtin_amdgcn_global_load_lds((const unsigned*)((const char*)(gbase) + (voff)[_i]), (PG8_LAS unsigned*)(lds + (bufoff) + ldsw + _i * 8192), 16, 0, 0); } while (0)
; #define PG8_LDA(dst, b, h) do { if constexpr (DT != 1) { _Pragma("unroll") for (int m = 0; m < 4; ++m) _Pragma("unroll") for (int k = 0; k < 2; ++k) dst[m][k] = *(const PG8_LAS bf16x8*)(lds + PG8_SA(b, h) + aoff + m * 2048 + k * 1024); } \
;         else { _Pragma("unroll") for (int m = 0; m < 4; ++m) dst##8[m] = ld32(lds + PG8_SA(b, h) + aoff + m * 2048); } } while (0)
; #define PG8_LDB(dst, b, h) do { if constexpr (DT != 1) { _Pragma("unroll") for (int n = 0; n < 2; ++n) _Pragma("unroll") for (int k = 0; k < 2; ++k) dst[n][k] = *(const PG8_LAS bf16x8*)(lds + PG8_SB(b, h) + boff + n * 2048 + k * 1024); } \
;         else { _Pragma("unroll") for (int n = 0; n < 2; ++n) dst##8[n] = ld32(lds + PG8_SB(b, h) + boff + n * 2048); } } while (0)
; #define PG8_WAIT_V(n) asm volatile("s_waitcnt vmcnt(" #n ")" ::: "memory")
; #define PG8_WAIT_L(n) asm volatile("s_waitcnt lgkmcnt(" #n ")" ::: "memory")
; #define PG8_BAR __builtin_amdgcn_s_barrier()
; #define PG8_SCHED __builtin_amdgcn_sched_barrier(0)
;     ...
;             const char* a1 = cA + (size_t)(t + 1) * kstep;
;             const char* a2 = last ? nA : cA + (size_t)(t + 2) * kstep; const char* b2 = last ? nB : cB + (size_t)(t + 2) * kstep;
;             const char* a3 = a2 + kstep; const char* b3 = b2 + kstep;
;             if (last && has_next) S.a_ready(nxt);
;             if constexpr (SP2) {
;             PG8_LDB(B0, 0, 0); PG8_LDB(B1, 0, 1); PG8_SCHED; PG8_LDA(At, 0, 0); PG8_STAGE(PG8_SA(1, 1), a1 + hstepA, voffA);
;             PG8_WAIT_V(8); PG8_WAIT_L(0); PG8_BAR; PG8_MMA(0, 0, At, B0); PG8_MMA(0, 1, At, B1); PG8_BAR; PG8_SCHED;
;             PG8_LDA(At, 0, 1); PG8_STAGE(PG8_SB(0, 0), b2, voffB); PG8_STAGE(PG8_SB(0, 1), b2 + hstepB, voffB); PG8_STAGE(PG8_SA(0, 0), a2, voffA);
;             PG8_WAIT_V(8); PG8_WAIT_L(0); PG8_BAR; PG8_MMA(1, 0, At, B0); PG8_MMA(1, 1, At, B1); PG8_BAR; PG8_SCHED;
.LBB0_1412:
	v_add_u32_e32 v162, s35, v168
	v_add_u32_e32 v166, s36, v168
	ds_read_b128 v[150:153], v162
	ds_read_b128 v[154:157], v162 offset:1024
	ds_read_b128 v[158:161], v162 offset:2048
	ds_read_b128 v[162:165], v162 offset:3072
	ds_read_b128 v[178:181], v166
	ds_read_b128 v[182:185], v166 offset:1024
	ds_read_b128 v[186:189], v166 offset:2048
	ds_read_b128 v[190:193], v166 offset:3072
	s_add_i32 s68, s26, 2
	s_add_u32 s27, s24, 0xfffc0080
	s_addc_u32 s28, s25, -1
	s_cmp_eq_u32 s61, s26
	s_cselect_b32 s26, s65, s66
	s_cselect_b32 s29, s15, s28
	s_cselect_b32 s28, s17, s27
	s_cselect_b32 s27, s64, s67
	s_add_i32 m0, s46, 0xc000
	ds_read_b128 v[194:197], v177
	ds_read_b128 v[198:201], v177 offset:1024
	ds_read_b128 v[202:205], v177 offset:2048
	ds_read_b128 v[206:209], v177 offset:3072
	ds_read_b128 v[210:213], v177 offset:4096
	ds_read_b128 v[214:217], v177 offset:5120
	ds_read_b128 v[218:221], v177 offset:6144
	ds_read_b128 v[222:225], v177 offset:7168
	global_load_lds_dwordx4 v144, s[24:25]
	s_add_i32 m0, s46, 0xe000
	s_nop 0
	global_load_lds_dwordx4 v142, s[24:25]
	s_waitcnt vmcnt(8)
	s_waitcnt lgkmcnt(0)
	s_barrier
	s_setprio 1
	s_waitcnt lgkmcnt(0)
	v_mfma_i32_16x16x64_i8 v[126:129], v[150:153], v[194:197], v[126:129]
	v_mfma_i32_16x16x64_i8 v[122:125], v[158:161], v[194:197], v[122:125]
	v_mfma_i32_16x16x64_i8 v[118:121], v[150:153], v[202:205], v[118:121]
	v_mfma_i32_16x16x64_i8 v[114:117], v[158:161], v[202:205], v[114:117]
	v_mfma_i32_16x16x64_i8 v[106:109], v[150:153], v[210:213], v[106:109]
	v_mfma_i32_16x16x64_i8 v[98:101], v[158:161], v[210:213], v[98:101]
	v_mfma_i32_16x16x64_i8 v[90:93], v[150:153], v[218:221], v[90:93]
	v_mfma_i32_16x16x64_i8 v[82:85], v[158:161], v[218:221], v[82:85]
	v_mfma_i32_16x16x64_i8 v[126:129], v[154:157], v[198:201], v[126:129]
	v_mfma_i32_16x16x64_i8 v[122:125], v[162:165], v[198:201], v[122:125]
	v_mfma_i32_16x16x64_i8 v[118:121], v[154:157], v[206:209], v[118:121]
	v_mfma_i32_16x16x64_i8 v[114:117], v[162:165], v[206:209], v[114:117]
	v_mfma_i32_16x16x64_i8 v[106:109], v[154:157], v[214:217], v[106:109]
	v_mfma_i32_16x16x64_i8 v[98:101], v[162:165], v[214:217], v[98:101]
	v_mfma_i32_16x16x64_i8 v[90:93], v[154:157], v[222:225], v[90:93]
	v_mfma_i32_16x16x64_i8 v[82:85], v[162:165], v[222:225], v[82:85]
	s_setprio 0
	s_setprio 1
	v_mfma_i32_16x16x64_i8 v[110:113], v[178:181], v[194:197], v[110:113]
	v_mfma_i32_16x16x64_i8 v[102:105], v[186:189], v[194:197], v[102:105]
	v_mfma_i32_16x16x64_i8 v[94:97], v[178:181], v[202:205], v[94:97]
	v_mfma_i32_16x16x64_i8 v[86:89], v[186:189], v[202:205], v[86:89]
	v_mfma_i32_16x16x64_i8 v[78:81], v[178:181], v[210:213], v[78:81]
	v_mfma_i32_16x16x64_i8 v[74:77], v[186:189], v[210:213], v[74:77]
	v_mfma_i32_16x16x64_i8 v[70:73], v[178:181], v[218:221], v[70:73]
	v_mfma_i32_16x16x64_i8 v[66:69], v[186:189], v[218:221], v[66:69]
	v_mfma_i32_16x16x64_i8 v[110:113], v[182:185], v[198:201], v[110:113]
	v_mfma_i32_16x16x64_i8 v[102:105], v[190:193], v[198:201], v[102:105]
	v_mfma_i32_16x16x64_i8 v[94:97], v[182:185], v[206:209], v[94:97]
	v_mfma_i32_16x16x64_i8 v[86:89], v[190:193], v[206:209], v[86:89]
	v_mfma_i32_16x16x64_i8 v[78:81], v[182:185], v[214:217], v[78:81]
	v_mfma_i32_16x16x64_i8 v[74:77], v[190:193], v[214:217], v[74:77]
	v_mfma_i32_16x16x64_i8 v[70:73], v[182:185], v[222:225], v[70:73]
	v_mfma_i32_16x16x64_i8 v[66:69], v[190:193], v[222:225], v[66:69]
	s_setprio 0
	s_barrier
	s_mov_b32 m0, s23
	s_add_u32 s98, s26, 0x80
	s_addc_u32 s99, s27, 0
	s_add_u32 s70, s26, 0x40000
	ds_read_b128 v[194:197], v177 offset:16384
	ds_read_b128 v[198:201], v177 offset:17408
	ds_read_b128 v[202:205], v177 offset:18432
	ds_read_b128 v[206:209], v177 offset:19456
	ds_read_b128 v[210:213], v177 offset:20480
	ds_read_b128 v[214:217], v177 offset:21504
	ds_read_b128 v[218:221], v177 offset:22528
	ds_read_b128 v[222:225], v177 offset:23552
	global_load_lds_dwordx4 v132, s[26:27]
	s_mov_b32 m0, s43
	s_addc_u32 s71, s27, 0
	global_load_lds_dwordx4 v136, s[26:27]
	s_mov_b32 m0, s44
	s_nop 0
	global_load_lds_dwordx4 v132, s[70:71]
	s_mov_b32 m0, s45
	s_nop 0
	global_load_lds_dwordx4 v136, s[70:71]
	s_add_u32 s100, s28, 0x80
	s_addc_u32 s101, s29, 0
	s_mov_b32 m0, s46
	s_nop 0
	global_load_lds_dwordx4 v130, s[28:29]
	s_mov_b32 m0, s47
	s_nop 0
	global_load_lds_dwordx4 v134, s[28:29]
	s_waitcnt vmcnt(8)
	s_waitcnt lgkmcnt(0)
	s_barrier
	s_setprio 1
	s_waitcnt lgkmcnt(0)
	v_mfma_i32_16x16x64_i8 v[62:65], v[150:153], v[194:197], v[62:65]
	v_mfma_i32_16x16x64_i8 v[58:61], v[158:161], v[194:197], v[58:61]
	v_mfma_i32_16x16x64_i8 v[54:57], v[150:153], v[202:205], v[54:57]
	v_mfma_i32_16x16x64_i8 v[50:53], v[158:161], v[202:205], v[50:53]
	v_mfma_i32_16x16x64_i8 v[42:45], v[150:153], v[210:213], v[42:45]
	v_mfma_i32_16x16x64_i8 v[34:37], v[158:161], v[210:213], v[34:37]
	v_mfma_i32_16x16x64_i8 v[26:29], v[150:153], v[218:221], v[26:29]
	v_mfma_i32_16x16x64_i8 v[18:21], v[158:161], v[218:221], v[18:21]
	v_mfma_i32_16x16x64_i8 v[62:65], v[154:157], v[198:201], v[62:65]
	v_mfma_i32_16x16x64_i8 v[58:61], v[162:165], v[198:201], v[58:61]
	v_mfma_i32_16x16x64_i8 v[54:57], v[154:157], v[206:209], v[54:57]
	v_mfma_i32_16x16x64_i8 v[50:53], v[162:165], v[206:209], v[50:53]
	v_mfma_i32_16x16x64_i8 v[42:45], v[154:157], v[214:217], v[42:45]
	v_mfma_i32_16x16x64_i8 v[34:37], v[162:165], v[214:217], v[34:37]
	v_mfma_i32_16x16x64_i8 v[26:29], v[154:157], v[222:225], v[26:29]
	v_mfma_i32_16x16x64_i8 v[18:21], v[162:165], v[222:225], v[18:21]
	s_setprio 0
	s_setprio 1
	v_mfma_i32_16x16x64_i8 v[46:49], v[178:181], v[194:197], v[46:49]
	v_mfma_i32_16x16x64_i8 v[38:41], v[186:189], v[194:197], v[38:41]
	v_mfma_i32_16x16x64_i8 v[30:33], v[178:181], v[202:205], v[30:33]
	v_mfma_i32_16x16x64_i8 v[22:25], v[186:189], v[202:205], v[22:25]
	v_mfma_i32_16x16x64_i8 v[14:17], v[178:181], v[210:213], v[14:17]
	v_mfma_i32_16x16x64_i8 v[10:13], v[186:189], v[210:213], v[10:13]
	v_mfma_i32_16x16x64_i8 v[6:9], v[178:181], v[218:221], v[6:9]
	v_mfma_i32_16x16x64_i8 v[2:5], v[186:189], v[218:221], v[2:5]
	v_mfma_i32_16x16x64_i8 v[46:49], v[182:185], v[198:201], v[46:49]
	v_mfma_i32_16x16x64_i8 v[38:41], v[190:193], v[198:201], v[38:41]
	v_mfma_i32_16x16x64_i8 v[30:33], v[182:185], v[206:209], v[30:33]
	v_mfma_i32_16x16x64_i8 v[22:25], v[190:193], v[206:209], v[22:25]
	v_mfma_i32_16x16x64_i8 v[14:17], v[182:185], v[214:217], v[14:17]
	v_mfma_i32_16x16x64_i8 v[10:13], v[190:193], v[214:217], v[10:13]
	v_mfma_i32_16x16x64_i8 v[6:9], v[182:185], v[222:225], v[6:9]
	v_mfma_i32_16x16x64_i8 v[2:5], v[190:193], v[222:225], v[2:5]
	s_setprio 0
	s_barrier
; #define PG8_STAGE(bufoff, gbase, voff) do { _Pragma("unroll") for (int _i = 0; _i < 2; ++_i) \
;         __builtin_amdgcn_global_load_lds((const unsigned*)((const char*)(gbase) + (voff)[_i]), (PG8_LAS unsigned*)(lds + (bufoff) + ldsw + _i * 8192), 16, 0, 0); } while (0)
; #define PG8_LDA(dst, b, h) do { if constexpr (DT != 1) { _Pragma("unroll") for (int m = 0; m < 4; ++m) _Pragma("unroll") for (int k = 0; k < 2; ++k) dst[m][k] = *(const PG8_LAS bf16x8*)(lds + PG8_SA(b, h) + aoff + m * 2048 + k * 1024); } \
;         else { _Pragma("unroll") for (int m = 0; m < 4; ++m) dst##8[m] = ld32(lds + PG8_SA(b, h) + aoff + m * 2048); } } while (0)
; #define PG8_LDB(dst, b, h) do { if constexpr (DT != 1) { _Pragma("unroll") for (int n = 0; n < 2; ++n) _Pragma("unroll") for (int k = 0; k < 2; ++k) dst[n][k] = *(const PG8_LAS bf16x8*)(lds + PG8_SB(b, h) + boff + n * 2048 + k * 1024); } \
;         else { _Pragma("unroll") for (int n = 0; n < 2; ++n) dst##8[n] = ld32(lds + PG8_SB(b, h) + boff + n * 2048); } } while (0)
; #define PG8_WAIT_V(n) asm volatile("s_waitcnt vmcnt(" #n ")" ::: "memory")
; #define PG8_WAIT_L(n) asm volatile("s_waitcnt lgkmcnt(" #n ")" ::: "memory")
; #define PG8_BAR __builtin_amdgcn_s_barrier()
; #define PG8_SCHED __builtin_amdgcn_sched_barrier(0)
;     ...
;             PG8_LDB(B0, 1, 0); PG8_LDB(B1, 1, 1); PG8_SCHED; PG8_LDA(At, 1, 0); PG8_STAGE(PG8_SA(0, 1), a2 + hstepA, voffA);
;             PG8_WAIT_V(8); PG8_WAIT_L(0); PG8_BAR; PG8_MMA(0, 0, At, B0); PG8_MMA(0, 1, At, B1); PG8_BAR; PG8_SCHED;
;             PG8_LDA(At, 1, 1); PG8_STAGE(PG8_SB(1, 0), b3, voffB); PG8_STAGE(PG8_SB(1, 1), b3 + hstepB, voffB); PG8_STAGE(PG8_SA(1, 0), a3, voffA);
;             PG8_WAIT_V(8); PG8_WAIT_L(0); PG8_BAR; PG8_MMA(1, 0, At, B0); PG8_MMA(1, 1, At, B1); PG8_BAR; PG8_SCHED;
	v_add_u32_e32 v162, s51, v168
	v_add_u32_e32 v190, s52, v168
	ds_read_b128 v[150:153], v162
	ds_read_b128 v[154:157], v162 offset:1024
	ds_read_b128 v[158:161], v162 offset:2048
	ds_read_b128 v[162:165], v162 offset:3072
	ds_read_b128 v[178:181], v190
	ds_read_b128 v[182:185], v190 offset:1024
	ds_read_b128 v[186:189], v190 offset:2048
	ds_read_b128 v[190:193], v190 offset:3072
	s_add_u32 s28, s28, 0x40000
	s_addc_u32 s29, s29, 0
	s_mov_b32 m0, s48
	ds_read_b128 v[194:197], v177 offset:32768
	ds_read_b128 v[198:201], v177 offset:33792
	ds_read_b128 v[202:205], v177 offset:34816
	ds_read_b128 v[206:209], v177 offset:35840
	ds_read_b128 v[210:213], v177 offset:36864
	ds_read_b128 v[214:217], v177 offset:37888
	ds_read_b128 v[218:221], v177 offset:38912
	ds_read_b128 v[222:225], v177 offset:39936
	global_load_lds_dwordx4 v130, s[28:29]
	s_mov_b32 m0, s49
	s_nop 0
	global_load_lds_dwordx4 v134, s[28:29]
	s_waitcnt vmcnt(8)
	s_waitcnt lgkmcnt(0)
	s_barrier
	s_setprio 1
	s_waitcnt lgkmcnt(0)
	v_mfma_i32_16x16x64_i8 v[126:129], v[150:153], v[194:197], v[126:129]
	v_mfma_i32_16x16x64_i8 v[122:125], v[158:161], v[194:197], v[122:125]
	v_mfma_i32_16x16x64_i8 v[118:121], v[150:153], v[202:205], v[118:121]
	v_mfma_i32_16x16x64_i8 v[114:117], v[158:161], v[202:205], v[114:117]
	v_mfma_i32_16x16x64_i8 v[106:109], v[150:153], v[210:213], v[106:109]
	v_mfma_i32_16x16x64_i8 v[98:101], v[158:161], v[210:213], v[98:101]
	v_mfma_i32_16x16x64_i8 v[90:93], v[150:153], v[218:221], v[90:93]
	v_mfma_i32_16x16x64_i8 v[82:85], v[158:161], v[218:221], v[82:85]
	v_mfma_i32_16x16x64_i8 v[126:129], v[154:157], v[198:201], v[126:129]
	v_mfma_i32_16x16x64_i8 v[122:125], v[162:165], v[198:201], v[122:125]
	v_mfma_i32_16x16x64_i8 v[118:121], v[154:157], v[206:209], v[118:121]
	v_mfma_i32_16x16x64_i8 v[114:117], v[162:165], v[206:209], v[114:117]
	v_mfma_i32_16x16x64_i8 v[106:109], v[154:157], v[214:217], v[106:109]
	v_mfma_i32_16x16x64_i8 v[98:101], v[162:165], v[214:217], v[98:101]
	v_mfma_i32_16x16x64_i8 v[90:93], v[154:157], v[222:225], v[90:93]
	v_mfma_i32_16x16x64_i8 v[82:85], v[162:165], v[222:225], v[82:85]
	s_setprio 0
	s_setprio 1
	v_mfma_i32_16x16x64_i8 v[110:113], v[178:181], v[194:197], v[110:113]
	v_mfma_i32_16x16x64_i8 v[102:105], v[186:189], v[194:197], v[102:105]
	v_mfma_i32_16x16x64_i8 v[94:97], v[178:181], v[202:205], v[94:97]
	v_mfma_i32_16x16x64_i8 v[86:89], v[186:189], v[202:205], v[86:89]
	v_mfma_i32_16x16x64_i8 v[78:81], v[178:181], v[210:213], v[78:81]
	v_mfma_i32_16x16x64_i8 v[74:77], v[186:189], v[210:213], v[74:77]
	v_mfma_i32_16x16x64_i8 v[70:73], v[178:181], v[218:221], v[70:73]
	v_mfma_i32_16x16x64_i8 v[66:69], v[186:189], v[218:221], v[66:69]
	v_mfma_i32_16x16x64_i8 v[110:113], v[182:185], v[198:201], v[110:113]
	v_mfma_i32_16x16x64_i8 v[102:105], v[190:193], v[198:201], v[102:105]
	v_mfma_i32_16x16x64_i8 v[94:97], v[182:185], v[206:209], v[94:97]
	v_mfma_i32_16x16x64_i8 v[86:89], v[190:193], v[206:209], v[86:89]
	v_mfma_i32_16x16x64_i8 v[78:81], v[182:185], v[214:217], v[78:81]
	v_mfma_i32_16x16x64_i8 v[74:77], v[190:193], v[214:217], v[74:77]
	v_mfma_i32_16x16x64_i8 v[70:73], v[182:185], v[222:225], v[70:73]
	v_mfma_i32_16x16x64_i8 v[66:69], v[190:193], v[222:225], v[66:69]
	s_setprio 0
	s_barrier
	s_mov_b32 m0, s55
	s_add_u32 s26, s26, 0x40080
	ds_read_b128 v[194:197], v177 offset:49152
	ds_read_b128 v[198:201], v177 offset:50176
	ds_read_b128 v[202:205], v177 offset:51200
	ds_read_b128 v[206:209], v177 offset:52224
	ds_read_b128 v[210:213], v177 offset:53248
	ds_read_b128 v[214:217], v177 offset:54272
	ds_read_b128 v[218:221], v177 offset:55296
	ds_read_b128 v[222:225], v177 offset:56320
	global_load_lds_dwordx4 v132, s[98:99]
	s_mov_b32 m0, s56
	s_addc_u32 s27, s27, 0
	global_load_lds_dwordx4 v136, s[98:99]
	s_mov_b32 m0, s59
	s_nop 0
	global_load_lds_dwordx4 v132, s[26:27]
	s_mov_b32 m0, s60
	s_nop 0
	global_load_lds_dwordx4 v136, s[26:27]
	s_mov_b32 m0, s57
	s_nop 0
	global_load_lds_dwordx4 v130, s[100:101]
	s_mov_b32 m0, s58
	s_nop 0
	global_load_lds_dwordx4 v134, s[100:101]
	s_waitcnt vmcnt(8)
	s_waitcnt lgkmcnt(0)
	s_barrier
; #define PG8_WAIT_V(n) asm volatile("s_waitcnt vmcnt(" #n ")" ::: "memory")
; #define PG8_WAIT_L(n) asm volatile("s_waitcnt lgkmcnt(" #n ")" ::: "memory")
; #define PG8_BAR __builtin_amdgcn_s_barrier()
; #define PG8_SCHED __builtin_amdgcn_sched_barrier(0)
; __device__ __forceinline__ f32x4 i32bits_to_f32(f32x4 v) { return (f32x4){(float)__float_as_int(v.x), (float)__float_as_int(v.y), (float)__float_as_int(v.z), (float)__float_as_int(v.w)}; }
;     ...
;             PG8_WAIT_V(8); PG8_WAIT_L(0); PG8_BAR; PG8_MMA(1, 0, At, B0); PG8_MMA(1, 1, At, B1); PG8_BAR; PG8_SCHED;
	s_setprio 1
	s_waitcnt lgkmcnt(0)
	v_mfma_i32_16x16x64_i8 v[62:65], v[150:153], v[194:197], v[62:65]
	v_mfma_i32_16x16x64_i8 v[58:61], v[158:161], v[194:197], v[58:61]
	v_mfma_i32_16x16x64_i8 v[54:57], v[150:153], v[202:205], v[54:57]
	v_mfma_i32_16x16x64_i8 v[50:53], v[158:161], v[202:205], v[50:53]
	v_mfma_i32_16x16x64_i8 v[42:45], v[150:153], v[210:213], v[42:45]
	v_mfma_i32_16x16x64_i8 v[34:37], v[158:161], v[210:213], v[34:37]
	v_mfma_i32_16x16x64_i8 v[26:29], v[150:153], v[218:221], v[26:29]
	v_mfma_i32_16x16x64_i8 v[18:21], v[158:161], v[218:221], v[18:21]
	v_mfma_i32_16x16x64_i8 v[62:65], v[154:157], v[198:201], v[62:65]
	v_mfma_i32_16x16x64_i8 v[58:61], v[162:165], v[198:201], v[58:61]
	v_mfma_i32_16x16x64_i8 v[54:57], v[154:157], v[206:209], v[54:57]
	v_mfma_i32_16x16x64_i8 v[50:53], v[162:165], v[206:209], v[50:53]
	v_mfma_i32_16x16x64_i8 v[42:45], v[154:157], v[214:217], v[42:45]
	v_mfma_i32_16x16x64_i8 v[34:37], v[162:165], v[214:217], v[34:37]
	v_mfma_i32_16x16x64_i8 v[26:29], v[154:157], v[222:225], v[26:29]
	v_mfma_i32_16x16x64_i8 v[18:21], v[162:165], v[222:225], v[18:21]
	s_setprio 0
	s_setprio 1
	v_mfma_i32_16x16x64_i8 v[46:49], v[178:181], v[194:197], v[46:49]
	v_mfma_i32_16x16x64_i8 v[38:41], v[186:189], v[194:197], v[38:41]
	v_mfma_i32_16x16x64_i8 v[30:33], v[178:181], v[202:205], v[30:33]
	v_mfma_i32_16x16x64_i8 v[22:25], v[186:189], v[202:205], v[22:25]
	v_mfma_i32_16x16x64_i8 v[14:17], v[178:181], v[210:213], v[14:17]
	v_mfma_i32_16x16x64_i8 v[10:13], v[186:189], v[210:213], v[10:13]
	v_mfma_i32_16x16x64_i8 v[6:9], v[178:181], v[218:221], v[6:9]
	v_mfma_i32_16x16x64_i8 v[2:5], v[186:189], v[218:221], v[2:5]
	v_mfma_i32_16x16x64_i8 v[46:49], v[182:185], v[198:201], v[46:49]
	v_mfma_i32_16x16x64_i8 v[38:41], v[190:193], v[198:201], v[38:41]
	v_mfma_i32_16x16x64_i8 v[30:33], v[182:185], v[206:209], v[30:33]
	v_mfma_i32_16x16x64_i8 v[22:25], v[190:193], v[206:209], v[22:25]
	v_mfma_i32_16x16x64_i8 v[14:17], v[182:185], v[214:217], v[14:17]
	v_mfma_i32_16x16x64_i8 v[10:13], v[190:193], v[214:217], v[10:13]
	v_mfma_i32_16x16x64_i8 v[6:9], v[182:185], v[222:225], v[6:9]
	v_mfma_i32_16x16x64_i8 v[2:5], v[190:193], v[222:225], v[2:5]
	s_setprio 0
	s_barrier
	s_add_u32 s66, s66, 0x100
	s_addc_u32 s67, s67, 0
	s_add_u32 s24, s24, 0x100
	s_addc_u32 s25, s25, 0
	s_cmp_ge_i32 s68, s54
	s_mov_b32 s26, s68
	s_cbranch_scc0 .LBB0_1412
	v_cvt_f32_i32_e32 v150, v126
	v_cvt_f32_i32_e32 v151, v127
	v_cvt_f32_i32_e32 v126, v128
	v_cvt_f32_i32_e32 v127, v129
	v_cvt_f32_i32_e32 v122, v122
	v_cvt_f32_i32_e32 v123, v123
	v_cvt_f32_i32_e32 v124, v124
	v_cvt_f32_i32_e32 v125, v125
	v_cvt_f32_i32_e32 v158, v110
	v_cvt_f32_i32_e32 v159, v111
	v_cvt_f32_i32_e32 v160, v112
	v_cvt_f32_i32_e32 v161, v113
	v_cvt_f32_i32_e32 v162, v102
	v_cvt_f32_i32_e32 v163, v103
	v_cvt_f32_i32_e32 v164, v104
	v_cvt_f32_i32_e32 v165, v105
	v_cvt_f32_i32_e32 v152, v118
	v_cvt_f32_i32_e32 v153, v119
	v_cvt_f32_i32_e32 v154, v120
	v_cvt_f32_i32_e32 v155, v121
	v_cvt_f32_i32_e32 v128, v114
	v_cvt_f32_i32_e32 v129, v115
	v_cvt_f32_i32_e32 v156, v116
	v_cvt_f32_i32_e32 v157, v117
	v_cvt_f32_i32_e32 v116, v94
	v_cvt_f32_i32_e32 v117, v95
	v_cvt_f32_i32_e32 v120, v96
	v_cvt_f32_i32_e32 v121, v97
	v_cvt_f32_i32_e32 v114, v86
	v_cvt_f32_i32_e32 v115, v87
	v_cvt_f32_i32_e32 v118, v88
	v_cvt_f32_i32_e32 v119, v89
	v_cvt_f32_i32_e32 v102, v106
	v_cvt_f32_i32_e32 v103, v107
	v_cvt_f32_i32_e32 v104, v108
	v_cvt_f32_i32_e32 v105, v109
	v_cvt_f32_i32_e32 v98, v98
	v_cvt_f32_i32_e32 v99, v99
	v_cvt_f32_i32_e32 v100, v100
	v_cvt_f32_i32_e32 v101, v101
	v_cvt_f32_i32_e32 v108, v78
	v_cvt_f32_i32_e32 v109, v79
	v_cvt_f32_i32_e32 v112, v80
	v_cvt_f32_i32_e32 v113, v81
	v_cvt_f32_i32_e32 v106, v74
	v_cvt_f32_i32_e32 v107, v75
	v_cvt_f32_i32_e32 v110, v76
	v_cvt_f32_i32_e32 v111, v77
	v_cvt_f32_i32_e32 v76, v90
	v_cvt_f32_i32_e32 v77, v91
	v_cvt_f32_i32_e32 v80, v92
	v_cvt_f32_i32_e32 v81, v93
	v_cvt_f32_i32_e32 v74, v82
	v_cvt_f32_i32_e32 v75, v83
	v_cvt_f32_i32_e32 v78, v84
	v_cvt_f32_i32_e32 v79, v85
	v_cvt_f32_i32_e32 v92, v70
	v_cvt_f32_i32_e32 v93, v71
	v_cvt_f32_i32_e32 v96, v72
	v_cvt_f32_i32_e32 v97, v73
	v_cvt_f32_i32_e32 v90, v66
	v_cvt_f32_i32_e32 v91, v67
	v_cvt_f32_i32_e32 v94, v68
	v_cvt_f32_i32_e32 v95, v69
	v_cvt_f32_i32_e32 v68, v62
	v_cvt_f32_i32_e32 v69, v63
	v_cvt_f32_i32_e32 v72, v64
	v_cvt_f32_i32_e32 v73, v65
	v_cvt_f32_i32_e32 v66, v58
	v_cvt_f32_i32_e32 v67, v59
	v_cvt_f32_i32_e32 v70, v60
	v_cvt_f32_i32_e32 v71, v61
	v_cvt_f32_i32_e32 v84, v46
	v_cvt_f32_i32_e32 v85, v47
	v_cvt_f32_i32_e32 v88, v48
	v_cvt_f32_i32_e32 v89, v49
	v_cvt_f32_i32_e32 v82, v38
	v_cvt_f32_i32_e32 v83, v39
	v_cvt_f32_i32_e32 v86, v40
	v_cvt_f32_i32_e32 v87, v41
	v_cvt_f32_i32_e32 v54, v54
	v_cvt_f32_i32_e32 v55, v55
	v_cvt_f32_i32_e32 v56, v56
	v_cvt_f32_i32_e32 v57, v57
	v_cvt_f32_i32_e32 v50, v50
	v_cvt_f32_i32_e32 v51, v51
	v_cvt_f32_i32_e32 v52, v52
	v_cvt_f32_i32_e32 v53, v53
	v_cvt_f32_i32_e32 v60, v30
	v_cvt_f32_i32_e32 v61, v31
	v_cvt_f32_i32_e32 v64, v32
	v_cvt_f32_i32_e32 v65, v33
	v_cvt_f32_i32_e32 v58, v22
	v_cvt_f32_i32_e32 v59, v23
	v_cvt_f32_i32_e32 v62, v24
	v_cvt_f32_i32_e32 v63, v25
	v_cvt_f32_i32_e32 v38, v42
	v_cvt_f32_i32_e32 v39, v43
	v_cvt_f32_i32_e32 v40, v44
	v_cvt_f32_i32_e32 v41, v45
	v_cvt_f32_i32_e32 v34, v34
	v_cvt_f32_i32_e32 v35, v35
	v_cvt_f32_i32_e32 v36, v36
	v_cvt_f32_i32_e32 v37, v37
	v_cvt_f32_i32_e32 v44, v14
	v_cvt_f32_i32_e32 v45, v15
	v_cvt_f32_i32_e32 v48, v16
	v_cvt_f32_i32_e32 v49, v17
	v_cvt_f32_i32_e32 v42, v10
	v_cvt_f32_i32_e32 v43, v11
	v_cvt_f32_i32_e32 v46, v12
	v_cvt_f32_i32_e32 v47, v13
	v_cvt_f32_i32_e32 v22, v26
	v_cvt_f32_i32_e32 v23, v27
	v_cvt_f32_i32_e32 v24, v28
	v_cvt_f32_i32_e32 v25, v29
	v_cvt_f32_i32_e32 v18, v18
	v_cvt_f32_i32_e32 v19, v19
	v_cvt_f32_i32_e32 v20, v20
	v_cvt_f32_i32_e32 v21, v21
	v_cvt_f32_i32_e32 v28, v6
	v_cvt_f32_i32_e32 v29, v7
	v_cvt_f32_i32_e32 v32, v8
	v_cvt_f32_i32_e32 v33, v9
	v_cvt_f32_i32_e32 v26, v2
	v_cvt_f32_i32_e32 v27, v3
	v_cvt_f32_i32_e32 v30, v4
	v_cvt_f32_i32_e32 v31, v5

; #define PG8_STAGE(bufoff, gbase, voff) do { _Pragma("unroll") for (int _i = 0; _i < 2; ++_i) \
;         __builtin_amdgcn_global_load_lds((const unsigned*)((const char*)(gbase) + (voff)[_i]), (PG8_LAS unsigned*)(lds + (bufoff) + ldsw + _i * 8192), 16, 0, 0); } while (0)
; #define PG8_LDA(dst, b, h) do { if constexpr (DT != 1) { _Pragma("unroll") for (int m = 0; m < 4; ++m) _Pragma("unroll") for (int k = 0; k < 2; ++k) dst[m][k] = *(const PG8_LAS bf16x8*)(lds + PG8_SA(b, h) + aoff + m * 2048 + k * 1024); } \
;         else { _Pragma("unroll") for (int m = 0; m < 4; ++m) dst##8[m] = ld32(lds + PG8_SA(b, h) + aoff + m * 2048); } } while (0)
; #define PG8_LDB(dst, b, h) do { if constexpr (DT != 1) { _Pragma("unroll") for (int n = 0; n < 2; ++n) _Pragma("unroll") for (int k = 0; k < 2; ++k) dst[n][k] = *(const PG8_LAS bf16x8*)(lds + PG8_SB(b, h) + boff + n * 2048 + k * 1024); } \
;         else { _Pragma("unroll") for (int n = 0; n < 2; ++n) dst##8[n] = ld32(lds + PG8_SB(b, h) + boff + n * 2048); } } while (0)
; #define PG8_WAIT_V(n) asm volatile("s_waitcnt vmcnt(" #n ")" ::: "memory")
; #define PG8_WAIT_L(n) asm volatile("s_waitcnt lgkmcnt(" #n ")" ::: "memory")
; #define PG8_BAR __builtin_amdgcn_s_barrier()
; #define PG8_SCHED __builtin_amdgcn_sched_barrier(0)
;     ...
;             const char* a1 = cA + (size_t)(t + 1) * kstep;
;             const char* a2 = last ? nA : cA + (size_t)(t + 2) * kstep; const char* b2 = last ? nB : cB + (size_t)(t + 2) * kstep;
;             const char* a3 = a2 + kstep; const char* b3 = b2 + kstep;
;             if (last && has_next) S.a_ready(nxt);
;             if constexpr (SP2) {
;             PG8_LDB(B0, 0, 0); PG8_LDB(B1, 0, 1); PG8_SCHED; PG8_LDA(At, 0, 0); PG8_STAGE(PG8_SA(1, 1), a1 + hstepA, voffA);
;             PG8_WAIT_V(8); PG8_WAIT_L(0); PG8_BAR; PG8_MMA(0, 0, At, B0); PG8_MMA(0, 1, At, B1); PG8_BAR; PG8_SCHED;
;             PG8_LDA(At, 0, 1); PG8_STAGE(PG8_SB(0, 0), b2, voffB); PG8_STAGE(PG8_SB(0, 1), b2 + hstepB, voffB); PG8_STAGE(PG8_SA(0, 0), a2, voffA);
;             PG8_WAIT_V(8); PG8_WAIT_L(0); PG8_BAR; PG8_MMA(1, 0, At, B0); PG8_MMA(1, 1, At, B1); PG8_BAR; PG8_SCHED;
.LBB0_2262:
	ds_read_b128 v[154:157], v148
	ds_read_b128 v[158:161], v148 offset:1024
	ds_read_b128 v[162:165], v148 offset:2048
	ds_read_b128 v[166:169], v148 offset:3072
	ds_read_b128 v[170:173], v149
	ds_read_b128 v[174:177], v149 offset:1024
	ds_read_b128 v[178:181], v149 offset:2048
	ds_read_b128 v[182:185], v149 offset:3072
	s_add_i32 s65, s28, 2
	s_add_u32 s29, s26, 0xfff80080
	s_addc_u32 s30, s27, -1
	s_cmp_eq_u32 s61, s28
	s_cselect_b32 s28, s23, s25
	s_cselect_b32 s31, s2, s30
	s_cselect_b32 s30, s15, s29
	s_cselect_b32 s29, s17, s64
	s_add_i32 m0, s44, 0xc000
	ds_read_b128 v[186:189], v150
	ds_read_b128 v[190:193], v150 offset:1024
	ds_read_b128 v[194:197], v150 offset:2048
	ds_read_b128 v[198:201], v150 offset:3072
	ds_read_b128 v[202:205], v150 offset:4096
	ds_read_b128 v[206:209], v150 offset:5120
	ds_read_b128 v[210:213], v150 offset:6144
	ds_read_b128 v[214:217], v150 offset:7168
	global_load_lds_dwordx4 v142, s[26:27]
	s_add_i32 m0, s44, 0xe000
	s_nop 0
	global_load_lds_dwordx4 v140, s[26:27]
	s_waitcnt vmcnt(8)
	s_waitcnt lgkmcnt(0)
	s_barrier
	s_setprio 1
	s_waitcnt lgkmcnt(0)
	v_mfma_f32_16x16x32_bf16 v[126:129], v[154:157], v[186:189], v[126:129]
	v_mfma_f32_16x16x32_bf16 v[122:125], v[162:165], v[186:189], v[122:125]
	v_mfma_f32_16x16x32_bf16 v[110:113], v[154:157], v[194:197], v[110:113]
	v_mfma_f32_16x16x32_bf16 v[106:109], v[162:165], v[194:197], v[106:109]
	v_mfma_f32_16x16x32_bf16 v[94:97], v[154:157], v[202:205], v[94:97]
	v_mfma_f32_16x16x32_bf16 v[90:93], v[162:165], v[202:205], v[90:93]
	v_mfma_f32_16x16x32_bf16 v[78:81], v[154:157], v[210:213], v[78:81]
	v_mfma_f32_16x16x32_bf16 v[74:77], v[162:165], v[210:213], v[74:77]
	v_mfma_f32_16x16x32_bf16 v[126:129], v[158:161], v[190:193], v[126:129]
	v_mfma_f32_16x16x32_bf16 v[122:125], v[166:169], v[190:193], v[122:125]
	v_mfma_f32_16x16x32_bf16 v[110:113], v[158:161], v[198:201], v[110:113]
	v_mfma_f32_16x16x32_bf16 v[106:109], v[166:169], v[198:201], v[106:109]
	v_mfma_f32_16x16x32_bf16 v[94:97], v[158:161], v[206:209], v[94:97]
	v_mfma_f32_16x16x32_bf16 v[90:93], v[166:169], v[206:209], v[90:93]
	v_mfma_f32_16x16x32_bf16 v[78:81], v[158:161], v[214:217], v[78:81]
	v_mfma_f32_16x16x32_bf16 v[74:77], v[166:169], v[214:217], v[74:77]
	s_setprio 0
	s_setprio 1
	v_mfma_f32_16x16x32_bf16 v[118:121], v[170:173], v[186:189], v[118:121]
	v_mfma_f32_16x16x32_bf16 v[114:117], v[178:181], v[186:189], v[114:117]
	v_mfma_f32_16x16x32_bf16 v[102:105], v[170:173], v[194:197], v[102:105]
	v_mfma_f32_16x16x32_bf16 v[98:101], v[178:181], v[194:197], v[98:101]
	v_mfma_f32_16x16x32_bf16 v[86:89], v[170:173], v[202:205], v[86:89]
	v_mfma_f32_16x16x32_bf16 v[82:85], v[178:181], v[202:205], v[82:85]
	v_mfma_f32_16x16x32_bf16 v[70:73], v[170:173], v[210:213], v[70:73]
	v_mfma_f32_16x16x32_bf16 v[66:69], v[178:181], v[210:213], v[66:69]
	v_mfma_f32_16x16x32_bf16 v[118:121], v[174:177], v[190:193], v[118:121]
	v_mfma_f32_16x16x32_bf16 v[114:117], v[182:185], v[190:193], v[114:117]
	v_mfma_f32_16x16x32_bf16 v[102:105], v[174:177], v[198:201], v[102:105]
	v_mfma_f32_16x16x32_bf16 v[98:101], v[182:185], v[198:201], v[98:101]
	v_mfma_f32_16x16x32_bf16 v[86:89], v[174:177], v[206:209], v[86:89]
	v_mfma_f32_16x16x32_bf16 v[82:85], v[182:185], v[206:209], v[82:85]
	v_mfma_f32_16x16x32_bf16 v[70:73], v[174:177], v[214:217], v[70:73]
	v_mfma_f32_16x16x32_bf16 v[66:69], v[182:185], v[214:217], v[66:69]
	s_setprio 0
	s_barrier
	s_mov_b32 m0, s40
	s_add_u32 s98, s28, 0x80
	s_addc_u32 s99, s29, 0
	s_add_u32 s66, s28, 0x80000
	ds_read_b128 v[186:189], v150 offset:16384
	ds_read_b128 v[190:193], v150 offset:17408
	ds_read_b128 v[194:197], v150 offset:18432
	ds_read_b128 v[198:201], v150 offset:19456
	ds_read_b128 v[202:205], v150 offset:20480
	ds_read_b128 v[206:209], v150 offset:21504
	ds_read_b128 v[210:213], v150 offset:22528
	ds_read_b128 v[214:217], v150 offset:23552
	global_load_lds_dwordx4 v132, s[28:29]
	s_mov_b32 m0, s41
	s_addc_u32 s67, s29, 0
	global_load_lds_dwordx4 v136, s[28:29]
	s_mov_b32 m0, s42
	s_nop 0
	global_load_lds_dwordx4 v132, s[66:67]
	s_mov_b32 m0, s43
	s_nop 0
	global_load_lds_dwordx4 v136, s[66:67]
	s_add_u32 s100, s30, 0x80
	s_addc_u32 s101, s31, 0
	s_mov_b32 m0, s44
	s_nop 0
	global_load_lds_dwordx4 v130, s[30:31]
	s_mov_b32 m0, s45
	s_nop 0
	global_load_lds_dwordx4 v134, s[30:31]
	s_waitcnt vmcnt(8)
	s_waitcnt lgkmcnt(0)
	s_barrier
	s_setprio 1
	s_waitcnt lgkmcnt(0)
	v_mfma_f32_16x16x32_bf16 v[62:65], v[154:157], v[186:189], v[62:65]
	v_mfma_f32_16x16x32_bf16 v[58:61], v[162:165], v[186:189], v[58:61]
	v_mfma_f32_16x16x32_bf16 v[46:49], v[154:157], v[194:197], v[46:49]
	v_mfma_f32_16x16x32_bf16 v[42:45], v[162:165], v[194:197], v[42:45]
	v_mfma_f32_16x16x32_bf16 v[30:33], v[154:157], v[202:205], v[30:33]
	v_mfma_f32_16x16x32_bf16 v[26:29], v[162:165], v[202:205], v[26:29]
	v_mfma_f32_16x16x32_bf16 v[14:17], v[154:157], v[210:213], v[14:17]
	v_mfma_f32_16x16x32_bf16 v[10:13], v[162:165], v[210:213], v[10:13]
	v_mfma_f32_16x16x32_bf16 v[62:65], v[158:161], v[190:193], v[62:65]
	v_mfma_f32_16x16x32_bf16 v[58:61], v[166:169], v[190:193], v[58:61]
	v_mfma_f32_16x16x32_bf16 v[46:49], v[158:161], v[198:201], v[46:49]
	v_mfma_f32_16x16x32_bf16 v[42:45], v[166:169], v[198:201], v[42:45]
	v_mfma_f32_16x16x32_bf16 v[30:33], v[158:161], v[206:209], v[30:33]
	v_mfma_f32_16x16x32_bf16 v[26:29], v[166:169], v[206:209], v[26:29]
	v_mfma_f32_16x16x32_bf16 v[14:17], v[158:161], v[214:217], v[14:17]
	v_mfma_f32_16x16x32_bf16 v[10:13], v[166:169], v[214:217], v[10:13]
	s_setprio 0
	s_setprio 1
	v_mfma_f32_16x16x32_bf16 v[54:57], v[170:173], v[186:189], v[54:57]
	v_mfma_f32_16x16x32_bf16 v[50:53], v[178:181], v[186:189], v[50:53]
	v_mfma_f32_16x16x32_bf16 v[38:41], v[170:173], v[194:197], v[38:41]
	v_mfma_f32_16x16x32_bf16 v[34:37], v[178:181], v[194:197], v[34:37]
	v_mfma_f32_16x16x32_bf16 v[22:25], v[170:173], v[202:205], v[22:25]
	v_mfma_f32_16x16x32_bf16 v[18:21], v[178:181], v[202:205], v[18:21]
	v_mfma_f32_16x16x32_bf16 v[6:9], v[170:173], v[210:213], v[6:9]
	v_mfma_f32_16x16x32_bf16 v[2:5], v[178:181], v[210:213], v[2:5]
	v_mfma_f32_16x16x32_bf16 v[54:57], v[174:177], v[190:193], v[54:57]
	v_mfma_f32_16x16x32_bf16 v[50:53], v[182:185], v[190:193], v[50:53]
	v_mfma_f32_16x16x32_bf16 v[38:41], v[174:177], v[198:201], v[38:41]
	v_mfma_f32_16x16x32_bf16 v[34:37], v[182:185], v[198:201], v[34:37]
	v_mfma_f32_16x16x32_bf16 v[22:25], v[174:177], v[206:209], v[22:25]
	v_mfma_f32_16x16x32_bf16 v[18:21], v[182:185], v[206:209], v[18:21]
	v_mfma_f32_16x16x32_bf16 v[6:9], v[174:177], v[214:217], v[6:9]
	v_mfma_f32_16x16x32_bf16 v[2:5], v[182:185], v[214:217], v[2:5]
	s_setprio 0
	s_barrier
; #define PG8_STAGE(bufoff, gbase, voff) do { _Pragma("unroll") for (int _i = 0; _i < 2; ++_i) \
;         __builtin_amdgcn_global_load_lds((const unsigned*)((const char*)(gbase) + (voff)[_i]), (PG8_LAS unsigned*)(lds + (bufoff) + ldsw + _i * 8192), 16, 0, 0); } while (0)
; #define PG8_LDA(dst, b, h) do { if constexpr (DT != 1) { _Pragma("unroll") for (int m = 0; m < 4; ++m) _Pragma("unroll") for (int k = 0; k < 2; ++k) dst[m][k] = *(const PG8_LAS bf16x8*)(lds + PG8_SA(b, h) + aoff + m * 2048 + k * 1024); } \
;         else { _Pragma("unroll") for (int m = 0; m < 4; ++m) dst##8[m] = ld32(lds + PG8_SA(b, h) + aoff + m * 2048); } } while (0)
; #define PG8_LDB(dst, b, h) do { if constexpr (DT != 1) { _Pragma("unroll") for (int n = 0; n < 2; ++n) _Pragma("unroll") for (int k = 0; k < 2; ++k) dst[n][k] = *(const PG8_LAS bf16x8*)(lds + PG8_SB(b, h) + boff + n * 2048 + k * 1024); } \
;         else { _Pragma("unroll") for (int n = 0; n < 2; ++n) dst##8[n] = ld32(lds + PG8_SB(b, h) + boff + n * 2048); } } while (0)
; #define PG8_WAIT_V(n) asm volatile("s_waitcnt vmcnt(" #n ")" ::: "memory")
; #define PG8_WAIT_L(n) asm volatile("s_waitcnt lgkmcnt(" #n ")" ::: "memory")
; #define PG8_BAR __builtin_amdgcn_s_barrier()
; #define PG8_SCHED __builtin_amdgcn_sched_barrier(0)
;     ...
;             PG8_LDB(B0, 1, 0); PG8_LDB(B1, 1, 1); PG8_SCHED; PG8_LDA(At, 1, 0); PG8_STAGE(PG8_SA(0, 1), a2 + hstepA, voffA);
;             PG8_WAIT_V(8); PG8_WAIT_L(0); PG8_BAR; PG8_MMA(0, 0, At, B0); PG8_MMA(0, 1, At, B1); PG8_BAR; PG8_SCHED;
;             PG8_LDA(At, 1, 1); PG8_STAGE(PG8_SB(1, 0), b3, voffB); PG8_STAGE(PG8_SB(1, 1), b3 + hstepB, voffB); PG8_STAGE(PG8_SA(1, 0), a3, voffA);
;             PG8_WAIT_V(8); PG8_WAIT_L(0); PG8_BAR; PG8_MMA(1, 0, At, B0); PG8_MMA(1, 1, At, B1); PG8_BAR; PG8_SCHED;
	ds_read_b128 v[154:157], v151
	ds_read_b128 v[158:161], v151 offset:1024
	ds_read_b128 v[162:165], v151 offset:2048
	ds_read_b128 v[166:169], v151 offset:3072
	ds_read_b128 v[170:173], v152
	ds_read_b128 v[174:177], v152 offset:1024
	ds_read_b128 v[178:181], v152 offset:2048
	ds_read_b128 v[182:185], v152 offset:3072
	s_add_u32 s30, s30, 0x80000
	s_addc_u32 s31, s31, 0
	s_mov_b32 m0, s46
	ds_read_b128 v[186:189], v150 offset:32768
	ds_read_b128 v[190:193], v150 offset:33792
	ds_read_b128 v[194:197], v150 offset:34816
	ds_read_b128 v[198:201], v150 offset:35840
	ds_read_b128 v[202:205], v150 offset:36864
	ds_read_b128 v[206:209], v150 offset:37888
	ds_read_b128 v[210:213], v150 offset:38912
	ds_read_b128 v[214:217], v150 offset:39936
	global_load_lds_dwordx4 v130, s[30:31]
	s_mov_b32 m0, s47
	s_nop 0
	global_load_lds_dwordx4 v134, s[30:31]
	s_waitcnt vmcnt(8)
	s_waitcnt lgkmcnt(0)
	s_barrier
	s_setprio 1
	s_waitcnt lgkmcnt(0)
	v_mfma_f32_16x16x32_bf16 v[126:129], v[154:157], v[186:189], v[126:129]
	v_mfma_f32_16x16x32_bf16 v[122:125], v[162:165], v[186:189], v[122:125]
	v_mfma_f32_16x16x32_bf16 v[110:113], v[154:157], v[194:197], v[110:113]
	v_mfma_f32_16x16x32_bf16 v[106:109], v[162:165], v[194:197], v[106:109]
	v_mfma_f32_16x16x32_bf16 v[94:97], v[154:157], v[202:205], v[94:97]
	v_mfma_f32_16x16x32_bf16 v[90:93], v[162:165], v[202:205], v[90:93]
	v_mfma_f32_16x16x32_bf16 v[78:81], v[154:157], v[210:213], v[78:81]
	v_mfma_f32_16x16x32_bf16 v[74:77], v[162:165], v[210:213], v[74:77]
	v_mfma_f32_16x16x32_bf16 v[126:129], v[158:161], v[190:193], v[126:129]
	v_mfma_f32_16x16x32_bf16 v[122:125], v[166:169], v[190:193], v[122:125]
	v_mfma_f32_16x16x32_bf16 v[110:113], v[158:161], v[198:201], v[110:113]
	v_mfma_f32_16x16x32_bf16 v[106:109], v[166:169], v[198:201], v[106:109]
	v_mfma_f32_16x16x32_bf16 v[94:97], v[158:161], v[206:209], v[94:97]
	v_mfma_f32_16x16x32_bf16 v[90:93], v[166:169], v[206:209], v[90:93]
	v_mfma_f32_16x16x32_bf16 v[78:81], v[158:161], v[214:217], v[78:81]
	v_mfma_f32_16x16x32_bf16 v[74:77], v[166:169], v[214:217], v[74:77]
	s_setprio 0
	s_setprio 1
	v_mfma_f32_16x16x32_bf16 v[118:121], v[170:173], v[186:189], v[118:121]
	v_mfma_f32_16x16x32_bf16 v[114:117], v[178:181], v[186:189], v[114:117]
	v_mfma_f32_16x16x32_bf16 v[102:105], v[170:173], v[194:197], v[102:105]
	v_mfma_f32_16x16x32_bf16 v[98:101], v[178:181], v[194:197], v[98:101]
	v_mfma_f32_16x16x32_bf16 v[86:89], v[170:173], v[202:205], v[86:89]
	v_mfma_f32_16x16x32_bf16 v[82:85], v[178:181], v[202:205], v[82:85]
	v_mfma_f32_16x16x32_bf16 v[70:73], v[170:173], v[210:213], v[70:73]
	v_mfma_f32_16x16x32_bf16 v[66:69], v[178:181], v[210:213], v[66:69]
	v_mfma_f32_16x16x32_bf16 v[118:121], v[174:177], v[190:193], v[118:121]
	v_mfma_f32_16x16x32_bf16 v[114:117], v[182:185], v[190:193], v[114:117]
	v_mfma_f32_16x16x32_bf16 v[102:105], v[174:177], v[198:201], v[102:105]
	v_mfma_f32_16x16x32_bf16 v[98:101], v[182:185], v[198:201], v[98:101]
	v_mfma_f32_16x16x32_bf16 v[86:89], v[174:177], v[206:209], v[86:89]
	v_mfma_f32_16x16x32_bf16 v[82:85], v[182:185], v[206:209], v[82:85]
	v_mfma_f32_16x16x32_bf16 v[70:73], v[174:177], v[214:217], v[70:73]
	v_mfma_f32_16x16x32_bf16 v[66:69], v[182:185], v[214:217], v[66:69]
	s_setprio 0
	s_barrier
	s_mov_b32 m0, s53
	s_add_u32 s28, s28, 0x80080
	ds_read_b128 v[186:189], v150 offset:49152
	ds_read_b128 v[190:193], v150 offset:50176
	ds_read_b128 v[194:197], v150 offset:51200
	ds_read_b128 v[198:201], v150 offset:52224
	ds_read_b128 v[202:205], v150 offset:53248
	ds_read_b128 v[206:209], v150 offset:54272
	ds_read_b128 v[210:213], v150 offset:55296
	ds_read_b128 v[214:217], v150 offset:56320
	global_load_lds_dwordx4 v132, s[98:99]
	s_mov_b32 m0, s54
	s_addc_u32 s29, s29, 0
	global_load_lds_dwordx4 v136, s[98:99]
	s_mov_b32 m0, s57
	s_nop 0
	global_load_lds_dwordx4 v132, s[28:29]
	s_mov_b32 m0, s58
	s_nop 0
	global_load_lds_dwordx4 v136, s[28:29]
	s_mov_b32 m0, s55
	s_nop 0
	global_load_lds_dwordx4 v130, s[100:101]
	s_mov_b32 m0, s56
	s_nop 0
	global_load_lds_dwordx4 v134, s[100:101]
	s_waitcnt vmcnt(8)
	s_waitcnt lgkmcnt(0)
	s_barrier
	s_setprio 1
	s_waitcnt lgkmcnt(0)
	v_mfma_f32_16x16x32_bf16 v[62:65], v[154:157], v[186:189], v[62:65]
	v_mfma_f32_16x16x32_bf16 v[58:61], v[162:165], v[186:189], v[58:61]
	v_mfma_f32_16x16x32_bf16 v[46:49], v[154:157], v[194:197], v[46:49]
	v_mfma_f32_16x16x32_bf16 v[42:45], v[162:165], v[194:197], v[42:45]
	v_mfma_f32_16x16x32_bf16 v[30:33], v[154:157], v[202:205], v[30:33]
	v_mfma_f32_16x16x32_bf16 v[26:29], v[162:165], v[202:205], v[26:29]
	v_mfma_f32_16x16x32_bf16 v[14:17], v[154:157], v[210:213], v[14:17]
	v_mfma_f32_16x16x32_bf16 v[10:13], v[162:165], v[210:213], v[10:13]
	v_mfma_f32_16x16x32_bf16 v[62:65], v[158:161], v[190:193], v[62:65]
	v_mfma_f32_16x16x32_bf16 v[58:61], v[166:169], v[190:193], v[58:61]
	v_mfma_f32_16x16x32_bf16 v[46:49], v[158:161], v[198:201], v[46:49]
	v_mfma_f32_16x16x32_bf16 v[42:45], v[166:169], v[198:201], v[42:45]
	v_mfma_f32_16x16x32_bf16 v[30:33], v[158:161], v[206:209], v[30:33]
	v_mfma_f32_16x16x32_bf16 v[26:29], v[166:169], v[206:209], v[26:29]
	v_mfma_f32_16x16x32_bf16 v[14:17], v[158:161], v[214:217], v[14:17]
	v_mfma_f32_16x16x32_bf16 v[10:13], v[166:169], v[214:217], v[10:13]
	s_setprio 0
	s_setprio 1
	v_mfma_f32_16x16x32_bf16 v[54:57], v[170:173], v[186:189], v[54:57]
	v_mfma_f32_16x16x32_bf16 v[50:53], v[178:181], v[186:189], v[50:53]
	v_mfma_f32_16x16x32_bf16 v[38:41], v[170:173], v[194:197], v[38:41]
	v_mfma_f32_16x16x32_bf16 v[34:37], v[178:181], v[194:197], v[34:37]
	v_mfma_f32_16x16x32_bf16 v[22:25], v[170:173], v[202:205], v[22:25]
	v_mfma_f32_16x16x32_bf16 v[18:21], v[178:181], v[202:205], v[18:21]
	v_mfma_f32_16x16x32_bf16 v[6:9], v[170:173], v[210:213], v[6:9]
	v_mfma_f32_16x16x32_bf16 v[2:5], v[178:181], v[210:213], v[2:5]
	v_mfma_f32_16x16x32_bf16 v[54:57], v[174:177], v[190:193], v[54:57]
	v_mfma_f32_16x16x32_bf16 v[50:53], v[182:185], v[190:193], v[50:53]
	v_mfma_f32_16x16x32_bf16 v[38:41], v[174:177], v[198:201], v[38:41]
	v_mfma_f32_16x16x32_bf16 v[34:37], v[182:185], v[198:201], v[34:37]
	v_mfma_f32_16x16x32_bf16 v[22:25], v[174:177], v[206:209], v[22:25]
	v_mfma_f32_16x16x32_bf16 v[18:21], v[182:185], v[206:209], v[18:21]
	v_mfma_f32_16x16x32_bf16 v[6:9], v[174:177], v[214:217], v[6:9]
	v_mfma_f32_16x16x32_bf16 v[2:5], v[182:185], v[214:217], v[2:5]
	s_setprio 0
	s_barrier
	s_add_u32 s25, s25, 0x100
	s_addc_u32 s64, s64, 0
	s_add_u32 s26, s26, 0x100
	s_addc_u32 s27, s27, 0
	s_cmp_ge_i32 s65, s52
	s_mov_b32 s28, s65
	s_cbranch_scc0 .LBB0_2262

; #define PG8_STAGE(bufoff, gbase, voff) do { _Pragma("unroll") for (int _i = 0; _i < 2; ++_i) \
;         __builtin_amdgcn_global_load_lds((const unsigned*)((const char*)(gbase) + (voff)[_i]), (PG8_LAS unsigned*)(lds + (bufoff) + ldsw + _i * 8192), 16, 0, 0); } while (0)
; #define PG8_LDA(dst, b, h) do { if constexpr (DT != 1) { _Pragma("unroll") for (int m = 0; m < 4; ++m) _Pragma("unroll") for (int k = 0; k < 2; ++k) dst[m][k] = *(const PG8_LAS bf16x8*)(lds + PG8_SA(b, h) + aoff + m * 2048 + k * 1024); } \
;         else { _Pragma("unroll") for (int m = 0; m < 4; ++m) dst##8[m] = ld32(lds + PG8_SA(b, h) + aoff + m * 2048); } } while (0)
; #define PG8_LDB(dst, b, h) do { if constexpr (DT != 1) { _Pragma("unroll") for (int n = 0; n < 2; ++n) _Pragma("unroll") for (int k = 0; k < 2; ++k) dst[n][k] = *(const PG8_LAS bf16x8*)(lds + PG8_SB(b, h) + boff + n * 2048 + k * 1024); } \
;         else { _Pragma("unroll") for (int n = 0; n < 2; ++n) dst##8[n] = ld32(lds + PG8_SB(b, h) + boff + n * 2048); } } while (0)
; #define PG8_WAIT_V(n) asm volatile("s_waitcnt vmcnt(" #n ")" ::: "memory")
; #define PG8_WAIT_L(n) asm volatile("s_waitcnt lgkmcnt(" #n ")" ::: "memory")
; #define PG8_BAR __builtin_amdgcn_s_barrier()
; #define PG8_SCHED __builtin_amdgcn_sched_barrier(0)
;     ...
;             const char* a1 = cA + (size_t)(t + 1) * kstep;
;             const char* a2 = last ? nA : cA + (size_t)(t + 2) * kstep; const char* b2 = last ? nB : cB + (size_t)(t + 2) * kstep;
;             const char* a3 = a2 + kstep; const char* b3 = b2 + kstep;
;             if (last && has_next) S.a_ready(nxt);
;             if constexpr (SP2) {
;             PG8_LDB(B0, 0, 0); PG8_LDB(B1, 0, 1); PG8_SCHED; PG8_LDA(At, 0, 0); PG8_STAGE(PG8_SA(1, 1), a1 + hstepA, voffA);
;             PG8_WAIT_V(8); PG8_WAIT_L(0); PG8_BAR; PG8_MMA(0, 0, At, B0); PG8_MMA(0, 1, At, B1); PG8_BAR; PG8_SCHED;
;             PG8_LDA(At, 0, 1); PG8_STAGE(PG8_SB(0, 0), b2, voffB); PG8_STAGE(PG8_SB(0, 1), b2 + hstepB, voffB); PG8_STAGE(PG8_SA(0, 0), a2, voffA);
;             PG8_WAIT_V(8); PG8_WAIT_L(0); PG8_BAR; PG8_MMA(1, 0, At, B0); PG8_MMA(1, 1, At, B1); PG8_BAR; PG8_SCHED;
.LBB0_3356:
	ds_read_b128 v[130:133], v173
	ds_read_b128 v[134:137], v173 offset:1024
	ds_read_b128 v[138:141], v173 offset:2048
	ds_read_b128 v[142:145], v173 offset:3072
	ds_read_b128 v[164:167], v174
	ds_read_b128 v[168:171], v174 offset:1024
	ds_read_b128 v[178:181], v174 offset:2048
	ds_read_b128 v[182:185], v174 offset:3072
	s_add_i32 s78, s42, 2
	s_add_u32 s43, s40, 0xffff0080
	s_addc_u32 s44, s41, -1
	s_cmp_eq_u32 s74, s42
	s_cselect_b32 s42, s39, s76
	s_cselect_b32 s45, s3, s44
	s_cselect_b32 s44, s29, s43
	s_cselect_b32 s43, s31, s77
	s_add_i32 m0, s56, 0xc000
	ds_read_b128 v[186:189], v175
	ds_read_b128 v[190:193], v175 offset:1024
	ds_read_b128 v[194:197], v175 offset:2048
	ds_read_b128 v[198:201], v175 offset:3072
	ds_read_b128 v[202:205], v175 offset:4096
	ds_read_b128 v[206:209], v175 offset:5120
	ds_read_b128 v[210:213], v175 offset:6144
	ds_read_b128 v[214:217], v175 offset:7168
	global_load_lds_dwordx4 v158, s[40:41]
	s_add_i32 m0, s56, 0xe000
	s_nop 0
	global_load_lds_dwordx4 v156, s[40:41]
	s_waitcnt vmcnt(8)
	s_waitcnt lgkmcnt(0)
	s_barrier
	s_setprio 1
	s_waitcnt lgkmcnt(0)
	v_mfma_f32_16x16x32_bf16 v[126:129], v[130:133], v[186:189], v[126:129]
	v_mfma_f32_16x16x32_bf16 v[122:125], v[138:141], v[186:189], v[122:125]
	v_mfma_f32_16x16x32_bf16 v[110:113], v[130:133], v[194:197], v[110:113]
	v_mfma_f32_16x16x32_bf16 v[106:109], v[138:141], v[194:197], v[106:109]
	v_mfma_f32_16x16x32_bf16 v[94:97], v[130:133], v[202:205], v[94:97]
	v_mfma_f32_16x16x32_bf16 v[90:93], v[138:141], v[202:205], v[90:93]
	v_mfma_f32_16x16x32_bf16 v[78:81], v[130:133], v[210:213], v[78:81]
	v_mfma_f32_16x16x32_bf16 v[74:77], v[138:141], v[210:213], v[74:77]
	v_mfma_f32_16x16x32_bf16 v[126:129], v[134:137], v[190:193], v[126:129]
	v_mfma_f32_16x16x32_bf16 v[122:125], v[142:145], v[190:193], v[122:125]
	v_mfma_f32_16x16x32_bf16 v[110:113], v[134:137], v[198:201], v[110:113]
	v_mfma_f32_16x16x32_bf16 v[106:109], v[142:145], v[198:201], v[106:109]
	v_mfma_f32_16x16x32_bf16 v[94:97], v[134:137], v[206:209], v[94:97]
	v_mfma_f32_16x16x32_bf16 v[90:93], v[142:145], v[206:209], v[90:93]
	v_mfma_f32_16x16x32_bf16 v[78:81], v[134:137], v[214:217], v[78:81]
	v_mfma_f32_16x16x32_bf16 v[74:77], v[142:145], v[214:217], v[74:77]
	s_setprio 0
	s_setprio 1
	v_mfma_f32_16x16x32_bf16 v[118:121], v[164:167], v[186:189], v[118:121]
	v_mfma_f32_16x16x32_bf16 v[114:117], v[178:181], v[186:189], v[114:117]
	v_mfma_f32_16x16x32_bf16 v[102:105], v[164:167], v[194:197], v[102:105]
	v_mfma_f32_16x16x32_bf16 v[98:101], v[178:181], v[194:197], v[98:101]
	v_mfma_f32_16x16x32_bf16 v[86:89], v[164:167], v[202:205], v[86:89]
	v_mfma_f32_16x16x32_bf16 v[82:85], v[178:181], v[202:205], v[82:85]
	v_mfma_f32_16x16x32_bf16 v[70:73], v[164:167], v[210:213], v[70:73]
	v_mfma_f32_16x16x32_bf16 v[66:69], v[178:181], v[210:213], v[66:69]
	v_mfma_f32_16x16x32_bf16 v[118:121], v[168:171], v[190:193], v[118:121]
	v_mfma_f32_16x16x32_bf16 v[114:117], v[182:185], v[190:193], v[114:117]
	v_mfma_f32_16x16x32_bf16 v[102:105], v[168:171], v[198:201], v[102:105]
	v_mfma_f32_16x16x32_bf16 v[98:101], v[182:185], v[198:201], v[98:101]
	v_mfma_f32_16x16x32_bf16 v[86:89], v[168:171], v[206:209], v[86:89]
	v_mfma_f32_16x16x32_bf16 v[82:85], v[182:185], v[206:209], v[82:85]
	v_mfma_f32_16x16x32_bf16 v[70:73], v[168:171], v[214:217], v[70:73]
	v_mfma_f32_16x16x32_bf16 v[66:69], v[182:185], v[214:217], v[66:69]
	s_setprio 0
	s_barrier
	s_mov_b32 m0, s52
	s_add_u32 s98, s42, 0x80
	s_addc_u32 s99, s43, 0
	s_add_u32 s80, s42, 0x10000
	ds_read_b128 v[186:189], v175 offset:16384
	ds_read_b128 v[190:193], v175 offset:17408
	ds_read_b128 v[194:197], v175 offset:18432
	ds_read_b128 v[198:201], v175 offset:19456
	ds_read_b128 v[202:205], v175 offset:20480
	ds_read_b128 v[206:209], v175 offset:21504
	ds_read_b128 v[210:213], v175 offset:22528
	ds_read_b128 v[214:217], v175 offset:23552
	global_load_lds_dwordx4 v148, s[42:43]
	s_mov_b32 m0, s53
	s_addc_u32 s81, s43, 0
	global_load_lds_dwordx4 v152, s[42:43]
	s_mov_b32 m0, s54
	s_nop 0
	global_load_lds_dwordx4 v148, s[80:81]
	s_mov_b32 m0, s55
	s_nop 0
	global_load_lds_dwordx4 v152, s[80:81]
	s_add_u32 s100, s44, 0x80
	s_addc_u32 s101, s45, 0
	s_mov_b32 m0, s56
	s_nop 0
	global_load_lds_dwordx4 v146, s[44:45]
	s_mov_b32 m0, s57
	s_nop 0
	global_load_lds_dwordx4 v150, s[44:45]
	s_waitcnt vmcnt(8)
	s_waitcnt lgkmcnt(0)
	s_barrier
	s_setprio 1
	s_waitcnt lgkmcnt(0)
	v_mfma_f32_16x16x32_bf16 v[62:65], v[130:133], v[186:189], v[62:65]
	v_mfma_f32_16x16x32_bf16 v[58:61], v[138:141], v[186:189], v[58:61]
	v_mfma_f32_16x16x32_bf16 v[46:49], v[130:133], v[194:197], v[46:49]
	v_mfma_f32_16x16x32_bf16 v[42:45], v[138:141], v[194:197], v[42:45]
	v_mfma_f32_16x16x32_bf16 v[30:33], v[130:133], v[202:205], v[30:33]
	v_mfma_f32_16x16x32_bf16 v[26:29], v[138:141], v[202:205], v[26:29]
	v_mfma_f32_16x16x32_bf16 v[14:17], v[130:133], v[210:213], v[14:17]
	v_mfma_f32_16x16x32_bf16 v[10:13], v[138:141], v[210:213], v[10:13]
	v_mfma_f32_16x16x32_bf16 v[62:65], v[134:137], v[190:193], v[62:65]
	v_mfma_f32_16x16x32_bf16 v[58:61], v[142:145], v[190:193], v[58:61]
	v_mfma_f32_16x16x32_bf16 v[46:49], v[134:137], v[198:201], v[46:49]
	v_mfma_f32_16x16x32_bf16 v[42:45], v[142:145], v[198:201], v[42:45]
	v_mfma_f32_16x16x32_bf16 v[30:33], v[134:137], v[206:209], v[30:33]
	v_mfma_f32_16x16x32_bf16 v[26:29], v[142:145], v[206:209], v[26:29]
	v_mfma_f32_16x16x32_bf16 v[14:17], v[134:137], v[214:217], v[14:17]
	v_mfma_f32_16x16x32_bf16 v[10:13], v[142:145], v[214:217], v[10:13]
	s_setprio 0
	s_setprio 1
	v_mfma_f32_16x16x32_bf16 v[54:57], v[164:167], v[186:189], v[54:57]
	v_mfma_f32_16x16x32_bf16 v[50:53], v[178:181], v[186:189], v[50:53]
	v_mfma_f32_16x16x32_bf16 v[38:41], v[164:167], v[194:197], v[38:41]
	v_mfma_f32_16x16x32_bf16 v[34:37], v[178:181], v[194:197], v[34:37]
	v_mfma_f32_16x16x32_bf16 v[22:25], v[164:167], v[202:205], v[22:25]
	v_mfma_f32_16x16x32_bf16 v[18:21], v[178:181], v[202:205], v[18:21]
	v_mfma_f32_16x16x32_bf16 v[6:9], v[164:167], v[210:213], v[6:9]
	v_mfma_f32_16x16x32_bf16 v[2:5], v[178:181], v[210:213], v[2:5]
	v_mfma_f32_16x16x32_bf16 v[54:57], v[168:171], v[190:193], v[54:57]
	v_mfma_f32_16x16x32_bf16 v[50:53], v[182:185], v[190:193], v[50:53]
	v_mfma_f32_16x16x32_bf16 v[38:41], v[168:171], v[198:201], v[38:41]
	v_mfma_f32_16x16x32_bf16 v[34:37], v[182:185], v[198:201], v[34:37]
	v_mfma_f32_16x16x32_bf16 v[22:25], v[168:171], v[206:209], v[22:25]
	v_mfma_f32_16x16x32_bf16 v[18:21], v[182:185], v[206:209], v[18:21]
	v_mfma_f32_16x16x32_bf16 v[6:9], v[168:171], v[214:217], v[6:9]
	v_mfma_f32_16x16x32_bf16 v[2:5], v[182:185], v[214:217], v[2:5]
	s_setprio 0
	s_barrier
; #define PG8_STAGE(bufoff, gbase, voff) do { _Pragma("unroll") for (int _i = 0; _i < 2; ++_i) \
;         __builtin_amdgcn_global_load_lds((const unsigned*)((const char*)(gbase) + (voff)[_i]), (PG8_LAS unsigned*)(lds + (bufoff) + ldsw + _i * 8192), 16, 0, 0); } while (0)
; #define PG8_LDA(dst, b, h) do { if constexpr (DT != 1) { _Pragma("unroll") for (int m = 0; m < 4; ++m) _Pragma("unroll") for (int k = 0; k < 2; ++k) dst[m][k] = *(const PG8_LAS bf16x8*)(lds + PG8_SA(b, h) + aoff + m * 2048 + k * 1024); } \
;         else { _Pragma("unroll") for (int m = 0; m < 4; ++m) dst##8[m] = ld32(lds + PG8_SA(b, h) + aoff + m * 2048); } } while (0)
; #define PG8_LDB(dst, b, h) do { if constexpr (DT != 1) { _Pragma("unroll") for (int n = 0; n < 2; ++n) _Pragma("unroll") for (int k = 0; k < 2; ++k) dst[n][k] = *(const PG8_LAS bf16x8*)(lds + PG8_SB(b, h) + boff + n * 2048 + k * 1024); } \
;         else { _Pragma("unroll") for (int n = 0; n < 2; ++n) dst##8[n] = ld32(lds + PG8_SB(b, h) + boff + n * 2048); } } while (0)
; #define PG8_WAIT_V(n) asm volatile("s_waitcnt vmcnt(" #n ")" ::: "memory")
; #define PG8_WAIT_L(n) asm volatile("s_waitcnt lgkmcnt(" #n ")" ::: "memory")
; #define PG8_BAR __builtin_amdgcn_s_barrier()
; #define PG8_SCHED __builtin_amdgcn_sched_barrier(0)
;     ...
;             PG8_LDB(B0, 1, 0); PG8_LDB(B1, 1, 1); PG8_SCHED; PG8_LDA(At, 1, 0); PG8_STAGE(PG8_SA(0, 1), a2 + hstepA, voffA);
;             PG8_WAIT_V(8); PG8_WAIT_L(0); PG8_BAR; PG8_MMA(0, 0, At, B0); PG8_MMA(0, 1, At, B1); PG8_BAR; PG8_SCHED;
;             PG8_LDA(At, 1, 1); PG8_STAGE(PG8_SB(1, 0), b3, voffB); PG8_STAGE(PG8_SB(1, 1), b3 + hstepB, voffB); PG8_STAGE(PG8_SA(1, 0), a3, voffA);
;             PG8_WAIT_V(8); PG8_WAIT_L(0); PG8_BAR; PG8_MMA(1, 0, At, B0); PG8_MMA(1, 1, At, B1); PG8_BAR; PG8_SCHED;
	ds_read_b128 v[130:133], v176
	ds_read_b128 v[134:137], v176 offset:1024
	ds_read_b128 v[138:141], v176 offset:2048
	ds_read_b128 v[142:145], v176 offset:3072
	ds_read_b128 v[164:167], v177
	ds_read_b128 v[168:171], v177 offset:1024
	ds_read_b128 v[178:181], v177 offset:2048
	ds_read_b128 v[182:185], v177 offset:3072
	s_add_u32 s44, s44, 0x10000
	s_addc_u32 s45, s45, 0
	s_mov_b32 m0, s58
	ds_read_b128 v[186:189], v175 offset:32768
	ds_read_b128 v[190:193], v175 offset:33792
	ds_read_b128 v[194:197], v175 offset:34816
	ds_read_b128 v[198:201], v175 offset:35840
	ds_read_b128 v[202:205], v175 offset:36864
	ds_read_b128 v[206:209], v175 offset:37888
	ds_read_b128 v[210:213], v175 offset:38912
	ds_read_b128 v[214:217], v175 offset:39936
	global_load_lds_dwordx4 v146, s[44:45]
	s_mov_b32 m0, s59
	s_nop 0
	global_load_lds_dwordx4 v150, s[44:45]
	s_waitcnt vmcnt(8)
	s_waitcnt lgkmcnt(0)
	s_barrier
	s_setprio 1
	s_waitcnt lgkmcnt(0)
	v_mfma_f32_16x16x32_bf16 v[126:129], v[130:133], v[186:189], v[126:129]
	v_mfma_f32_16x16x32_bf16 v[122:125], v[138:141], v[186:189], v[122:125]
	v_mfma_f32_16x16x32_bf16 v[110:113], v[130:133], v[194:197], v[110:113]
	v_mfma_f32_16x16x32_bf16 v[106:109], v[138:141], v[194:197], v[106:109]
	v_mfma_f32_16x16x32_bf16 v[94:97], v[130:133], v[202:205], v[94:97]
	v_mfma_f32_16x16x32_bf16 v[90:93], v[138:141], v[202:205], v[90:93]
	v_mfma_f32_16x16x32_bf16 v[78:81], v[130:133], v[210:213], v[78:81]
	v_mfma_f32_16x16x32_bf16 v[74:77], v[138:141], v[210:213], v[74:77]
	v_mfma_f32_16x16x32_bf16 v[126:129], v[134:137], v[190:193], v[126:129]
	v_mfma_f32_16x16x32_bf16 v[122:125], v[142:145], v[190:193], v[122:125]
	v_mfma_f32_16x16x32_bf16 v[110:113], v[134:137], v[198:201], v[110:113]
	v_mfma_f32_16x16x32_bf16 v[106:109], v[142:145], v[198:201], v[106:109]
	v_mfma_f32_16x16x32_bf16 v[94:97], v[134:137], v[206:209], v[94:97]
	v_mfma_f32_16x16x32_bf16 v[90:93], v[142:145], v[206:209], v[90:93]
	v_mfma_f32_16x16x32_bf16 v[78:81], v[134:137], v[214:217], v[78:81]
	v_mfma_f32_16x16x32_bf16 v[74:77], v[142:145], v[214:217], v[74:77]
	s_setprio 0
	s_setprio 1
	v_mfma_f32_16x16x32_bf16 v[118:121], v[164:167], v[186:189], v[118:121]
	v_mfma_f32_16x16x32_bf16 v[114:117], v[178:181], v[186:189], v[114:117]
	v_mfma_f32_16x16x32_bf16 v[102:105], v[164:167], v[194:197], v[102:105]
	v_mfma_f32_16x16x32_bf16 v[98:101], v[178:181], v[194:197], v[98:101]
	v_mfma_f32_16x16x32_bf16 v[86:89], v[164:167], v[202:205], v[86:89]
	v_mfma_f32_16x16x32_bf16 v[82:85], v[178:181], v[202:205], v[82:85]
	v_mfma_f32_16x16x32_bf16 v[70:73], v[164:167], v[210:213], v[70:73]
	v_mfma_f32_16x16x32_bf16 v[66:69], v[178:181], v[210:213], v[66:69]
	v_mfma_f32_16x16x32_bf16 v[118:121], v[168:171], v[190:193], v[118:121]
	v_mfma_f32_16x16x32_bf16 v[114:117], v[182:185], v[190:193], v[114:117]
	v_mfma_f32_16x16x32_bf16 v[102:105], v[168:171], v[198:201], v[102:105]
	v_mfma_f32_16x16x32_bf16 v[98:101], v[182:185], v[198:201], v[98:101]
	v_mfma_f32_16x16x32_bf16 v[86:89], v[168:171], v[206:209], v[86:89]
	v_mfma_f32_16x16x32_bf16 v[82:85], v[182:185], v[206:209], v[82:85]
	v_mfma_f32_16x16x32_bf16 v[70:73], v[168:171], v[214:217], v[70:73]
	v_mfma_f32_16x16x32_bf16 v[66:69], v[182:185], v[214:217], v[66:69]
	s_setprio 0
	s_barrier
	s_mov_b32 m0, s66
	s_add_u32 s42, s42, 0x10080
	ds_read_b128 v[186:189], v175 offset:49152
	ds_read_b128 v[190:193], v175 offset:50176
	ds_read_b128 v[194:197], v175 offset:51200
	ds_read_b128 v[198:201], v175 offset:52224
	ds_read_b128 v[202:205], v175 offset:53248
	ds_read_b128 v[206:209], v175 offset:54272
	ds_read_b128 v[210:213], v175 offset:55296
	ds_read_b128 v[214:217], v175 offset:56320
	global_load_lds_dwordx4 v148, s[98:99]
	s_mov_b32 m0, s67
	s_addc_u32 s43, s43, 0
	global_load_lds_dwordx4 v152, s[98:99]
	s_mov_b32 m0, s70
	s_nop 0
	global_load_lds_dwordx4 v148, s[42:43]
	s_mov_b32 m0, s71
	s_nop 0
	global_load_lds_dwordx4 v152, s[42:43]
	s_mov_b32 m0, s68
	s_nop 0
	global_load_lds_dwordx4 v146, s[100:101]
	s_mov_b32 m0, s69
	s_nop 0
	global_load_lds_dwordx4 v150, s[100:101]
	s_waitcnt vmcnt(8)
	s_waitcnt lgkmcnt(0)
	s_barrier
	s_setprio 1
	s_waitcnt lgkmcnt(0)
	v_mfma_f32_16x16x32_bf16 v[62:65], v[130:133], v[186:189], v[62:65]
	v_mfma_f32_16x16x32_bf16 v[58:61], v[138:141], v[186:189], v[58:61]
	v_mfma_f32_16x16x32_bf16 v[46:49], v[130:133], v[194:197], v[46:49]
	v_mfma_f32_16x16x32_bf16 v[42:45], v[138:141], v[194:197], v[42:45]
	v_mfma_f32_16x16x32_bf16 v[30:33], v[130:133], v[202:205], v[30:33]
	v_mfma_f32_16x16x32_bf16 v[26:29], v[138:141], v[202:205], v[26:29]
	v_mfma_f32_16x16x32_bf16 v[14:17], v[130:133], v[210:213], v[14:17]
	v_mfma_f32_16x16x32_bf16 v[10:13], v[138:141], v[210:213], v[10:13]
	v_mfma_f32_16x16x32_bf16 v[62:65], v[134:137], v[190:193], v[62:65]
	v_mfma_f32_16x16x32_bf16 v[58:61], v[142:145], v[190:193], v[58:61]
	v_mfma_f32_16x16x32_bf16 v[46:49], v[134:137], v[198:201], v[46:49]
	v_mfma_f32_16x16x32_bf16 v[42:45], v[142:145], v[198:201], v[42:45]
	v_mfma_f32_16x16x32_bf16 v[30:33], v[134:137], v[206:209], v[30:33]
	v_mfma_f32_16x16x32_bf16 v[26:29], v[142:145], v[206:209], v[26:29]
	v_mfma_f32_16x16x32_bf16 v[14:17], v[134:137], v[214:217], v[14:17]
	v_mfma_f32_16x16x32_bf16 v[10:13], v[142:145], v[214:217], v[10:13]
	s_setprio 0
	s_setprio 1
	v_mfma_f32_16x16x32_bf16 v[54:57], v[164:167], v[186:189], v[54:57]
	v_mfma_f32_16x16x32_bf16 v[50:53], v[178:181], v[186:189], v[50:53]
	v_mfma_f32_16x16x32_bf16 v[38:41], v[164:167], v[194:197], v[38:41]
	v_mfma_f32_16x16x32_bf16 v[34:37], v[178:181], v[194:197], v[34:37]
	v_mfma_f32_16x16x32_bf16 v[22:25], v[164:167], v[202:205], v[22:25]
	v_mfma_f32_16x16x32_bf16 v[18:21], v[178:181], v[202:205], v[18:21]
	v_mfma_f32_16x16x32_bf16 v[6:9], v[164:167], v[210:213], v[6:9]
	v_mfma_f32_16x16x32_bf16 v[2:5], v[178:181], v[210:213], v[2:5]
	v_mfma_f32_16x16x32_bf16 v[54:57], v[168:171], v[190:193], v[54:57]
	v_mfma_f32_16x16x32_bf16 v[50:53], v[182:185], v[190:193], v[50:53]
	v_mfma_f32_16x16x32_bf16 v[38:41], v[168:171], v[198:201], v[38:41]
	v_mfma_f32_16x16x32_bf16 v[34:37], v[182:185], v[198:201], v[34:37]
	v_mfma_f32_16x16x32_bf16 v[22:25], v[168:171], v[206:209], v[22:25]
	v_mfma_f32_16x16x32_bf16 v[18:21], v[182:185], v[206:209], v[18:21]
	v_mfma_f32_16x16x32_bf16 v[6:9], v[168:171], v[214:217], v[6:9]
	v_mfma_f32_16x16x32_bf16 v[2:5], v[182:185], v[214:217], v[2:5]
	s_setprio 0
	s_barrier
	s_add_u32 s76, s76, 0x100
	s_addc_u32 s77, s77, 0
	s_add_u32 s40, s40, 0x100
	s_addc_u32 s41, s41, 0
	s_cmp_ge_i32 s78, s65
	s_mov_b32 s42, s78
	s_cbranch_scc0 .LBB0_3356
	v_readlane_b32 s76, v247, 9

; #define PG8_STAGE(bufoff, gbase, voff) do { _Pragma("unroll") for (int _i = 0; _i < 2; ++_i) \
;         __builtin_amdgcn_global_load_lds((const unsigned*)((const char*)(gbase) + (voff)[_i]), (PG8_LAS unsigned*)(lds + (bufoff) + ldsw + _i * 8192), 16, 0, 0); } while (0)
; #define PG8_LDA(dst, b, h) do { if constexpr (DT != 1) { _Pragma("unroll") for (int m = 0; m < 4; ++m) _Pragma("unroll") for (int k = 0; k < 2; ++k) dst[m][k] = *(const PG8_LAS bf16x8*)(lds + PG8_SA(b, h) + aoff + m * 2048 + k * 1024); } \
;         else { _Pragma("unroll") for (int m = 0; m < 4; ++m) dst##8[m] = ld32(lds + PG8_SA(b, h) + aoff + m * 2048); } } while (0)
; #define PG8_LDB(dst, b, h) do { if constexpr (DT != 1) { _Pragma("unroll") for (int n = 0; n < 2; ++n) _Pragma("unroll") for (int k = 0; k < 2; ++k) dst[n][k] = *(const PG8_LAS bf16x8*)(lds + PG8_SB(b, h) + boff + n * 2048 + k * 1024); } \
;         else { _Pragma("unroll") for (int n = 0; n < 2; ++n) dst##8[n] = ld32(lds + PG8_SB(b, h) + boff + n * 2048); } } while (0)
; #define PG8_WAIT_V(n) asm volatile("s_waitcnt vmcnt(" #n ")" ::: "memory")
; #define PG8_WAIT_L(n) asm volatile("s_waitcnt lgkmcnt(" #n ")" ::: "memory")
; #define PG8_BAR __builtin_amdgcn_s_barrier()
; #define PG8_SCHED __builtin_amdgcn_sched_barrier(0)
;     ...
;             const char* a1 = cA + (size_t)(t + 1) * kstep;
;             const char* a2 = last ? nA : cA + (size_t)(t + 2) * kstep; const char* b2 = last ? nB : cB + (size_t)(t + 2) * kstep;
;             const char* a3 = a2 + kstep; const char* b3 = b2 + kstep;
;             if (last && has_next) S.a_ready(nxt);
;             if constexpr (SP2) {
;             PG8_LDB(B0, 0, 0); PG8_LDB(B1, 0, 1); PG8_SCHED; PG8_LDA(At, 0, 0); PG8_STAGE(PG8_SA(1, 1), a1 + hstepA, voffA);
;             PG8_WAIT_V(8); PG8_WAIT_L(0); PG8_BAR; PG8_MMA(0, 0, At, B0); PG8_MMA(0, 1, At, B1); PG8_BAR; PG8_SCHED;
;             PG8_LDA(At, 0, 1); PG8_STAGE(PG8_SB(0, 0), b2, voffB); PG8_STAGE(PG8_SB(0, 1), b2 + hstepB, voffB); PG8_STAGE(PG8_SA(0, 0), a2, voffA);
;             PG8_WAIT_V(8); PG8_WAIT_L(0); PG8_BAR; PG8_MMA(1, 0, At, B0); PG8_MMA(1, 1, At, B1); PG8_BAR; PG8_SCHED;
.LBB0_4141:
	v_add_u32_e32 v160, s35, v164
	ds_read_b128 v[122:125], v160
	ds_read_b128 v[126:129], v160 offset:1024
	ds_read_b128 v[130:133], v160 offset:2048
	ds_read_b128 v[170:173], v160 offset:3072
	v_add_u32_e32 v160, s36, v164
	ds_read_b128 v[174:177], v160
	ds_read_b128 v[178:181], v160 offset:1024
	ds_read_b128 v[182:185], v160 offset:2048
	ds_read_b128 v[186:189], v160 offset:3072
	s_add_i32 s69, s26, 2
	s_add_u32 s27, s24, 0xfffc0080
	s_addc_u32 s28, s25, -1
	s_cmp_eq_u32 s61, s26
	s_cselect_b32 s26, s66, s67
	s_cselect_b32 s29, s15, s28
	s_cselect_b32 s28, s17, s27
	s_cselect_b32 s27, s65, s68
	s_add_i32 m0, s46, 0xc000
	ds_read_b128 v[190:193], v167
	ds_read_b128 v[194:197], v167 offset:1024
	ds_read_b128 v[198:201], v167 offset:2048
	ds_read_b128 v[202:205], v167 offset:3072
	ds_read_b128 v[206:209], v167 offset:4096
	ds_read_b128 v[210:213], v167 offset:5120
	ds_read_b128 v[214:217], v167 offset:6144
	ds_read_b128 v[218:221], v167 offset:7168
	global_load_lds_dwordx4 v154, s[24:25]
	s_add_i32 m0, s46, 0xe000
	s_nop 0
	global_load_lds_dwordx4 v152, s[24:25]
	s_waitcnt vmcnt(8)
	s_waitcnt lgkmcnt(0)
	s_barrier
	s_setprio 1
	s_waitcnt lgkmcnt(0)
	v_mfma_i32_16x16x64_i8 v[134:137], v[122:125], v[190:193], v[134:137]
	v_mfma_i32_16x16x64_i8 v[114:117], v[130:133], v[190:193], v[114:117]
	v_mfma_i32_16x16x64_i8 v[106:109], v[122:125], v[198:201], v[106:109]
	v_mfma_i32_16x16x64_i8 v[98:101], v[130:133], v[198:201], v[98:101]
	v_mfma_i32_16x16x64_i8 v[90:93], v[122:125], v[206:209], v[90:93]
	v_mfma_i32_16x16x64_i8 v[82:85], v[130:133], v[206:209], v[82:85]
	v_mfma_i32_16x16x64_i8 v[74:77], v[122:125], v[214:217], v[74:77]
	v_mfma_i32_16x16x64_i8 v[66:69], v[130:133], v[214:217], v[66:69]
	v_mfma_i32_16x16x64_i8 v[134:137], v[126:129], v[194:197], v[134:137]
	v_mfma_i32_16x16x64_i8 v[114:117], v[170:173], v[194:197], v[114:117]
	v_mfma_i32_16x16x64_i8 v[106:109], v[126:129], v[202:205], v[106:109]
	v_mfma_i32_16x16x64_i8 v[98:101], v[170:173], v[202:205], v[98:101]
	v_mfma_i32_16x16x64_i8 v[90:93], v[126:129], v[210:213], v[90:93]
	v_mfma_i32_16x16x64_i8 v[82:85], v[170:173], v[210:213], v[82:85]
	v_mfma_i32_16x16x64_i8 v[74:77], v[126:129], v[218:221], v[74:77]
	v_mfma_i32_16x16x64_i8 v[66:69], v[170:173], v[218:221], v[66:69]
	s_setprio 0
	s_setprio 1
	v_mfma_i32_16x16x64_i8 v[138:141], v[174:177], v[190:193], v[138:141]
	v_mfma_i32_16x16x64_i8 v[118:121], v[182:185], v[190:193], v[118:121]
	v_mfma_i32_16x16x64_i8 v[110:113], v[174:177], v[198:201], v[110:113]
	v_mfma_i32_16x16x64_i8 v[102:105], v[182:185], v[198:201], v[102:105]
	v_mfma_i32_16x16x64_i8 v[94:97], v[174:177], v[206:209], v[94:97]
	v_mfma_i32_16x16x64_i8 v[86:89], v[182:185], v[206:209], v[86:89]
	v_mfma_i32_16x16x64_i8 v[78:81], v[174:177], v[214:217], v[78:81]
	v_mfma_i32_16x16x64_i8 v[70:73], v[182:185], v[214:217], v[70:73]
	v_mfma_i32_16x16x64_i8 v[138:141], v[178:181], v[194:197], v[138:141]
	v_mfma_i32_16x16x64_i8 v[118:121], v[186:189], v[194:197], v[118:121]
	v_mfma_i32_16x16x64_i8 v[110:113], v[178:181], v[202:205], v[110:113]
	v_mfma_i32_16x16x64_i8 v[102:105], v[186:189], v[202:205], v[102:105]
	v_mfma_i32_16x16x64_i8 v[94:97], v[178:181], v[210:213], v[94:97]
	v_mfma_i32_16x16x64_i8 v[86:89], v[186:189], v[210:213], v[86:89]
	v_mfma_i32_16x16x64_i8 v[78:81], v[178:181], v[218:221], v[78:81]
	v_mfma_i32_16x16x64_i8 v[70:73], v[186:189], v[218:221], v[70:73]
	s_setprio 0
	s_barrier
	s_mov_b32 m0, s23
	s_add_u32 s98, s26, 0x80
	s_addc_u32 s99, s27, 0
	s_add_u32 s70, s26, 0x40000
	ds_read_b128 v[190:193], v167 offset:16384
	ds_read_b128 v[194:197], v167 offset:17408
	ds_read_b128 v[198:201], v167 offset:18432
	ds_read_b128 v[202:205], v167 offset:19456
	ds_read_b128 v[206:209], v167 offset:20480
	ds_read_b128 v[210:213], v167 offset:21504
	ds_read_b128 v[214:217], v167 offset:22528
	ds_read_b128 v[218:221], v167 offset:23552
	global_load_lds_dwordx4 v144, s[26:27]
	s_mov_b32 m0, s43
	s_addc_u32 s71, s27, 0
	global_load_lds_dwordx4 v148, s[26:27]
	s_mov_b32 m0, s44
	s_nop 0
	global_load_lds_dwordx4 v144, s[70:71]
	s_mov_b32 m0, s45
	s_nop 0
	global_load_lds_dwordx4 v148, s[70:71]
	s_add_u32 s100, s28, 0x80
	s_addc_u32 s101, s29, 0
	s_mov_b32 m0, s46
	s_nop 0
	global_load_lds_dwordx4 v142, s[28:29]
	s_mov_b32 m0, s47
	s_nop 0
	global_load_lds_dwordx4 v146, s[28:29]
	s_waitcnt vmcnt(8)
	s_waitcnt lgkmcnt(0)
	s_barrier
	s_setprio 1
	s_waitcnt lgkmcnt(0)
	v_mfma_i32_16x16x64_i8 v[58:61], v[122:125], v[190:193], v[58:61]
	v_mfma_i32_16x16x64_i8 v[50:53], v[130:133], v[190:193], v[50:53]
	v_mfma_i32_16x16x64_i8 v[42:45], v[122:125], v[198:201], v[42:45]
	v_mfma_i32_16x16x64_i8 v[34:37], v[130:133], v[198:201], v[34:37]
	v_mfma_i32_16x16x64_i8 v[26:29], v[122:125], v[206:209], v[26:29]
	v_mfma_i32_16x16x64_i8 v[18:21], v[130:133], v[206:209], v[18:21]
	v_mfma_i32_16x16x64_i8 v[10:13], v[122:125], v[214:217], v[10:13]
	v_mfma_i32_16x16x64_i8 v[2:5], v[130:133], v[214:217], v[2:5]
	v_mfma_i32_16x16x64_i8 v[58:61], v[126:129], v[194:197], v[58:61]
	v_mfma_i32_16x16x64_i8 v[50:53], v[170:173], v[194:197], v[50:53]
	v_mfma_i32_16x16x64_i8 v[42:45], v[126:129], v[202:205], v[42:45]
	v_mfma_i32_16x16x64_i8 v[34:37], v[170:173], v[202:205], v[34:37]
	v_mfma_i32_16x16x64_i8 v[26:29], v[126:129], v[210:213], v[26:29]
	v_mfma_i32_16x16x64_i8 v[18:21], v[170:173], v[210:213], v[18:21]
	v_mfma_i32_16x16x64_i8 v[10:13], v[126:129], v[218:221], v[10:13]
	v_mfma_i32_16x16x64_i8 v[2:5], v[170:173], v[218:221], v[2:5]
	s_setprio 0
	s_setprio 1
	v_mfma_i32_16x16x64_i8 v[62:65], v[174:177], v[190:193], v[62:65]
	v_mfma_i32_16x16x64_i8 v[54:57], v[182:185], v[190:193], v[54:57]
	v_mfma_i32_16x16x64_i8 v[46:49], v[174:177], v[198:201], v[46:49]
	v_mfma_i32_16x16x64_i8 v[38:41], v[182:185], v[198:201], v[38:41]
	v_mfma_i32_16x16x64_i8 v[30:33], v[174:177], v[206:209], v[30:33]
	v_mfma_i32_16x16x64_i8 v[22:25], v[182:185], v[206:209], v[22:25]
	v_mfma_i32_16x16x64_i8 v[14:17], v[174:177], v[214:217], v[14:17]
	v_mfma_i32_16x16x64_i8 v[6:9], v[182:185], v[214:217], v[6:9]
	v_mfma_i32_16x16x64_i8 v[62:65], v[178:181], v[194:197], v[62:65]
	v_mfma_i32_16x16x64_i8 v[54:57], v[186:189], v[194:197], v[54:57]
	v_mfma_i32_16x16x64_i8 v[46:49], v[178:181], v[202:205], v[46:49]
	v_mfma_i32_16x16x64_i8 v[38:41], v[186:189], v[202:205], v[38:41]
	v_mfma_i32_16x16x64_i8 v[30:33], v[178:181], v[210:213], v[30:33]
	v_mfma_i32_16x16x64_i8 v[22:25], v[186:189], v[210:213], v[22:25]
	v_mfma_i32_16x16x64_i8 v[14:17], v[178:181], v[218:221], v[14:17]
	v_mfma_i32_16x16x64_i8 v[6:9], v[186:189], v[218:221], v[6:9]
	s_setprio 0
	s_barrier
; #define PG8_STAGE(bufoff, gbase, voff) do { _Pragma("unroll") for (int _i = 0; _i < 2; ++_i) \
;         __builtin_amdgcn_global_load_lds((const unsigned*)((const char*)(gbase) + (voff)[_i]), (PG8_LAS unsigned*)(lds + (bufoff) + ldsw + _i * 8192), 16, 0, 0); } while (0)
; #define PG8_LDA(dst, b, h) do { if constexpr (DT != 1) { _Pragma("unroll") for (int m = 0; m < 4; ++m) _Pragma("unroll") for (int k = 0; k < 2; ++k) dst[m][k] = *(const PG8_LAS bf16x8*)(lds + PG8_SA(b, h) + aoff + m * 2048 + k * 1024); } \
;         else { _Pragma("unroll") for (int m = 0; m < 4; ++m) dst##8[m] = ld32(lds + PG8_SA(b, h) + aoff + m * 2048); } } while (0)
; #define PG8_LDB(dst, b, h) do { if constexpr (DT != 1) { _Pragma("unroll") for (int n = 0; n < 2; ++n) _Pragma("unroll") for (int k = 0; k < 2; ++k) dst[n][k] = *(const PG8_LAS bf16x8*)(lds + PG8_SB(b, h) + boff + n * 2048 + k * 1024); } \
;         else { _Pragma("unroll") for (int n = 0; n < 2; ++n) dst##8[n] = ld32(lds + PG8_SB(b, h) + boff + n * 2048); } } while (0)
; #define PG8_WAIT_V(n) asm volatile("s_waitcnt vmcnt(" #n ")" ::: "memory")
; #define PG8_WAIT_L(n) asm volatile("s_waitcnt lgkmcnt(" #n ")" ::: "memory")
; #define PG8_BAR __builtin_amdgcn_s_barrier()
; #define PG8_SCHED __builtin_amdgcn_sched_barrier(0)
;     ...
;             PG8_LDB(B0, 1, 0); PG8_LDB(B1, 1, 1); PG8_SCHED; PG8_LDA(At, 1, 0); PG8_STAGE(PG8_SA(0, 1), a2 + hstepA, voffA);
;             PG8_WAIT_V(8); PG8_WAIT_L(0); PG8_BAR; PG8_MMA(0, 0, At, B0); PG8_MMA(0, 1, At, B1); PG8_BAR; PG8_SCHED;
;             PG8_LDA(At, 1, 1); PG8_STAGE(PG8_SB(1, 0), b3, voffB); PG8_STAGE(PG8_SB(1, 1), b3 + hstepB, voffB); PG8_STAGE(PG8_SA(1, 0), a3, voffA);
;             PG8_WAIT_V(8); PG8_WAIT_L(0); PG8_BAR; PG8_MMA(1, 0, At, B0); PG8_MMA(1, 1, At, B1); PG8_BAR; PG8_SCHED;
	v_add_u32_e32 v160, s51, v164
	ds_read_b128 v[122:125], v160
	ds_read_b128 v[126:129], v160 offset:1024
	ds_read_b128 v[130:133], v160 offset:2048
	ds_read_b128 v[170:173], v160 offset:3072
	v_add_u32_e32 v160, s52, v164
	ds_read_b128 v[174:177], v160
	ds_read_b128 v[178:181], v160 offset:1024
	ds_read_b128 v[182:185], v160 offset:2048
	ds_read_b128 v[186:189], v160 offset:3072
	s_add_u32 s28, s28, 0x40000
	s_addc_u32 s29, s29, 0
	s_mov_b32 m0, s48
	ds_read_b128 v[190:193], v167 offset:32768
	ds_read_b128 v[194:197], v167 offset:33792
	ds_read_b128 v[198:201], v167 offset:34816
	ds_read_b128 v[202:205], v167 offset:35840
	ds_read_b128 v[206:209], v167 offset:36864
	ds_read_b128 v[210:213], v167 offset:37888
	ds_read_b128 v[214:217], v167 offset:38912
	ds_read_b128 v[218:221], v167 offset:39936
	global_load_lds_dwordx4 v142, s[28:29]
	s_mov_b32 m0, s49
	s_nop 0
	global_load_lds_dwordx4 v146, s[28:29]
	s_waitcnt vmcnt(8)
	s_waitcnt lgkmcnt(0)
	s_barrier
	s_setprio 1
	s_waitcnt lgkmcnt(0)
	v_mfma_i32_16x16x64_i8 v[134:137], v[122:125], v[190:193], v[134:137]
	v_mfma_i32_16x16x64_i8 v[114:117], v[130:133], v[190:193], v[114:117]
	v_mfma_i32_16x16x64_i8 v[106:109], v[122:125], v[198:201], v[106:109]
	v_mfma_i32_16x16x64_i8 v[98:101], v[130:133], v[198:201], v[98:101]
	v_mfma_i32_16x16x64_i8 v[90:93], v[122:125], v[206:209], v[90:93]
	v_mfma_i32_16x16x64_i8 v[82:85], v[130:133], v[206:209], v[82:85]
	v_mfma_i32_16x16x64_i8 v[74:77], v[122:125], v[214:217], v[74:77]
	v_mfma_i32_16x16x64_i8 v[66:69], v[130:133], v[214:217], v[66:69]
	v_mfma_i32_16x16x64_i8 v[134:137], v[126:129], v[194:197], v[134:137]
	v_mfma_i32_16x16x64_i8 v[114:117], v[170:173], v[194:197], v[114:117]
	v_mfma_i32_16x16x64_i8 v[106:109], v[126:129], v[202:205], v[106:109]
	v_mfma_i32_16x16x64_i8 v[98:101], v[170:173], v[202:205], v[98:101]
	v_mfma_i32_16x16x64_i8 v[90:93], v[126:129], v[210:213], v[90:93]
	v_mfma_i32_16x16x64_i8 v[82:85], v[170:173], v[210:213], v[82:85]
	v_mfma_i32_16x16x64_i8 v[74:77], v[126:129], v[218:221], v[74:77]
	v_mfma_i32_16x16x64_i8 v[66:69], v[170:173], v[218:221], v[66:69]
	s_setprio 0
	s_setprio 1
	v_mfma_i32_16x16x64_i8 v[138:141], v[174:177], v[190:193], v[138:141]
	v_mfma_i32_16x16x64_i8 v[118:121], v[182:185], v[190:193], v[118:121]
	v_mfma_i32_16x16x64_i8 v[110:113], v[174:177], v[198:201], v[110:113]
	v_mfma_i32_16x16x64_i8 v[102:105], v[182:185], v[198:201], v[102:105]
	v_mfma_i32_16x16x64_i8 v[94:97], v[174:177], v[206:209], v[94:97]
	v_mfma_i32_16x16x64_i8 v[86:89], v[182:185], v[206:209], v[86:89]
	v_mfma_i32_16x16x64_i8 v[78:81], v[174:177], v[214:217], v[78:81]
	v_mfma_i32_16x16x64_i8 v[70:73], v[182:185], v[214:217], v[70:73]
	v_mfma_i32_16x16x64_i8 v[138:141], v[178:181], v[194:197], v[138:141]
	v_mfma_i32_16x16x64_i8 v[118:121], v[186:189], v[194:197], v[118:121]
	v_mfma_i32_16x16x64_i8 v[110:113], v[178:181], v[202:205], v[110:113]
	v_mfma_i32_16x16x64_i8 v[102:105], v[186:189], v[202:205], v[102:105]
	v_mfma_i32_16x16x64_i8 v[94:97], v[178:181], v[210:213], v[94:97]
	v_mfma_i32_16x16x64_i8 v[86:89], v[186:189], v[210:213], v[86:89]
	v_mfma_i32_16x16x64_i8 v[78:81], v[178:181], v[218:221], v[78:81]
	v_mfma_i32_16x16x64_i8 v[70:73], v[186:189], v[218:221], v[70:73]
	s_setprio 0
	s_barrier
	s_mov_b32 m0, s55
	s_add_u32 s26, s26, 0x40080
	ds_read_b128 v[190:193], v167 offset:49152
	ds_read_b128 v[194:197], v167 offset:50176
	ds_read_b128 v[198:201], v167 offset:51200
	ds_read_b128 v[202:205], v167 offset:52224
	ds_read_b128 v[206:209], v167 offset:53248
	ds_read_b128 v[210:213], v167 offset:54272
	ds_read_b128 v[214:217], v167 offset:55296
	ds_read_b128 v[218:221], v167 offset:56320
	global_load_lds_dwordx4 v144, s[98:99]
	s_mov_b32 m0, s56
	s_addc_u32 s27, s27, 0
	global_load_lds_dwordx4 v148, s[98:99]
	s_mov_b32 m0, s59
	s_nop 0
	global_load_lds_dwordx4 v144, s[26:27]
	s_mov_b32 m0, s60
	s_nop 0
	global_load_lds_dwordx4 v148, s[26:27]
	s_mov_b32 m0, s57
	s_nop 0
	global_load_lds_dwordx4 v142, s[100:101]
	s_mov_b32 m0, s58
	s_nop 0
	global_load_lds_dwordx4 v146, s[100:101]
	s_waitcnt vmcnt(8)
	s_waitcnt lgkmcnt(0)
	s_barrier
	s_setprio 1
	s_waitcnt lgkmcnt(0)
	v_mfma_i32_16x16x64_i8 v[58:61], v[122:125], v[190:193], v[58:61]
	v_mfma_i32_16x16x64_i8 v[50:53], v[130:133], v[190:193], v[50:53]
	v_mfma_i32_16x16x64_i8 v[42:45], v[122:125], v[198:201], v[42:45]
	v_mfma_i32_16x16x64_i8 v[34:37], v[130:133], v[198:201], v[34:37]
	v_mfma_i32_16x16x64_i8 v[26:29], v[122:125], v[206:209], v[26:29]
	v_mfma_i32_16x16x64_i8 v[18:21], v[130:133], v[206:209], v[18:21]
	v_mfma_i32_16x16x64_i8 v[10:13], v[122:125], v[214:217], v[10:13]
	v_mfma_i32_16x16x64_i8 v[2:5], v[130:133], v[214:217], v[2:5]
	v_mfma_i32_16x16x64_i8 v[58:61], v[126:129], v[194:197], v[58:61]
	v_mfma_i32_16x16x64_i8 v[50:53], v[170:173], v[194:197], v[50:53]
	v_mfma_i32_16x16x64_i8 v[42:45], v[126:129], v[202:205], v[42:45]
	v_mfma_i32_16x16x64_i8 v[34:37], v[170:173], v[202:205], v[34:37]
	v_mfma_i32_16x16x64_i8 v[26:29], v[126:129], v[210:213], v[26:29]
	v_mfma_i32_16x16x64_i8 v[18:21], v[170:173], v[210:213], v[18:21]
	v_mfma_i32_16x16x64_i8 v[10:13], v[126:129], v[218:221], v[10:13]
	v_mfma_i32_16x16x64_i8 v[2:5], v[170:173], v[218:221], v[2:5]
	s_setprio 0
	s_setprio 1
	v_mfma_i32_16x16x64_i8 v[62:65], v[174:177], v[190:193], v[62:65]
	v_mfma_i32_16x16x64_i8 v[54:57], v[182:185], v[190:193], v[54:57]
	v_mfma_i32_16x16x64_i8 v[46:49], v[174:177], v[198:201], v[46:49]
	v_mfma_i32_16x16x64_i8 v[38:41], v[182:185], v[198:201], v[38:41]
	v_mfma_i32_16x16x64_i8 v[30:33], v[174:177], v[206:209], v[30:33]
	v_mfma_i32_16x16x64_i8 v[22:25], v[182:185], v[206:209], v[22:25]
	v_mfma_i32_16x16x64_i8 v[14:17], v[174:177], v[214:217], v[14:17]
	v_mfma_i32_16x16x64_i8 v[6:9], v[182:185], v[214:217], v[6:9]
	v_mfma_i32_16x16x64_i8 v[62:65], v[178:181], v[194:197], v[62:65]
	v_mfma_i32_16x16x64_i8 v[54:57], v[186:189], v[194:197], v[54:57]
	v_mfma_i32_16x16x64_i8 v[46:49], v[178:181], v[202:205], v[46:49]
	v_mfma_i32_16x16x64_i8 v[38:41], v[186:189], v[202:205], v[38:41]
	v_mfma_i32_16x16x64_i8 v[30:33], v[178:181], v[210:213], v[30:33]
	v_mfma_i32_16x16x64_i8 v[22:25], v[186:189], v[210:213], v[22:25]
	v_mfma_i32_16x16x64_i8 v[14:17], v[178:181], v[218:221], v[14:17]
	v_mfma_i32_16x16x64_i8 v[6:9], v[186:189], v[218:221], v[6:9]
	s_setprio 0
	s_barrier
	s_add_u32 s67, s67, 0x100
	s_addc_u32 s68, s68, 0
	s_add_u32 s24, s24, 0x100
	s_addc_u32 s25, s25, 0
	s_cmp_ge_i32 s69, s54
	s_mov_b32 s26, s69
	s_cbranch_scc0 .LBB0_4141

; #define PG8_STAGE(bufoff, gbase, voff) do { _Pragma("unroll") for (int _i = 0; _i < 2; ++_i) \
;         __builtin_amdgcn_global_load_lds((const unsigned*)((const char*)(gbase) + (voff)[_i]), (PG8_LAS unsigned*)(lds + (bufoff) + ldsw + _i * 8192), 16, 0, 0); } while (0)
; #define PG8_LDA(dst, b, h) do { if constexpr (DT != 1) { _Pragma("unroll") for (int m = 0; m < 4; ++m) _Pragma("unroll") for (int k = 0; k < 2; ++k) dst[m][k] = *(const PG8_LAS bf16x8*)(lds + PG8_SA(b, h) + aoff + m * 2048 + k * 1024); } \
;         else { _Pragma("unroll") for (int m = 0; m < 4; ++m) dst##8[m] = ld32(lds + PG8_SA(b, h) + aoff + m * 2048); } } while (0)
; #define PG8_LDB(dst, b, h) do { if constexpr (DT != 1) { _Pragma("unroll") for (int n = 0; n < 2; ++n) _Pragma("unroll") for (int k = 0; k < 2; ++k) dst[n][k] = *(const PG8_LAS bf16x8*)(lds + PG8_SB(b, h) + boff + n * 2048 + k * 1024); } \
;         else { _Pragma("unroll") for (int n = 0; n < 2; ++n) dst##8[n] = ld32(lds + PG8_SB(b, h) + boff + n * 2048); } } while (0)
; #define PG8_WAIT_V(n) asm volatile("s_waitcnt vmcnt(" #n ")" ::: "memory")
; #define PG8_WAIT_L(n) asm volatile("s_waitcnt lgkmcnt(" #n ")" ::: "memory")
; #define PG8_BAR __builtin_amdgcn_s_barrier()
; #define PG8_SCHED __builtin_amdgcn_sched_barrier(0)
;     ...
;             const char* a1 = cA + (size_t)(t + 1) * kstep;
;             const char* a2 = last ? nA : cA + (size_t)(t + 2) * kstep; const char* b2 = last ? nB : cB + (size_t)(t + 2) * kstep;
;             const char* a3 = a2 + kstep; const char* b3 = b2 + kstep;
;             if (last && has_next) S.a_ready(nxt);
;             if constexpr (SP2) {
;             PG8_LDB(B0, 0, 0); PG8_LDB(B1, 0, 1); PG8_SCHED; PG8_LDA(At, 0, 0); PG8_STAGE(PG8_SA(1, 1), a1 + hstepA, voffA);
;             PG8_WAIT_V(8); PG8_WAIT_L(0); PG8_BAR; PG8_MMA(0, 0, At, B0); PG8_MMA(0, 1, At, B1); PG8_BAR; PG8_SCHED;
;             PG8_LDA(At, 0, 1); PG8_STAGE(PG8_SB(0, 0), b2, voffB); PG8_STAGE(PG8_SB(0, 1), b2 + hstepB, voffB); PG8_STAGE(PG8_SA(0, 0), a2, voffA);
;             PG8_WAIT_V(8); PG8_WAIT_L(0); PG8_BAR; PG8_MMA(1, 0, At, B0); PG8_MMA(1, 1, At, B1); PG8_BAR; PG8_SCHED;
.LBB0_4350:
	v_add_u32_e32 v164, s37, v170
	v_add_u32_e32 v168, s38, v170
	ds_read_b128 v[152:155], v164
	ds_read_b128 v[156:159], v164 offset:1024
	ds_read_b128 v[160:163], v164 offset:2048
	ds_read_b128 v[164:167], v164 offset:3072
	ds_read_b128 v[180:183], v168
	ds_read_b128 v[184:187], v168 offset:1024
	ds_read_b128 v[188:191], v168 offset:2048
	ds_read_b128 v[192:195], v168 offset:3072
	s_add_i32 s70, s28, 2
	s_add_u32 s29, s26, 0xfffc0080
	s_addc_u32 s30, s27, -1
	s_cmp_eq_u32 s64, s28
	s_cselect_b32 s28, s67, s68
	s_cselect_b32 s31, s17, s30
	s_cselect_b32 s30, s19, s29
	s_cselect_b32 s29, s66, s69
	s_add_i32 m0, s49, 0xc000
	ds_read_b128 v[196:199], v179
	ds_read_b128 v[200:203], v179 offset:1024
	ds_read_b128 v[204:207], v179 offset:2048
	ds_read_b128 v[208:211], v179 offset:3072
	ds_read_b128 v[212:215], v179 offset:4096
	ds_read_b128 v[216:219], v179 offset:5120
	ds_read_b128 v[220:223], v179 offset:6144
	ds_read_b128 v[224:227], v179 offset:7168
	global_load_lds_dwordx4 v146, s[26:27]
	s_add_i32 m0, s49, 0xe000
	s_nop 0
	global_load_lds_dwordx4 v144, s[26:27]
	s_waitcnt vmcnt(8)
	s_waitcnt lgkmcnt(0)
	s_barrier
	s_setprio 1
	s_waitcnt lgkmcnt(0)
	v_mfma_i32_16x16x64_i8 v[126:129], v[152:155], v[196:199], v[126:129]
	v_mfma_i32_16x16x64_i8 v[122:125], v[160:163], v[196:199], v[122:125]
	v_mfma_i32_16x16x64_i8 v[118:121], v[152:155], v[204:207], v[118:121]
	v_mfma_i32_16x16x64_i8 v[114:117], v[160:163], v[204:207], v[114:117]
	v_mfma_i32_16x16x64_i8 v[110:113], v[152:155], v[212:215], v[110:113]
	v_mfma_i32_16x16x64_i8 v[106:109], v[160:163], v[212:215], v[106:109]
	v_mfma_i32_16x16x64_i8 v[102:105], v[152:155], v[220:223], v[102:105]
	v_mfma_i32_16x16x64_i8 v[98:101], v[160:163], v[220:223], v[98:101]
	v_mfma_i32_16x16x64_i8 v[126:129], v[156:159], v[200:203], v[126:129]
	v_mfma_i32_16x16x64_i8 v[122:125], v[164:167], v[200:203], v[122:125]
	v_mfma_i32_16x16x64_i8 v[118:121], v[156:159], v[208:211], v[118:121]
	v_mfma_i32_16x16x64_i8 v[114:117], v[164:167], v[208:211], v[114:117]
	v_mfma_i32_16x16x64_i8 v[110:113], v[156:159], v[216:219], v[110:113]
	v_mfma_i32_16x16x64_i8 v[106:109], v[164:167], v[216:219], v[106:109]
	v_mfma_i32_16x16x64_i8 v[102:105], v[156:159], v[224:227], v[102:105]
	v_mfma_i32_16x16x64_i8 v[98:101], v[164:167], v[224:227], v[98:101]
	s_setprio 0
	s_setprio 1
	v_mfma_i32_16x16x64_i8 v[94:97], v[180:183], v[196:199], v[94:97]
	v_mfma_i32_16x16x64_i8 v[86:89], v[188:191], v[196:199], v[86:89]
	v_mfma_i32_16x16x64_i8 v[78:81], v[180:183], v[204:207], v[78:81]
	v_mfma_i32_16x16x64_i8 v[70:73], v[188:191], v[204:207], v[70:73]
	v_mfma_i32_16x16x64_i8 v[62:65], v[180:183], v[212:215], v[62:65]
	v_mfma_i32_16x16x64_i8 v[54:57], v[188:191], v[212:215], v[54:57]
	v_mfma_i32_16x16x64_i8 v[46:49], v[180:183], v[220:223], v[46:49]
	v_mfma_i32_16x16x64_i8 v[38:41], v[188:191], v[220:223], v[38:41]
	v_mfma_i32_16x16x64_i8 v[94:97], v[184:187], v[200:203], v[94:97]
	v_mfma_i32_16x16x64_i8 v[86:89], v[192:195], v[200:203], v[86:89]
	v_mfma_i32_16x16x64_i8 v[78:81], v[184:187], v[208:211], v[78:81]
	v_mfma_i32_16x16x64_i8 v[70:73], v[192:195], v[208:211], v[70:73]
	v_mfma_i32_16x16x64_i8 v[62:65], v[184:187], v[216:219], v[62:65]
	v_mfma_i32_16x16x64_i8 v[54:57], v[192:195], v[216:219], v[54:57]
	v_mfma_i32_16x16x64_i8 v[46:49], v[184:187], v[224:227], v[46:49]
	v_mfma_i32_16x16x64_i8 v[38:41], v[192:195], v[224:227], v[38:41]
	s_setprio 0
	s_barrier
	s_mov_b32 m0, s45
	s_add_u32 s98, s28, 0x80
	s_addc_u32 s99, s29, 0
	s_add_u32 s72, s28, 0x40000
	ds_read_b128 v[196:199], v179 offset:16384
	ds_read_b128 v[200:203], v179 offset:17408
	ds_read_b128 v[204:207], v179 offset:18432
	ds_read_b128 v[208:211], v179 offset:19456
	ds_read_b128 v[212:215], v179 offset:20480
	ds_read_b128 v[216:219], v179 offset:21504
	ds_read_b128 v[220:223], v179 offset:22528
	ds_read_b128 v[224:227], v179 offset:23552
	global_load_lds_dwordx4 v132, s[28:29]
	s_mov_b32 m0, s46
	s_addc_u32 s73, s29, 0
	global_load_lds_dwordx4 v136, s[28:29]
	s_mov_b32 m0, s47
	s_nop 0
	global_load_lds_dwordx4 v132, s[72:73]
	s_mov_b32 m0, s48
	s_nop 0
	global_load_lds_dwordx4 v136, s[72:73]
	s_add_u32 s100, s30, 0x80
	s_addc_u32 s101, s31, 0
	s_mov_b32 m0, s49
	s_nop 0
	global_load_lds_dwordx4 v130, s[30:31]
	s_mov_b32 m0, s50
	s_nop 0
	global_load_lds_dwordx4 v134, s[30:31]
	s_waitcnt vmcnt(8)
	s_waitcnt lgkmcnt(0)
	s_barrier
	s_setprio 1
	s_waitcnt lgkmcnt(0)
	v_mfma_i32_16x16x64_i8 v[90:93], v[152:155], v[196:199], v[90:93]
	v_mfma_i32_16x16x64_i8 v[82:85], v[160:163], v[196:199], v[82:85]
	v_mfma_i32_16x16x64_i8 v[74:77], v[152:155], v[204:207], v[74:77]
	v_mfma_i32_16x16x64_i8 v[66:69], v[160:163], v[204:207], v[66:69]
	v_mfma_i32_16x16x64_i8 v[58:61], v[152:155], v[212:215], v[58:61]
	v_mfma_i32_16x16x64_i8 v[50:53], v[160:163], v[212:215], v[50:53]
	v_mfma_i32_16x16x64_i8 v[42:45], v[152:155], v[220:223], v[42:45]
	v_mfma_i32_16x16x64_i8 v[34:37], v[160:163], v[220:223], v[34:37]
	v_mfma_i32_16x16x64_i8 v[90:93], v[156:159], v[200:203], v[90:93]
	v_mfma_i32_16x16x64_i8 v[82:85], v[164:167], v[200:203], v[82:85]
	v_mfma_i32_16x16x64_i8 v[74:77], v[156:159], v[208:211], v[74:77]
	v_mfma_i32_16x16x64_i8 v[66:69], v[164:167], v[208:211], v[66:69]
	v_mfma_i32_16x16x64_i8 v[58:61], v[156:159], v[216:219], v[58:61]
	v_mfma_i32_16x16x64_i8 v[50:53], v[164:167], v[216:219], v[50:53]
	v_mfma_i32_16x16x64_i8 v[42:45], v[156:159], v[224:227], v[42:45]
	v_mfma_i32_16x16x64_i8 v[34:37], v[164:167], v[224:227], v[34:37]
	s_setprio 0
	s_setprio 1
	v_mfma_i32_16x16x64_i8 v[30:33], v[180:183], v[196:199], v[30:33]
	v_mfma_i32_16x16x64_i8 v[26:29], v[188:191], v[196:199], v[26:29]
	v_mfma_i32_16x16x64_i8 v[22:25], v[180:183], v[204:207], v[22:25]
	v_mfma_i32_16x16x64_i8 v[18:21], v[188:191], v[204:207], v[18:21]
	v_mfma_i32_16x16x64_i8 v[14:17], v[180:183], v[212:215], v[14:17]
	v_mfma_i32_16x16x64_i8 v[10:13], v[188:191], v[212:215], v[10:13]
	v_mfma_i32_16x16x64_i8 v[6:9], v[180:183], v[220:223], v[6:9]
	v_mfma_i32_16x16x64_i8 v[2:5], v[188:191], v[220:223], v[2:5]
	v_mfma_i32_16x16x64_i8 v[30:33], v[184:187], v[200:203], v[30:33]
	v_mfma_i32_16x16x64_i8 v[26:29], v[192:195], v[200:203], v[26:29]
	v_mfma_i32_16x16x64_i8 v[22:25], v[184:187], v[208:211], v[22:25]
	v_mfma_i32_16x16x64_i8 v[18:21], v[192:195], v[208:211], v[18:21]
	v_mfma_i32_16x16x64_i8 v[14:17], v[184:187], v[216:219], v[14:17]
	v_mfma_i32_16x16x64_i8 v[10:13], v[192:195], v[216:219], v[10:13]
	v_mfma_i32_16x16x64_i8 v[6:9], v[184:187], v[224:227], v[6:9]
	v_mfma_i32_16x16x64_i8 v[2:5], v[192:195], v[224:227], v[2:5]
	s_setprio 0
	s_barrier
; #define PG8_STAGE(bufoff, gbase, voff) do { _Pragma("unroll") for (int _i = 0; _i < 2; ++_i) \
;         __builtin_amdgcn_global_load_lds((const unsigned*)((const char*)(gbase) + (voff)[_i]), (PG8_LAS unsigned*)(lds + (bufoff) + ldsw + _i * 8192), 16, 0, 0); } while (0)
; #define PG8_LDA(dst, b, h) do { if constexpr (DT != 1) { _Pragma("unroll") for (int m = 0; m < 4; ++m) _Pragma("unroll") for (int k = 0; k < 2; ++k) dst[m][k] = *(const PG8_LAS bf16x8*)(lds + PG8_SA(b, h) + aoff + m * 2048 + k * 1024); } \
;         else { _Pragma("unroll") for (int m = 0; m < 4; ++m) dst##8[m] = ld32(lds + PG8_SA(b, h) + aoff + m * 2048); } } while (0)
; #define PG8_LDB(dst, b, h) do { if constexpr (DT != 1) { _Pragma("unroll") for (int n = 0; n < 2; ++n) _Pragma("unroll") for (int k = 0; k < 2; ++k) dst[n][k] = *(const PG8_LAS bf16x8*)(lds + PG8_SB(b, h) + boff + n * 2048 + k * 1024); } \
;         else { _Pragma("unroll") for (int n = 0; n < 2; ++n) dst##8[n] = ld32(lds + PG8_SB(b, h) + boff + n * 2048); } } while (0)
; #define PG8_WAIT_V(n) asm volatile("s_waitcnt vmcnt(" #n ")" ::: "memory")
; #define PG8_WAIT_L(n) asm volatile("s_waitcnt lgkmcnt(" #n ")" ::: "memory")
; #define PG8_BAR __builtin_amdgcn_s_barrier()
; #define PG8_SCHED __builtin_amdgcn_sched_barrier(0)
;     ...
;             PG8_LDB(B0, 1, 0); PG8_LDB(B1, 1, 1); PG8_SCHED; PG8_LDA(At, 1, 0); PG8_STAGE(PG8_SA(0, 1), a2 + hstepA, voffA);
;             PG8_WAIT_V(8); PG8_WAIT_L(0); PG8_BAR; PG8_MMA(0, 0, At, B0); PG8_MMA(0, 1, At, B1); PG8_BAR; PG8_SCHED;
;             PG8_LDA(At, 1, 1); PG8_STAGE(PG8_SB(1, 0), b3, voffB); PG8_STAGE(PG8_SB(1, 1), b3 + hstepB, voffB); PG8_STAGE(PG8_SA(1, 0), a3, voffA);
;             PG8_WAIT_V(8); PG8_WAIT_L(0); PG8_BAR; PG8_MMA(1, 0, At, B0); PG8_MMA(1, 1, At, B1); PG8_BAR; PG8_SCHED;
	v_add_u32_e32 v164, s54, v170
	v_add_u32_e32 v192, s55, v170
	ds_read_b128 v[152:155], v164
	ds_read_b128 v[156:159], v164 offset:1024
	ds_read_b128 v[160:163], v164 offset:2048
	ds_read_b128 v[164:167], v164 offset:3072
	ds_read_b128 v[180:183], v192
	ds_read_b128 v[184:187], v192 offset:1024
	ds_read_b128 v[188:191], v192 offset:2048
	ds_read_b128 v[192:195], v192 offset:3072
	s_add_u32 s30, s30, 0x40000
	s_addc_u32 s31, s31, 0
	s_mov_b32 m0, s51
	ds_read_b128 v[196:199], v179 offset:32768
	ds_read_b128 v[200:203], v179 offset:33792
	ds_read_b128 v[204:207], v179 offset:34816
	ds_read_b128 v[208:211], v179 offset:35840
	ds_read_b128 v[212:215], v179 offset:36864
	ds_read_b128 v[216:219], v179 offset:37888
	ds_read_b128 v[220:223], v179 offset:38912
	ds_read_b128 v[224:227], v179 offset:39936
	global_load_lds_dwordx4 v130, s[30:31]
	s_mov_b32 m0, s52
	s_nop 0
	global_load_lds_dwordx4 v134, s[30:31]
	s_waitcnt vmcnt(8)
	s_waitcnt lgkmcnt(0)
	s_barrier
	s_setprio 1
	s_waitcnt lgkmcnt(0)
	v_mfma_i32_16x16x64_i8 v[126:129], v[152:155], v[196:199], v[126:129]
	v_mfma_i32_16x16x64_i8 v[122:125], v[160:163], v[196:199], v[122:125]
	v_mfma_i32_16x16x64_i8 v[118:121], v[152:155], v[204:207], v[118:121]
	v_mfma_i32_16x16x64_i8 v[114:117], v[160:163], v[204:207], v[114:117]
	v_mfma_i32_16x16x64_i8 v[110:113], v[152:155], v[212:215], v[110:113]
	v_mfma_i32_16x16x64_i8 v[106:109], v[160:163], v[212:215], v[106:109]
	v_mfma_i32_16x16x64_i8 v[102:105], v[152:155], v[220:223], v[102:105]
	v_mfma_i32_16x16x64_i8 v[98:101], v[160:163], v[220:223], v[98:101]
	v_mfma_i32_16x16x64_i8 v[126:129], v[156:159], v[200:203], v[126:129]
	v_mfma_i32_16x16x64_i8 v[122:125], v[164:167], v[200:203], v[122:125]
	v_mfma_i32_16x16x64_i8 v[118:121], v[156:159], v[208:211], v[118:121]
	v_mfma_i32_16x16x64_i8 v[114:117], v[164:167], v[208:211], v[114:117]
	v_mfma_i32_16x16x64_i8 v[110:113], v[156:159], v[216:219], v[110:113]
	v_mfma_i32_16x16x64_i8 v[106:109], v[164:167], v[216:219], v[106:109]
	v_mfma_i32_16x16x64_i8 v[102:105], v[156:159], v[224:227], v[102:105]
	v_mfma_i32_16x16x64_i8 v[98:101], v[164:167], v[224:227], v[98:101]
	s_setprio 0
	s_setprio 1
	v_mfma_i32_16x16x64_i8 v[94:97], v[180:183], v[196:199], v[94:97]
	v_mfma_i32_16x16x64_i8 v[86:89], v[188:191], v[196:199], v[86:89]
	v_mfma_i32_16x16x64_i8 v[78:81], v[180:183], v[204:207], v[78:81]
	v_mfma_i32_16x16x64_i8 v[70:73], v[188:191], v[204:207], v[70:73]
	v_mfma_i32_16x16x64_i8 v[62:65], v[180:183], v[212:215], v[62:65]
	v_mfma_i32_16x16x64_i8 v[54:57], v[188:191], v[212:215], v[54:57]
	v_mfma_i32_16x16x64_i8 v[46:49], v[180:183], v[220:223], v[46:49]
	v_mfma_i32_16x16x64_i8 v[38:41], v[188:191], v[220:223], v[38:41]
	v_mfma_i32_16x16x64_i8 v[94:97], v[184:187], v[200:203], v[94:97]
	v_mfma_i32_16x16x64_i8 v[86:89], v[192:195], v[200:203], v[86:89]
	v_mfma_i32_16x16x64_i8 v[78:81], v[184:187], v[208:211], v[78:81]
	v_mfma_i32_16x16x64_i8 v[70:73], v[192:195], v[208:211], v[70:73]
	v_mfma_i32_16x16x64_i8 v[62:65], v[184:187], v[216:219], v[62:65]
	v_mfma_i32_16x16x64_i8 v[54:57], v[192:195], v[216:219], v[54:57]
	v_mfma_i32_16x16x64_i8 v[46:49], v[184:187], v[224:227], v[46:49]
	v_mfma_i32_16x16x64_i8 v[38:41], v[192:195], v[224:227], v[38:41]
	s_setprio 0
	s_barrier
	s_mov_b32 m0, s58
	s_add_u32 s28, s28, 0x40080
	ds_read_b128 v[196:199], v179 offset:49152
	ds_read_b128 v[200:203], v179 offset:50176
	ds_read_b128 v[204:207], v179 offset:51200
	ds_read_b128 v[208:211], v179 offset:52224
	ds_read_b128 v[212:215], v179 offset:53248
	ds_read_b128 v[216:219], v179 offset:54272
	ds_read_b128 v[220:223], v179 offset:55296
	ds_read_b128 v[224:227], v179 offset:56320
	global_load_lds_dwordx4 v132, s[98:99]
	s_mov_b32 m0, s59
	s_addc_u32 s29, s29, 0
	global_load_lds_dwordx4 v136, s[98:99]
	s_mov_b32 m0, s62
	s_nop 0
	global_load_lds_dwordx4 v132, s[28:29]
	s_mov_b32 m0, s63
	s_nop 0
	global_load_lds_dwordx4 v136, s[28:29]
	s_mov_b32 m0, s60
	s_nop 0
	global_load_lds_dwordx4 v130, s[100:101]
	s_mov_b32 m0, s61
	s_nop 0
	global_load_lds_dwordx4 v134, s[100:101]
	s_waitcnt vmcnt(8)
	s_waitcnt lgkmcnt(0)
	s_barrier
; #define PG8_WAIT_V(n) asm volatile("s_waitcnt vmcnt(" #n ")" ::: "memory")
; #define PG8_WAIT_L(n) asm volatile("s_waitcnt lgkmcnt(" #n ")" ::: "memory")
; #define PG8_BAR __builtin_amdgcn_s_barrier()
; #define PG8_SCHED __builtin_amdgcn_sched_barrier(0)
; __device__ __forceinline__ f32x4 i32bits_to_f32(f32x4 v) { return (f32x4){(float)__float_as_int(v.x), (float)__float_as_int(v.y), (float)__float_as_int(v.z), (float)__float_as_int(v.w)}; }
;     ...
;             PG8_WAIT_V(8); PG8_WAIT_L(0); PG8_BAR; PG8_MMA(1, 0, At, B0); PG8_MMA(1, 1, At, B1); PG8_BAR; PG8_SCHED;
	s_setprio 1
	s_waitcnt lgkmcnt(0)
	v_mfma_i32_16x16x64_i8 v[90:93], v[152:155], v[196:199], v[90:93]
	v_mfma_i32_16x16x64_i8 v[82:85], v[160:163], v[196:199], v[82:85]
	v_mfma_i32_16x16x64_i8 v[74:77], v[152:155], v[204:207], v[74:77]
	v_mfma_i32_16x16x64_i8 v[66:69], v[160:163], v[204:207], v[66:69]
	v_mfma_i32_16x16x64_i8 v[58:61], v[152:155], v[212:215], v[58:61]
	v_mfma_i32_16x16x64_i8 v[50:53], v[160:163], v[212:215], v[50:53]
	v_mfma_i32_16x16x64_i8 v[42:45], v[152:155], v[220:223], v[42:45]
	v_mfma_i32_16x16x64_i8 v[34:37], v[160:163], v[220:223], v[34:37]
	v_mfma_i32_16x16x64_i8 v[90:93], v[156:159], v[200:203], v[90:93]
	v_mfma_i32_16x16x64_i8 v[82:85], v[164:167], v[200:203], v[82:85]
	v_mfma_i32_16x16x64_i8 v[74:77], v[156:159], v[208:211], v[74:77]
	v_mfma_i32_16x16x64_i8 v[66:69], v[164:167], v[208:211], v[66:69]
	v_mfma_i32_16x16x64_i8 v[58:61], v[156:159], v[216:219], v[58:61]
	v_mfma_i32_16x16x64_i8 v[50:53], v[164:167], v[216:219], v[50:53]
	v_mfma_i32_16x16x64_i8 v[42:45], v[156:159], v[224:227], v[42:45]
	v_mfma_i32_16x16x64_i8 v[34:37], v[164:167], v[224:227], v[34:37]
	s_setprio 0
	s_setprio 1
	v_mfma_i32_16x16x64_i8 v[30:33], v[180:183], v[196:199], v[30:33]
	v_mfma_i32_16x16x64_i8 v[26:29], v[188:191], v[196:199], v[26:29]
	v_mfma_i32_16x16x64_i8 v[22:25], v[180:183], v[204:207], v[22:25]
	v_mfma_i32_16x16x64_i8 v[18:21], v[188:191], v[204:207], v[18:21]
	v_mfma_i32_16x16x64_i8 v[14:17], v[180:183], v[212:215], v[14:17]
	v_mfma_i32_16x16x64_i8 v[10:13], v[188:191], v[212:215], v[10:13]
	v_mfma_i32_16x16x64_i8 v[6:9], v[180:183], v[220:223], v[6:9]
	v_mfma_i32_16x16x64_i8 v[2:5], v[188:191], v[220:223], v[2:5]
	v_mfma_i32_16x16x64_i8 v[30:33], v[184:187], v[200:203], v[30:33]
	v_mfma_i32_16x16x64_i8 v[26:29], v[192:195], v[200:203], v[26:29]
	v_mfma_i32_16x16x64_i8 v[22:25], v[184:187], v[208:211], v[22:25]
	v_mfma_i32_16x16x64_i8 v[18:21], v[192:195], v[208:211], v[18:21]
	v_mfma_i32_16x16x64_i8 v[14:17], v[184:187], v[216:219], v[14:17]
	v_mfma_i32_16x16x64_i8 v[10:13], v[192:195], v[216:219], v[10:13]
	v_mfma_i32_16x16x64_i8 v[6:9], v[184:187], v[224:227], v[6:9]
	v_mfma_i32_16x16x64_i8 v[2:5], v[192:195], v[224:227], v[2:5]
	s_setprio 0
	s_barrier
	s_add_u32 s68, s68, 0x100
	s_addc_u32 s69, s69, 0
	s_add_u32 s26, s26, 0x100
	s_addc_u32 s27, s27, 0
	s_cmp_ge_i32 s70, s57
	s_mov_b32 s28, s70
	s_cbranch_scc0 .LBB0_4350
	v_cvt_f32_i32_e32 v166, v126
	v_cvt_f32_i32_e32 v167, v127
	v_cvt_f32_i32_e32 v160, v128
	v_cvt_f32_i32_e32 v161, v129
	v_cvt_f32_i32_e32 v162, v122
	v_cvt_f32_i32_e32 v163, v123
	v_cvt_f32_i32_e32 v164, v124
	v_cvt_f32_i32_e32 v165, v125
	v_cvt_f32_i32_e32 v152, v118
	v_cvt_f32_i32_e32 v153, v119
	v_cvt_f32_i32_e32 v154, v120
	v_cvt_f32_i32_e32 v155, v121
	v_cvt_f32_i32_e32 v156, v114
	v_cvt_f32_i32_e32 v157, v115
	v_cvt_f32_i32_e32 v158, v116
	v_cvt_f32_i32_e32 v159, v117
	v_cvt_f32_i32_e32 v110, v110
	v_cvt_f32_i32_e32 v111, v111
	v_cvt_f32_i32_e32 v112, v112
	v_cvt_f32_i32_e32 v113, v113
	v_cvt_f32_i32_e32 v106, v106
	v_cvt_f32_i32_e32 v107, v107
	v_cvt_f32_i32_e32 v108, v108
	v_cvt_f32_i32_e32 v109, v109
	v_cvt_f32_i32_e32 v102, v102
	v_cvt_f32_i32_e32 v103, v103
	v_cvt_f32_i32_e32 v104, v104
	v_cvt_f32_i32_e32 v105, v105
	v_cvt_f32_i32_e32 v98, v98
	v_cvt_f32_i32_e32 v99, v99
	v_cvt_f32_i32_e32 v100, v100
	v_cvt_f32_i32_e32 v101, v101
	v_cvt_f32_i32_e32 v90, v90
	v_cvt_f32_i32_e32 v91, v91
	v_cvt_f32_i32_e32 v92, v92
	v_cvt_f32_i32_e32 v93, v93
	v_cvt_f32_i32_e32 v82, v82
	v_cvt_f32_i32_e32 v83, v83
	v_cvt_f32_i32_e32 v84, v84
	v_cvt_f32_i32_e32 v85, v85
	v_cvt_f32_i32_e32 v74, v74
	v_cvt_f32_i32_e32 v75, v75
	v_cvt_f32_i32_e32 v76, v76
	v_cvt_f32_i32_e32 v77, v77
	v_cvt_f32_i32_e32 v66, v66
	v_cvt_f32_i32_e32 v67, v67
	v_cvt_f32_i32_e32 v68, v68
	v_cvt_f32_i32_e32 v69, v69
	v_cvt_f32_i32_e32 v58, v58
	v_cvt_f32_i32_e32 v59, v59
	v_cvt_f32_i32_e32 v60, v60
	v_cvt_f32_i32_e32 v61, v61
	v_cvt_f32_i32_e32 v50, v50
	v_cvt_f32_i32_e32 v51, v51
	v_cvt_f32_i32_e32 v52, v52
	v_cvt_f32_i32_e32 v53, v53
	v_cvt_f32_i32_e32 v42, v42
	v_cvt_f32_i32_e32 v43, v43
	v_cvt_f32_i32_e32 v44, v44
	v_cvt_f32_i32_e32 v45, v45
	v_cvt_f32_i32_e32 v34, v34
	v_cvt_f32_i32_e32 v35, v35
	v_cvt_f32_i32_e32 v36, v36
	v_cvt_f32_i32_e32 v37, v37
	v_cvt_f32_i32_e32 v114, v94
	v_cvt_f32_i32_e32 v115, v95
	v_cvt_f32_i32_e32 v116, v96
	v_cvt_f32_i32_e32 v117, v97
	v_cvt_f32_i32_e32 v118, v86
	v_cvt_f32_i32_e32 v119, v87
	v_cvt_f32_i32_e32 v120, v88
	v_cvt_f32_i32_e32 v121, v89
	v_cvt_f32_i32_e32 v122, v78
	v_cvt_f32_i32_e32 v123, v79
	v_cvt_f32_i32_e32 v124, v80
	v_cvt_f32_i32_e32 v125, v81
	v_cvt_f32_i32_e32 v126, v70
	v_cvt_f32_i32_e32 v127, v71
	v_cvt_f32_i32_e32 v128, v72
	v_cvt_f32_i32_e32 v129, v73
	v_cvt_f32_i32_e32 v88, v62
	v_cvt_f32_i32_e32 v89, v63
	v_cvt_f32_i32_e32 v96, v64
	v_cvt_f32_i32_e32 v97, v65
	v_cvt_f32_i32_e32 v86, v54
	v_cvt_f32_i32_e32 v87, v55
	v_cvt_f32_i32_e32 v94, v56
	v_cvt_f32_i32_e32 v95, v57
	v_cvt_f32_i32_e32 v72, v46
	v_cvt_f32_i32_e32 v73, v47
	v_cvt_f32_i32_e32 v80, v48
	v_cvt_f32_i32_e32 v81, v49
	v_cvt_f32_i32_e32 v70, v38
	v_cvt_f32_i32_e32 v71, v39
	v_cvt_f32_i32_e32 v78, v40
	v_cvt_f32_i32_e32 v79, v41
	v_cvt_f32_i32_e32 v56, v30
	v_cvt_f32_i32_e32 v57, v31
	v_cvt_f32_i32_e32 v64, v32
	v_cvt_f32_i32_e32 v65, v33
	v_cvt_f32_i32_e32 v54, v26
	v_cvt_f32_i32_e32 v55, v27
	v_cvt_f32_i32_e32 v62, v28
	v_cvt_f32_i32_e32 v63, v29
	v_cvt_f32_i32_e32 v40, v22
	v_cvt_f32_i32_e32 v41, v23
	v_cvt_f32_i32_e32 v48, v24
	v_cvt_f32_i32_e32 v49, v25
	v_cvt_f32_i32_e32 v38, v18
	v_cvt_f32_i32_e32 v39, v19
	v_cvt_f32_i32_e32 v46, v20
	v_cvt_f32_i32_e32 v47, v21
	v_cvt_f32_i32_e32 v28, v14
	v_cvt_f32_i32_e32 v29, v15
	v_cvt_f32_i32_e32 v32, v16
	v_cvt_f32_i32_e32 v33, v17
	v_cvt_f32_i32_e32 v26, v10
	v_cvt_f32_i32_e32 v27, v11
	v_cvt_f32_i32_e32 v30, v12
	v_cvt_f32_i32_e32 v31, v13
	v_cvt_f32_i32_e32 v20, v6
	v_cvt_f32_i32_e32 v21, v7
	v_cvt_f32_i32_e32 v24, v8
	v_cvt_f32_i32_e32 v25, v9
	v_cvt_f32_i32_e32 v18, v2
	v_cvt_f32_i32_e32 v19, v3
	v_cvt_f32_i32_e32 v22, v4
	v_cvt_f32_i32_e32 v23, v5

; #define PG8_STAGE(bufoff, gbase, voff) do { _Pragma("unroll") for (int _i = 0; _i < 2; ++_i) \
;         __builtin_amdgcn_global_load_lds((const unsigned*)((const char*)(gbase) + (voff)[_i]), (PG8_LAS unsigned*)(lds + (bufoff) + ldsw + _i * 8192), 16, 0, 0); } while (0)
; #define PG8_LDA(dst, b, h) do { if constexpr (DT != 1) { _Pragma("unroll") for (int m = 0; m < 4; ++m) _Pragma("unroll") for (int k = 0; k < 2; ++k) dst[m][k] = *(const PG8_LAS bf16x8*)(lds + PG8_SA(b, h) + aoff + m * 2048 + k * 1024); } \
;         else { _Pragma("unroll") for (int m = 0; m < 4; ++m) dst##8[m] = ld32(lds + PG8_SA(b, h) + aoff + m * 2048); } } while (0)
; #define PG8_LDB(dst, b, h) do { if constexpr (DT != 1) { _Pragma("unroll") for (int n = 0; n < 2; ++n) _Pragma("unroll") for (int k = 0; k < 2; ++k) dst[n][k] = *(const PG8_LAS bf16x8*)(lds + PG8_SB(b, h) + boff + n * 2048 + k * 1024); } \
;         else { _Pragma("unroll") for (int n = 0; n < 2; ++n) dst##8[n] = ld32(lds + PG8_SB(b, h) + boff + n * 2048); } } while (0)
; #define PG8_WAIT_V(n) asm volatile("s_waitcnt vmcnt(" #n ")" ::: "memory")
; #define PG8_WAIT_L(n) asm volatile("s_waitcnt lgkmcnt(" #n ")" ::: "memory")
; #define PG8_BAR __builtin_amdgcn_s_barrier()
; #define PG8_SCHED __builtin_amdgcn_sched_barrier(0)
;     ...
;             const char* a1 = cA + (size_t)(t + 1) * kstep;
;             const char* a2 = last ? nA : cA + (size_t)(t + 2) * kstep; const char* b2 = last ? nB : cB + (size_t)(t + 2) * kstep;
;             const char* a3 = a2 + kstep; const char* b3 = b2 + kstep;
;             if (last && has_next) S.a_ready(nxt);
;             if constexpr (SP2) {
;             PG8_LDB(B0, 0, 0); PG8_LDB(B1, 0, 1); PG8_SCHED; PG8_LDA(At, 0, 0); PG8_STAGE(PG8_SA(1, 1), a1 + hstepA, voffA);
;             PG8_WAIT_V(8); PG8_WAIT_L(0); PG8_BAR; PG8_MMA(0, 0, At, B0); PG8_MMA(0, 1, At, B1); PG8_BAR; PG8_SCHED;
;             PG8_LDA(At, 0, 1); PG8_STAGE(PG8_SB(0, 0), b2, voffB); PG8_STAGE(PG8_SB(0, 1), b2 + hstepB, voffB); PG8_STAGE(PG8_SA(0, 0), a2, voffA);
;             PG8_WAIT_V(8); PG8_WAIT_L(0); PG8_BAR; PG8_MMA(1, 0, At, B0); PG8_MMA(1, 1, At, B1); PG8_BAR; PG8_SCHED;
.LBB0_4646:
	ds_read_b128 v[146:149], v157
	ds_read_b128 v[150:153], v157 offset:1024
	ds_read_b128 v[162:165], v157 offset:2048
	ds_read_b128 v[166:169], v157 offset:3072
	ds_read_b128 v[170:173], v158
	ds_read_b128 v[174:177], v158 offset:1024
	ds_read_b128 v[178:181], v158 offset:2048
	ds_read_b128 v[182:185], v158 offset:3072
	s_add_i32 s71, s38, 2
	s_add_u32 s39, s36, 0xfff80080
	s_addc_u32 s40, s37, -1
	s_cmp_eq_u32 s63, s38
	s_cselect_b32 s38, s68, s69
	s_cselect_b32 s41, s25, s40
	s_cselect_b32 s40, s27, s39
	s_cselect_b32 s39, s67, s70
	s_add_i32 m0, s51, 0xc000
	ds_read_b128 v[186:189], v159
	ds_read_b128 v[190:193], v159 offset:1024
	ds_read_b128 v[194:197], v159 offset:2048
	ds_read_b128 v[198:201], v159 offset:3072
	ds_read_b128 v[202:205], v159 offset:4096
	ds_read_b128 v[206:209], v159 offset:5120
	ds_read_b128 v[210:213], v159 offset:6144
	ds_read_b128 v[214:217], v159 offset:7168
	global_load_lds_dwordx4 v140, s[36:37]
	s_add_i32 m0, s51, 0xe000
	s_nop 0
	global_load_lds_dwordx4 v138, s[36:37]
	s_waitcnt vmcnt(8)
	s_waitcnt lgkmcnt(0)
	s_barrier
	s_setprio 1
	s_waitcnt lgkmcnt(0)
	v_mfma_f32_16x16x32_bf16 v[122:125], v[146:149], v[186:189], v[122:125]
	v_mfma_f32_16x16x32_bf16 v[126:129], v[162:165], v[186:189], v[126:129]
	v_mfma_f32_16x16x32_bf16 v[110:113], v[146:149], v[194:197], v[110:113]
	v_mfma_f32_16x16x32_bf16 v[106:109], v[162:165], v[194:197], v[106:109]
	v_mfma_f32_16x16x32_bf16 v[94:97], v[146:149], v[202:205], v[94:97]
	v_mfma_f32_16x16x32_bf16 v[90:93], v[162:165], v[202:205], v[90:93]
	v_mfma_f32_16x16x32_bf16 v[78:81], v[146:149], v[210:213], v[78:81]
	v_mfma_f32_16x16x32_bf16 v[74:77], v[162:165], v[210:213], v[74:77]
	v_mfma_f32_16x16x32_bf16 v[122:125], v[150:153], v[190:193], v[122:125]
	v_mfma_f32_16x16x32_bf16 v[126:129], v[166:169], v[190:193], v[126:129]
	v_mfma_f32_16x16x32_bf16 v[110:113], v[150:153], v[198:201], v[110:113]
	v_mfma_f32_16x16x32_bf16 v[106:109], v[166:169], v[198:201], v[106:109]
	v_mfma_f32_16x16x32_bf16 v[94:97], v[150:153], v[206:209], v[94:97]
	v_mfma_f32_16x16x32_bf16 v[90:93], v[166:169], v[206:209], v[90:93]
	v_mfma_f32_16x16x32_bf16 v[78:81], v[150:153], v[214:217], v[78:81]
	v_mfma_f32_16x16x32_bf16 v[74:77], v[166:169], v[214:217], v[74:77]
	s_setprio 0
	s_setprio 1
	v_mfma_f32_16x16x32_bf16 v[118:121], v[170:173], v[186:189], v[118:121]
	v_mfma_f32_16x16x32_bf16 v[114:117], v[178:181], v[186:189], v[114:117]
	v_mfma_f32_16x16x32_bf16 v[102:105], v[170:173], v[194:197], v[102:105]
	v_mfma_f32_16x16x32_bf16 v[98:101], v[178:181], v[194:197], v[98:101]
	v_mfma_f32_16x16x32_bf16 v[86:89], v[170:173], v[202:205], v[86:89]
	v_mfma_f32_16x16x32_bf16 v[82:85], v[178:181], v[202:205], v[82:85]
	v_mfma_f32_16x16x32_bf16 v[70:73], v[170:173], v[210:213], v[70:73]
	v_mfma_f32_16x16x32_bf16 v[66:69], v[178:181], v[210:213], v[66:69]
	v_mfma_f32_16x16x32_bf16 v[118:121], v[174:177], v[190:193], v[118:121]
	v_mfma_f32_16x16x32_bf16 v[114:117], v[182:185], v[190:193], v[114:117]
	v_mfma_f32_16x16x32_bf16 v[102:105], v[174:177], v[198:201], v[102:105]
	v_mfma_f32_16x16x32_bf16 v[98:101], v[182:185], v[198:201], v[98:101]
	v_mfma_f32_16x16x32_bf16 v[86:89], v[174:177], v[206:209], v[86:89]
	v_mfma_f32_16x16x32_bf16 v[82:85], v[182:185], v[206:209], v[82:85]
	v_mfma_f32_16x16x32_bf16 v[70:73], v[174:177], v[214:217], v[70:73]
	v_mfma_f32_16x16x32_bf16 v[66:69], v[182:185], v[214:217], v[66:69]
	s_setprio 0
	s_barrier
	s_mov_b32 m0, s35
	s_add_u32 s98, s38, 0x80
	s_addc_u32 s99, s39, 0
	s_add_u32 s72, s38, 0x80000
	ds_read_b128 v[186:189], v159 offset:16384
	ds_read_b128 v[190:193], v159 offset:17408
	ds_read_b128 v[194:197], v159 offset:18432
	ds_read_b128 v[198:201], v159 offset:19456
	ds_read_b128 v[202:205], v159 offset:20480
	ds_read_b128 v[206:209], v159 offset:21504
	ds_read_b128 v[210:213], v159 offset:22528
	ds_read_b128 v[214:217], v159 offset:23552
	global_load_lds_dwordx4 v132, s[38:39]
	s_mov_b32 m0, s48
	s_addc_u32 s73, s39, 0
	global_load_lds_dwordx4 v136, s[38:39]
	s_mov_b32 m0, s49
	s_nop 0
	global_load_lds_dwordx4 v132, s[72:73]
	s_mov_b32 m0, s50
	s_nop 0
	global_load_lds_dwordx4 v136, s[72:73]
	s_add_u32 s100, s40, 0x80
	s_addc_u32 s101, s41, 0
	s_mov_b32 m0, s51
	s_nop 0
	global_load_lds_dwordx4 v130, s[40:41]
	s_mov_b32 m0, s52
	s_nop 0
	global_load_lds_dwordx4 v134, s[40:41]
	s_waitcnt vmcnt(8)
	s_waitcnt lgkmcnt(0)
	s_barrier
	s_setprio 1
	s_waitcnt lgkmcnt(0)
	v_mfma_f32_16x16x32_bf16 v[62:65], v[146:149], v[186:189], v[62:65]
	v_mfma_f32_16x16x32_bf16 v[58:61], v[162:165], v[186:189], v[58:61]
	v_mfma_f32_16x16x32_bf16 v[46:49], v[146:149], v[194:197], v[46:49]
	v_mfma_f32_16x16x32_bf16 v[42:45], v[162:165], v[194:197], v[42:45]
	v_mfma_f32_16x16x32_bf16 v[30:33], v[146:149], v[202:205], v[30:33]
	v_mfma_f32_16x16x32_bf16 v[26:29], v[162:165], v[202:205], v[26:29]
	v_mfma_f32_16x16x32_bf16 v[14:17], v[146:149], v[210:213], v[14:17]
	v_mfma_f32_16x16x32_bf16 v[10:13], v[162:165], v[210:213], v[10:13]
	v_mfma_f32_16x16x32_bf16 v[62:65], v[150:153], v[190:193], v[62:65]
	v_mfma_f32_16x16x32_bf16 v[58:61], v[166:169], v[190:193], v[58:61]
	v_mfma_f32_16x16x32_bf16 v[46:49], v[150:153], v[198:201], v[46:49]
	v_mfma_f32_16x16x32_bf16 v[42:45], v[166:169], v[198:201], v[42:45]
	v_mfma_f32_16x16x32_bf16 v[30:33], v[150:153], v[206:209], v[30:33]
	v_mfma_f32_16x16x32_bf16 v[26:29], v[166:169], v[206:209], v[26:29]
	v_mfma_f32_16x16x32_bf16 v[14:17], v[150:153], v[214:217], v[14:17]
	v_mfma_f32_16x16x32_bf16 v[10:13], v[166:169], v[214:217], v[10:13]
	s_setprio 0
	s_setprio 1
	v_mfma_f32_16x16x32_bf16 v[54:57], v[170:173], v[186:189], v[54:57]
	v_mfma_f32_16x16x32_bf16 v[50:53], v[178:181], v[186:189], v[50:53]
	v_mfma_f32_16x16x32_bf16 v[38:41], v[170:173], v[194:197], v[38:41]
	v_mfma_f32_16x16x32_bf16 v[34:37], v[178:181], v[194:197], v[34:37]
	v_mfma_f32_16x16x32_bf16 v[22:25], v[170:173], v[202:205], v[22:25]
	v_mfma_f32_16x16x32_bf16 v[18:21], v[178:181], v[202:205], v[18:21]
	v_mfma_f32_16x16x32_bf16 v[6:9], v[170:173], v[210:213], v[6:9]
	v_mfma_f32_16x16x32_bf16 v[2:5], v[178:181], v[210:213], v[2:5]
	v_mfma_f32_16x16x32_bf16 v[54:57], v[174:177], v[190:193], v[54:57]
	v_mfma_f32_16x16x32_bf16 v[50:53], v[182:185], v[190:193], v[50:53]
	v_mfma_f32_16x16x32_bf16 v[38:41], v[174:177], v[198:201], v[38:41]
	v_mfma_f32_16x16x32_bf16 v[34:37], v[182:185], v[198:201], v[34:37]
	v_mfma_f32_16x16x32_bf16 v[22:25], v[174:177], v[206:209], v[22:25]
	v_mfma_f32_16x16x32_bf16 v[18:21], v[182:185], v[206:209], v[18:21]
	v_mfma_f32_16x16x32_bf16 v[6:9], v[174:177], v[214:217], v[6:9]
	v_mfma_f32_16x16x32_bf16 v[2:5], v[182:185], v[214:217], v[2:5]
	s_setprio 0
	s_barrier
; #define PG8_STAGE(bufoff, gbase, voff) do { _Pragma("unroll") for (int _i = 0; _i < 2; ++_i) \
;         __builtin_amdgcn_global_load_lds((const unsigned*)((const char*)(gbase) + (voff)[_i]), (PG8_LAS unsigned*)(lds + (bufoff) + ldsw + _i * 8192), 16, 0, 0); } while (0)
; #define PG8_LDA(dst, b, h) do { if constexpr (DT != 1) { _Pragma("unroll") for (int m = 0; m < 4; ++m) _Pragma("unroll") for (int k = 0; k < 2; ++k) dst[m][k] = *(const PG8_LAS bf16x8*)(lds + PG8_SA(b, h) + aoff + m * 2048 + k * 1024); } \
;         else { _Pragma("unroll") for (int m = 0; m < 4; ++m) dst##8[m] = ld32(lds + PG8_SA(b, h) + aoff + m * 2048); } } while (0)
; #define PG8_LDB(dst, b, h) do { if constexpr (DT != 1) { _Pragma("unroll") for (int n = 0; n < 2; ++n) _Pragma("unroll") for (int k = 0; k < 2; ++k) dst[n][k] = *(const PG8_LAS bf16x8*)(lds + PG8_SB(b, h) + boff + n * 2048 + k * 1024); } \
;         else { _Pragma("unroll") for (int n = 0; n < 2; ++n) dst##8[n] = ld32(lds + PG8_SB(b, h) + boff + n * 2048); } } while (0)
; #define PG8_WAIT_V(n) asm volatile("s_waitcnt vmcnt(" #n ")" ::: "memory")
; #define PG8_WAIT_L(n) asm volatile("s_waitcnt lgkmcnt(" #n ")" ::: "memory")
; #define PG8_BAR __builtin_amdgcn_s_barrier()
; #define PG8_SCHED __builtin_amdgcn_sched_barrier(0)
;     ...
;             PG8_LDB(B0, 1, 0); PG8_LDB(B1, 1, 1); PG8_SCHED; PG8_LDA(At, 1, 0); PG8_STAGE(PG8_SA(0, 1), a2 + hstepA, voffA);
;             PG8_WAIT_V(8); PG8_WAIT_L(0); PG8_BAR; PG8_MMA(0, 0, At, B0); PG8_MMA(0, 1, At, B1); PG8_BAR; PG8_SCHED;
;             PG8_LDA(At, 1, 1); PG8_STAGE(PG8_SB(1, 0), b3, voffB); PG8_STAGE(PG8_SB(1, 1), b3 + hstepB, voffB); PG8_STAGE(PG8_SA(1, 0), a3, voffA);
;             PG8_WAIT_V(8); PG8_WAIT_L(0); PG8_BAR; PG8_MMA(1, 0, At, B0); PG8_MMA(1, 1, At, B1); PG8_BAR; PG8_SCHED;
	ds_read_b128 v[146:149], v160
	ds_read_b128 v[150:153], v160 offset:1024
	ds_read_b128 v[162:165], v160 offset:2048
	ds_read_b128 v[166:169], v160 offset:3072
	ds_read_b128 v[170:173], v161
	ds_read_b128 v[174:177], v161 offset:1024
	ds_read_b128 v[178:181], v161 offset:2048
	ds_read_b128 v[182:185], v161 offset:3072
	s_add_u32 s40, s40, 0x80000
	s_addc_u32 s41, s41, 0
	s_mov_b32 m0, s53
	ds_read_b128 v[186:189], v159 offset:32768
	ds_read_b128 v[190:193], v159 offset:33792
	ds_read_b128 v[194:197], v159 offset:34816
	ds_read_b128 v[198:201], v159 offset:35840
	ds_read_b128 v[202:205], v159 offset:36864
	ds_read_b128 v[206:209], v159 offset:37888
	ds_read_b128 v[210:213], v159 offset:38912
	ds_read_b128 v[214:217], v159 offset:39936
	global_load_lds_dwordx4 v130, s[40:41]
	s_mov_b32 m0, s54
	s_nop 0
	global_load_lds_dwordx4 v134, s[40:41]
	s_waitcnt vmcnt(8)
	s_waitcnt lgkmcnt(0)
	s_barrier
	s_setprio 1
	s_waitcnt lgkmcnt(0)
	v_mfma_f32_16x16x32_bf16 v[122:125], v[146:149], v[186:189], v[122:125]
	v_mfma_f32_16x16x32_bf16 v[126:129], v[162:165], v[186:189], v[126:129]
	v_mfma_f32_16x16x32_bf16 v[110:113], v[146:149], v[194:197], v[110:113]
	v_mfma_f32_16x16x32_bf16 v[106:109], v[162:165], v[194:197], v[106:109]
	v_mfma_f32_16x16x32_bf16 v[94:97], v[146:149], v[202:205], v[94:97]
	v_mfma_f32_16x16x32_bf16 v[90:93], v[162:165], v[202:205], v[90:93]
	v_mfma_f32_16x16x32_bf16 v[78:81], v[146:149], v[210:213], v[78:81]
	v_mfma_f32_16x16x32_bf16 v[74:77], v[162:165], v[210:213], v[74:77]
	v_mfma_f32_16x16x32_bf16 v[122:125], v[150:153], v[190:193], v[122:125]
	v_mfma_f32_16x16x32_bf16 v[126:129], v[166:169], v[190:193], v[126:129]
	v_mfma_f32_16x16x32_bf16 v[110:113], v[150:153], v[198:201], v[110:113]
	v_mfma_f32_16x16x32_bf16 v[106:109], v[166:169], v[198:201], v[106:109]
	v_mfma_f32_16x16x32_bf16 v[94:97], v[150:153], v[206:209], v[94:97]
	v_mfma_f32_16x16x32_bf16 v[90:93], v[166:169], v[206:209], v[90:93]
	v_mfma_f32_16x16x32_bf16 v[78:81], v[150:153], v[214:217], v[78:81]
	v_mfma_f32_16x16x32_bf16 v[74:77], v[166:169], v[214:217], v[74:77]
	s_setprio 0
	s_setprio 1
	v_mfma_f32_16x16x32_bf16 v[118:121], v[170:173], v[186:189], v[118:121]
	v_mfma_f32_16x16x32_bf16 v[114:117], v[178:181], v[186:189], v[114:117]
	v_mfma_f32_16x16x32_bf16 v[102:105], v[170:173], v[194:197], v[102:105]
	v_mfma_f32_16x16x32_bf16 v[98:101], v[178:181], v[194:197], v[98:101]
	v_mfma_f32_16x16x32_bf16 v[86:89], v[170:173], v[202:205], v[86:89]
	v_mfma_f32_16x16x32_bf16 v[82:85], v[178:181], v[202:205], v[82:85]
	v_mfma_f32_16x16x32_bf16 v[70:73], v[170:173], v[210:213], v[70:73]
	v_mfma_f32_16x16x32_bf16 v[66:69], v[178:181], v[210:213], v[66:69]
	v_mfma_f32_16x16x32_bf16 v[118:121], v[174:177], v[190:193], v[118:121]
	v_mfma_f32_16x16x32_bf16 v[114:117], v[182:185], v[190:193], v[114:117]
	v_mfma_f32_16x16x32_bf16 v[102:105], v[174:177], v[198:201], v[102:105]
	v_mfma_f32_16x16x32_bf16 v[98:101], v[182:185], v[198:201], v[98:101]
	v_mfma_f32_16x16x32_bf16 v[86:89], v[174:177], v[206:209], v[86:89]
	v_mfma_f32_16x16x32_bf16 v[82:85], v[182:185], v[206:209], v[82:85]
	v_mfma_f32_16x16x32_bf16 v[70:73], v[174:177], v[214:217], v[70:73]
	v_mfma_f32_16x16x32_bf16 v[66:69], v[182:185], v[214:217], v[66:69]
	s_setprio 0
	s_barrier
	s_mov_b32 m0, s57
	s_add_u32 s38, s38, 0x80080
	ds_read_b128 v[186:189], v159 offset:49152
	ds_read_b128 v[190:193], v159 offset:50176
	ds_read_b128 v[194:197], v159 offset:51200
	ds_read_b128 v[198:201], v159 offset:52224
	ds_read_b128 v[202:205], v159 offset:53248
	ds_read_b128 v[206:209], v159 offset:54272
	ds_read_b128 v[210:213], v159 offset:55296
	ds_read_b128 v[214:217], v159 offset:56320
	global_load_lds_dwordx4 v132, s[98:99]
	s_mov_b32 m0, s58
	s_addc_u32 s39, s39, 0
	global_load_lds_dwordx4 v136, s[98:99]
	s_mov_b32 m0, s61
	s_nop 0
	global_load_lds_dwordx4 v132, s[38:39]
	s_mov_b32 m0, s62
	s_nop 0
	global_load_lds_dwordx4 v136, s[38:39]
	s_mov_b32 m0, s59
	s_nop 0
	global_load_lds_dwordx4 v130, s[100:101]
	s_mov_b32 m0, s60
	s_nop 0
	global_load_lds_dwordx4 v134, s[100:101]
	s_waitcnt vmcnt(8)
	s_waitcnt lgkmcnt(0)
	s_barrier
	s_setprio 1
	s_waitcnt lgkmcnt(0)
	v_mfma_f32_16x16x32_bf16 v[62:65], v[146:149], v[186:189], v[62:65]
	v_mfma_f32_16x16x32_bf16 v[58:61], v[162:165], v[186:189], v[58:61]
	v_mfma_f32_16x16x32_bf16 v[46:49], v[146:149], v[194:197], v[46:49]
	v_mfma_f32_16x16x32_bf16 v[42:45], v[162:165], v[194:197], v[42:45]
	v_mfma_f32_16x16x32_bf16 v[30:33], v[146:149], v[202:205], v[30:33]
	v_mfma_f32_16x16x32_bf16 v[26:29], v[162:165], v[202:205], v[26:29]
	v_mfma_f32_16x16x32_bf16 v[14:17], v[146:149], v[210:213], v[14:17]
	v_mfma_f32_16x16x32_bf16 v[10:13], v[162:165], v[210:213], v[10:13]
	v_mfma_f32_16x16x32_bf16 v[62:65], v[150:153], v[190:193], v[62:65]
	v_mfma_f32_16x16x32_bf16 v[58:61], v[166:169], v[190:193], v[58:61]
	v_mfma_f32_16x16x32_bf16 v[46:49], v[150:153], v[198:201], v[46:49]
	v_mfma_f32_16x16x32_bf16 v[42:45], v[166:169], v[198:201], v[42:45]
	v_mfma_f32_16x16x32_bf16 v[30:33], v[150:153], v[206:209], v[30:33]
	v_mfma_f32_16x16x32_bf16 v[26:29], v[166:169], v[206:209], v[26:29]
	v_mfma_f32_16x16x32_bf16 v[14:17], v[150:153], v[214:217], v[14:17]
	v_mfma_f32_16x16x32_bf16 v[10:13], v[166:169], v[214:217], v[10:13]
	s_setprio 0
	s_setprio 1
	v_mfma_f32_16x16x32_bf16 v[54:57], v[170:173], v[186:189], v[54:57]
	v_mfma_f32_16x16x32_bf16 v[50:53], v[178:181], v[186:189], v[50:53]
	v_mfma_f32_16x16x32_bf16 v[38:41], v[170:173], v[194:197], v[38:41]
	v_mfma_f32_16x16x32_bf16 v[34:37], v[178:181], v[194:197], v[34:37]
	v_mfma_f32_16x16x32_bf16 v[22:25], v[170:173], v[202:205], v[22:25]
	v_mfma_f32_16x16x32_bf16 v[18:21], v[178:181], v[202:205], v[18:21]
	v_mfma_f32_16x16x32_bf16 v[6:9], v[170:173], v[210:213], v[6:9]
	v_mfma_f32_16x16x32_bf16 v[2:5], v[178:181], v[210:213], v[2:5]
	v_mfma_f32_16x16x32_bf16 v[54:57], v[174:177], v[190:193], v[54:57]
	v_mfma_f32_16x16x32_bf16 v[50:53], v[182:185], v[190:193], v[50:53]
	v_mfma_f32_16x16x32_bf16 v[38:41], v[174:177], v[198:201], v[38:41]
	v_mfma_f32_16x16x32_bf16 v[34:37], v[182:185], v[198:201], v[34:37]
	v_mfma_f32_16x16x32_bf16 v[22:25], v[174:177], v[206:209], v[22:25]
	v_mfma_f32_16x16x32_bf16 v[18:21], v[182:185], v[206:209], v[18:21]
	v_mfma_f32_16x16x32_bf16 v[6:9], v[174:177], v[214:217], v[6:9]
	v_mfma_f32_16x16x32_bf16 v[2:5], v[182:185], v[214:217], v[2:5]
	s_setprio 0
	s_barrier
	s_add_u32 s69, s69, 0x100
	s_addc_u32 s70, s70, 0
	s_add_u32 s36, s36, 0x100
	s_addc_u32 s37, s37, 0
	s_cmp_ge_i32 s71, s56
	s_mov_b32 s38, s71
	s_cbranch_scc0 .LBB0_4646
